# wave reductions without LDS: ds_swizzle butterfly steps replaced by DPP quad_perm/row mirror and v_permlane16_swap (bit-identical); MoE expert-count load chains issued together; plus earlier changes
# speedup vs baseline: 1.0057x; 1.0057x over previous
.LBB0_241:
	s_min_i32 s14, s14, 0x2000
	s_ashr_i32 s14, s14, 11
	s_mul_hi_i32 s15, s14, 0xc000
	s_mul_i32 s14, s14, 0xc000
	v_mul_f32_e32 v92, v61, v61
	v_mul_f32_e32 v93, v57, v57
	s_add_u32 s14, s55, s14
	v_fmac_f32_e32 v92, v60, v60
	v_fmac_f32_e32 v93, v56, v56
	s_addc_u32 s15, s69, s15
	v_fmac_f32_e32 v92, v62, v62
	v_fmac_f32_e32 v93, v58, v58
	s_add_u32 s16, s14, 0x2000
	v_fmac_f32_e32 v92, v63, v63
	v_fmac_f32_e32 v93, v59, v59
	s_addc_u32 s17, s15, 0
	v_lshlrev_b64 v[104:105], 2, v[64:65]
	v_add_f32_e32 v108, v93, v92
	global_load_dwordx4 v[92:95], v[82:83], off
	v_lshl_add_u64 v[98:99], s[14:15], 0, v[104:105]
	v_lshl_add_u64 v[104:105], s[16:17], 0, v[104:105]
	global_load_dwordx4 v[100:103], v[98:99], off
	v_mul_f32_e32 v109, v53, v53
	global_load_dwordx4 v[104:107], v[104:105], off
	v_fmac_f32_e32 v109, v52, v52
	v_fmac_f32_e32 v109, v54, v54
	v_fmac_f32_e32 v109, v55, v55
	v_add_f32_e32 v108, v109, v108
	v_mul_f32_e32 v109, v49, v49
	v_fmac_f32_e32 v109, v48, v48
	v_fmac_f32_e32 v109, v50, v50
	v_fmac_f32_e32 v109, v51, v51
	v_add_f32_e32 v108, v109, v108
	v_mul_f32_e32 v109, v45, v45
	v_fmac_f32_e32 v109, v44, v44
	v_fmac_f32_e32 v109, v46, v46
	v_fmac_f32_e32 v109, v47, v47
	v_add_f32_e32 v108, v109, v108
	v_mul_f32_e32 v109, v41, v41
	v_fmac_f32_e32 v109, v40, v40
	v_fmac_f32_e32 v109, v42, v42
	v_fmac_f32_e32 v109, v43, v43
	v_add_f32_e32 v108, v109, v108
	v_mul_f32_e32 v109, v37, v37
	v_fmac_f32_e32 v109, v36, v36
	v_fmac_f32_e32 v109, v38, v38
	v_fmac_f32_e32 v109, v39, v39
	v_add_f32_e32 v108, v109, v108
	v_mul_f32_e32 v109, v1, v1
	v_fmac_f32_e32 v109, v0, v0
	v_fmac_f32_e32 v109, v2, v2
	v_fmac_f32_e32 v109, v3, v3
	v_add_f32_e32 v108, v109, v108
	s_mov_b32 s21, 0x74f8000
	v_mov_b32_e32 v121, 1
	v_mov_b32_e32 v120, v97
	v_mov_b32_e32 v217, 1
	s_waitcnt lgkmcnt(0)
	s_nop 1
	v_add_f32_dpp v108, v108, v108 quad_perm:[1,0,3,2] row_mask:0xf bank_mask:0xf
	s_waitcnt lgkmcnt(0)
	s_nop 1
	v_add_f32_dpp v108, v108, v108 quad_perm:[2,3,0,1] row_mask:0xf bank_mask:0xf
	s_waitcnt lgkmcnt(0)
	s_nop 1
	v_add_f32_dpp v108, v108, v108 row_half_mirror row_mask:0xf bank_mask:0xf
	s_waitcnt lgkmcnt(0)
	s_nop 1
	v_add_f32_dpp v108, v108, v108 row_mirror row_mask:0xf bank_mask:0xf
	v_mov_b32_e32 v109, v108
	s_waitcnt lgkmcnt(0)
	s_nop 1
	v_permlane16_swap_b32_e32 v108, v109
	v_add_f32_e32 v108, v108, v109
	v_mov_b32_e32 v109, v108
	s_nop 1
	v_permlane32_swap_b32_e32 v108, v109
	v_add_f32_e32 v108, v108, v109
	v_mov_b32_e32 v109, 0x358637bd
	v_fmamk_f32 v108, v108, 0x3a000000, v109
	v_mul_f32_e32 v109, 0x4b800000, v108
	v_cmp_gt_f32_e32 vcc, s33, v108
	s_waitcnt vmcnt(2)
	v_mov_b32_e32 v111, v94
	v_cndmask_b32_e32 v108, v108, v109, vcc
	v_rsq_f32_e32 v110, v108
	v_mov_b32_e32 v108, v60
	v_mov_b32_e32 v109, v62
	v_mov_b32_e32 v62, v61
	v_mul_f32_e32 v60, 0x45800000, v110
	v_cndmask_b32_e32 v60, v110, v60, vcc
	v_pk_mul_f32 v[108:109], v[108:109], v[60:61] op_sel_hi:[1,0]
	v_mov_b32_e32 v110, v92
	v_pk_mul_f32 v[62:63], v[62:63], v[60:61] op_sel_hi:[1,0]
	v_mov_b32_e32 v94, v93
	v_pk_mul_f32 v[92:93], v[110:111], v[108:109]
	s_waitcnt vmcnt(0)
	v_mov_b32_e32 v108, v104
	v_mov_b32_e32 v109, v106
	v_pk_mul_f32 v[62:63], v[94:95], v[62:63]
	v_mov_b32_e32 v94, v100
	v_mov_b32_e32 v95, v102
	v_mov_b32_e32 v106, v105
	v_pk_add_f32 v[104:105], v[108:109], 1.0 op_sel_hi:[1,0]
	v_mov_b32_e32 v102, v101
	v_pk_fma_f32 v[94:95], v[104:105], v[92:93], v[94:95]
	v_pk_add_f32 v[92:93], v[106:107], 1.0 op_sel_hi:[1,0]
	v_mov_b32_e32 v61, v97
	v_pk_fma_f32 v[62:63], v[92:93], v[62:63], v[102:103]
	v_lshl_add_u64 v[92:93], s[8:9], 0, v[64:65]
	v_cvt_pk_fp8_f32 v61, v94, v62
	v_add_co_u32_e32 v92, vcc, s21, v92
	v_and_b32_sdwa v100, v94, v121 dst_sel:DWORD dst_unused:UNUSED_PAD src0_sel:WORD_1 src1_sel:DWORD
	v_cvt_pk_fp8_f32 v61, v95, v63 op_sel:[0,0,1]
	v_addc_co_u32_e32 v93, vcc, 0, v93, vcc
	v_add3_u32 v94, v94, v100, s51
	v_and_b32_sdwa v100, v62, v121 dst_sel:DWORD dst_unused:UNUSED_PAD src0_sel:WORD_1 src1_sel:DWORD
	global_store_dword v[92:93], v61, off
	v_and_b32_sdwa v61, v95, v121 dst_sel:DWORD dst_unused:UNUSED_PAD src0_sel:WORD_1 src1_sel:DWORD
	v_add3_u32 v62, v62, v100, s51
	v_add3_u32 v61, v95, v61, s51
	v_and_b32_sdwa v95, v63, v121 dst_sel:DWORD dst_unused:UNUSED_PAD src0_sel:WORD_1 src1_sel:DWORD
	v_and_b32_e32 v62, 0xffff0000, v62
	v_add3_u32 v63, v63, v95, s51
	v_or_b32_sdwa v62, v62, v94 dst_sel:DWORD dst_unused:UNUSED_PAD src0_sel:DWORD src1_sel:WORD_1
	v_lshl_add_u64 v[94:95], s[8:9], 0, v[72:73]
	s_mov_b32 s21, 0x50f8000
	v_and_b32_e32 v63, 0xffff0000, v63
	v_add_co_u32_e32 v94, vcc, s21, v94
	v_or_b32_sdwa v63, v63, v61 dst_sel:DWORD dst_unused:UNUSED_PAD src0_sel:DWORD src1_sel:WORD_1
	s_nop 0
	v_addc_co_u32_e32 v95, vcc, 0, v95, vcc
	global_store_dwordx2 v[94:95], v[62:63], off
	global_load_dwordx4 v[100:103], v[82:83], off offset:1024
	v_lshl_add_u64 v[62:63], v[66:67], 2, s[16:17]
	global_load_dwordx4 v[104:107], v[62:63], off
	global_load_dwordx4 v[108:111], v[98:99], off offset:1024
	v_mov_b32_e32 v62, v56
	v_mov_b32_e32 v63, v58
	v_mov_b32_e32 v61, v97
	v_mov_b32_e32 v58, v57
	v_pk_mul_f32 v[56:57], v[62:63], v[60:61] op_sel_hi:[1,0]
	v_pk_mul_f32 v[58:59], v[58:59], v[60:61] op_sel_hi:[1,0]
	s_add_u32 s8, s8, s38
	s_addc_u32 s9, s9, s39
	s_andn2_b64 vcc, exec, s[10:11]
	s_waitcnt vmcnt(2)
	v_mov_b32_e32 v62, v100
	v_mov_b32_e32 v63, v102
	s_waitcnt vmcnt(1)
	v_mov_b32_e32 v112, v104
	v_mov_b32_e32 v113, v106
	v_mov_b32_e32 v102, v101
	v_mov_b32_e32 v106, v105
	s_waitcnt vmcnt(0)
	v_mov_b32_e32 v114, v108
	v_mov_b32_e32 v115, v110
	v_mov_b32_e32 v110, v109
	v_pk_mul_f32 v[56:57], v[62:63], v[56:57]
	v_pk_add_f32 v[62:63], v[112:113], 1.0 op_sel_hi:[1,0]
	v_pk_mul_f32 v[58:59], v[102:103], v[58:59]
	v_pk_add_f32 v[100:101], v[106:107], 1.0 op_sel_hi:[1,0]
	v_pk_fma_f32 v[56:57], v[62:63], v[56:57], v[114:115]
	v_pk_fma_f32 v[58:59], v[100:101], v[58:59], v[110:111]
	v_and_b32_sdwa v63, v56, v121 dst_sel:DWORD dst_unused:UNUSED_PAD src0_sel:WORD_1 src1_sel:DWORD
	v_cvt_pk_fp8_f32 v61, v56, v58
	v_and_b32_sdwa v100, v59, v121 dst_sel:DWORD dst_unused:UNUSED_PAD src0_sel:WORD_1 src1_sel:DWORD
	v_and_b32_sdwa v101, v58, v121 dst_sel:DWORD dst_unused:UNUSED_PAD src0_sel:WORD_1 src1_sel:DWORD
	v_and_b32_sdwa v62, v57, v121 dst_sel:DWORD dst_unused:UNUSED_PAD src0_sel:WORD_1 src1_sel:DWORD
	v_add3_u32 v56, v56, v63, s51
	v_add3_u32 v63, v59, v100, s51
	v_add3_u32 v58, v58, v101, s51
	v_cvt_pk_fp8_f32 v61, v57, v59 op_sel:[0,0,1]
	v_add3_u32 v62, v57, v62, s51
	v_and_b32_e32 v63, 0xffff0000, v63
	v_and_b32_e32 v58, 0xffff0000, v58
	v_or_b32_sdwa v57, v63, v62 dst_sel:DWORD dst_unused:UNUSED_PAD src0_sel:DWORD src1_sel:WORD_1
	v_or_b32_sdwa v56, v58, v56 dst_sel:DWORD dst_unused:UNUSED_PAD src0_sel:DWORD src1_sel:WORD_1
	global_store_dwordx2 v[94:95], v[56:57], off offset:512
	global_store_dword v[92:93], v61, off offset:256
	global_load_dwordx4 v[56:59], v[82:83], off offset:2048
	v_lshl_add_u64 v[62:63], v[68:69], 2, s[16:17]
	global_load_dwordx4 v[100:103], v[62:63], off
	global_load_dwordx4 v[104:107], v[98:99], off offset:2048
	v_mov_b32_e32 v62, v52
	v_mov_b32_e32 v63, v54
	v_mov_b32_e32 v61, v97
	v_mov_b32_e32 v54, v53
	v_pk_mul_f32 v[52:53], v[62:63], v[60:61] op_sel_hi:[1,0]
	v_pk_mul_f32 v[54:55], v[54:55], v[60:61] op_sel_hi:[1,0]
	s_waitcnt vmcnt(2)
	v_mov_b32_e32 v62, v56
	v_mov_b32_e32 v63, v58
	s_waitcnt vmcnt(1)
	v_mov_b32_e32 v108, v100
	v_mov_b32_e32 v109, v102
	v_mov_b32_e32 v58, v57
	v_mov_b32_e32 v102, v101
	s_waitcnt vmcnt(0)
	v_mov_b32_e32 v110, v104
	v_mov_b32_e32 v111, v106
	v_mov_b32_e32 v106, v105
	v_pk_mul_f32 v[52:53], v[52:53], v[62:63]
	v_pk_add_f32 v[56:57], v[108:109], 1.0 op_sel_hi:[1,0]
	v_pk_mul_f32 v[54:55], v[54:55], v[58:59]
	v_pk_add_f32 v[58:59], v[102:103], 1.0 op_sel_hi:[1,0]
	v_pk_fma_f32 v[52:53], v[52:53], v[56:57], v[110:111]
	v_pk_fma_f32 v[54:55], v[54:55], v[58:59], v[106:107]
	v_and_b32_sdwa v57, v52, v121 dst_sel:DWORD dst_unused:UNUSED_PAD src0_sel:WORD_1 src1_sel:DWORD
	v_cvt_pk_fp8_f32 v61, v52, v54
	v_and_b32_sdwa v58, v55, v121 dst_sel:DWORD dst_unused:UNUSED_PAD src0_sel:WORD_1 src1_sel:DWORD
	v_and_b32_sdwa v59, v54, v121 dst_sel:DWORD dst_unused:UNUSED_PAD src0_sel:WORD_1 src1_sel:DWORD
	v_and_b32_sdwa v56, v53, v121 dst_sel:DWORD dst_unused:UNUSED_PAD src0_sel:WORD_1 src1_sel:DWORD
	v_add3_u32 v52, v52, v57, s51
	v_add3_u32 v57, v55, v58, s51
	v_add3_u32 v54, v54, v59, s51
	v_cvt_pk_fp8_f32 v61, v53, v55 op_sel:[0,0,1]
	v_add3_u32 v56, v53, v56, s51
	v_and_b32_e32 v57, 0xffff0000, v57
	v_and_b32_e32 v54, 0xffff0000, v54
	v_or_b32_sdwa v53, v57, v56 dst_sel:DWORD dst_unused:UNUSED_PAD src0_sel:DWORD src1_sel:WORD_1
	v_or_b32_sdwa v52, v54, v52 dst_sel:DWORD dst_unused:UNUSED_PAD src0_sel:DWORD src1_sel:WORD_1
	global_store_dwordx2 v[94:95], v[52:53], off offset:1024
	global_store_dword v[92:93], v61, off offset:512
	global_load_dwordx4 v[52:55], v[82:83], off offset:3072
	v_lshl_add_u64 v[56:57], v[70:71], 2, s[16:17]
	global_load_dwordx4 v[56:59], v[56:57], off
	s_nop 0
	global_load_dwordx4 v[98:101], v[98:99], off offset:3072
	v_mov_b32_e32 v62, v48
	v_mov_b32_e32 v63, v50
	v_mov_b32_e32 v61, v97
	v_mov_b32_e32 v50, v49
	v_pk_mul_f32 v[48:49], v[62:63], v[60:61] op_sel_hi:[1,0]
	v_pk_mul_f32 v[50:51], v[50:51], v[60:61] op_sel_hi:[1,0]
	s_waitcnt vmcnt(2)
	v_mov_b32_e32 v62, v52
	v_mov_b32_e32 v63, v54
	s_waitcnt vmcnt(1)
	v_mov_b32_e32 v102, v56
	v_mov_b32_e32 v103, v58
	v_mov_b32_e32 v54, v53
	v_mov_b32_e32 v58, v57
	s_waitcnt vmcnt(0)
	v_mov_b32_e32 v104, v98
	v_mov_b32_e32 v105, v100
	v_mov_b32_e32 v100, v99
	v_pk_mul_f32 v[48:49], v[48:49], v[62:63]
	v_pk_add_f32 v[52:53], v[102:103], 1.0 op_sel_hi:[1,0]
	v_pk_mul_f32 v[50:51], v[50:51], v[54:55]
	v_pk_add_f32 v[54:55], v[58:59], 1.0 op_sel_hi:[1,0]
	v_pk_fma_f32 v[48:49], v[48:49], v[52:53], v[104:105]
	v_pk_fma_f32 v[50:51], v[50:51], v[54:55], v[100:101]
	v_and_b32_sdwa v53, v48, v121 dst_sel:DWORD dst_unused:UNUSED_PAD src0_sel:WORD_1 src1_sel:DWORD
	v_cvt_pk_fp8_f32 v61, v48, v50
	v_and_b32_sdwa v54, v51, v121 dst_sel:DWORD dst_unused:UNUSED_PAD src0_sel:WORD_1 src1_sel:DWORD
	v_and_b32_sdwa v55, v50, v121 dst_sel:DWORD dst_unused:UNUSED_PAD src0_sel:WORD_1 src1_sel:DWORD
	v_and_b32_sdwa v52, v49, v121 dst_sel:DWORD dst_unused:UNUSED_PAD src0_sel:WORD_1 src1_sel:DWORD
	v_add3_u32 v48, v48, v53, s51
	v_add3_u32 v53, v51, v54, s51
	v_add3_u32 v50, v50, v55, s51
	v_cvt_pk_fp8_f32 v61, v49, v51 op_sel:[0,0,1]
	v_add3_u32 v52, v49, v52, s51
	v_and_b32_e32 v53, 0xffff0000, v53
	v_and_b32_e32 v50, 0xffff0000, v50
	v_or_b32_sdwa v49, v53, v52 dst_sel:DWORD dst_unused:UNUSED_PAD src0_sel:DWORD src1_sel:WORD_1
	v_or_b32_sdwa v48, v50, v48 dst_sel:DWORD dst_unused:UNUSED_PAD src0_sel:DWORD src1_sel:WORD_1
	global_store_dwordx2 v[94:95], v[48:49], off offset:1536
	global_store_dword v[92:93], v61, off offset:768
	v_lshl_add_u64 v[52:53], s[16:17], 0, v[74:75]
	global_load_dwordx4 v[48:51], v[84:85], off
	v_lshl_add_u64 v[56:57], s[14:15], 0, v[74:75]
	global_load_dwordx4 v[52:55], v[52:53], off
	v_mov_b32_e32 v62, v44
	global_load_dwordx4 v[56:59], v[56:57], off
	v_mov_b32_e32 v63, v46
	v_mov_b32_e32 v61, v97
	v_mov_b32_e32 v46, v45
	v_pk_mul_f32 v[44:45], v[62:63], v[60:61] op_sel_hi:[1,0]
	v_pk_mul_f32 v[46:47], v[46:47], v[60:61] op_sel_hi:[1,0]
	s_waitcnt vmcnt(2)
	v_mov_b32_e32 v62, v48
	v_mov_b32_e32 v63, v50
	s_waitcnt vmcnt(1)
	v_mov_b32_e32 v98, v52
	v_mov_b32_e32 v99, v54
	v_mov_b32_e32 v50, v49
	v_mov_b32_e32 v54, v53
	s_waitcnt vmcnt(0)
	v_mov_b32_e32 v100, v56
	v_mov_b32_e32 v101, v58
	v_mov_b32_e32 v58, v57
	v_pk_mul_f32 v[44:45], v[44:45], v[62:63]
	v_pk_add_f32 v[48:49], v[98:99], 1.0 op_sel_hi:[1,0]
	v_pk_mul_f32 v[46:47], v[46:47], v[50:51]
	v_pk_add_f32 v[50:51], v[54:55], 1.0 op_sel_hi:[1,0]
	v_pk_fma_f32 v[44:45], v[44:45], v[48:49], v[100:101]
	v_pk_fma_f32 v[46:47], v[46:47], v[50:51], v[58:59]
	v_and_b32_sdwa v49, v44, v121 dst_sel:DWORD dst_unused:UNUSED_PAD src0_sel:WORD_1 src1_sel:DWORD
	v_cvt_pk_fp8_f32 v61, v44, v46
	v_and_b32_sdwa v50, v47, v121 dst_sel:DWORD dst_unused:UNUSED_PAD src0_sel:WORD_1 src1_sel:DWORD
	v_and_b32_sdwa v51, v46, v121 dst_sel:DWORD dst_unused:UNUSED_PAD src0_sel:WORD_1 src1_sel:DWORD
	v_and_b32_sdwa v48, v45, v121 dst_sel:DWORD dst_unused:UNUSED_PAD src0_sel:WORD_1 src1_sel:DWORD
	v_add3_u32 v44, v44, v49, s51
	v_add3_u32 v49, v47, v50, s51
	v_add3_u32 v46, v46, v51, s51
	v_cvt_pk_fp8_f32 v61, v45, v47 op_sel:[0,0,1]
	v_add3_u32 v48, v45, v48, s51
	v_and_b32_e32 v49, 0xffff0000, v49
	v_and_b32_e32 v46, 0xffff0000, v46
	v_or_b32_sdwa v45, v49, v48 dst_sel:DWORD dst_unused:UNUSED_PAD src0_sel:DWORD src1_sel:WORD_1
	v_or_b32_sdwa v44, v46, v44 dst_sel:DWORD dst_unused:UNUSED_PAD src0_sel:DWORD src1_sel:WORD_1
	global_store_dwordx2 v[94:95], v[44:45], off offset:2048
	global_store_dword v[92:93], v61, off offset:1024
	v_lshl_add_u64 v[48:49], s[16:17], 0, v[76:77]
	global_load_dwordx4 v[44:47], v[86:87], off
	v_lshl_add_u64 v[52:53], s[14:15], 0, v[76:77]
	global_load_dwordx4 v[48:51], v[48:49], off
	v_mov_b32_e32 v56, v40
	global_load_dwordx4 v[52:55], v[52:53], off
	v_mov_b32_e32 v57, v42
	v_mov_b32_e32 v61, v97
	v_mov_b32_e32 v42, v41
	v_pk_mul_f32 v[40:41], v[56:57], v[60:61] op_sel_hi:[1,0]
	v_pk_mul_f32 v[42:43], v[42:43], v[60:61] op_sel_hi:[1,0]
	s_waitcnt vmcnt(2)
	v_mov_b32_e32 v56, v44
	v_mov_b32_e32 v57, v46
	s_waitcnt vmcnt(1)
	v_mov_b32_e32 v58, v48
	v_mov_b32_e32 v59, v50
	v_mov_b32_e32 v46, v45
	v_mov_b32_e32 v50, v49
	s_waitcnt vmcnt(0)
	v_mov_b32_e32 v62, v52
	v_mov_b32_e32 v63, v54
	v_mov_b32_e32 v54, v53
	v_pk_mul_f32 v[40:41], v[40:41], v[56:57]
	v_pk_add_f32 v[44:45], v[58:59], 1.0 op_sel_hi:[1,0]
	v_pk_mul_f32 v[42:43], v[42:43], v[46:47]
	v_pk_add_f32 v[46:47], v[50:51], 1.0 op_sel_hi:[1,0]
	v_pk_fma_f32 v[40:41], v[40:41], v[44:45], v[62:63]
	v_pk_fma_f32 v[42:43], v[42:43], v[46:47], v[54:55]
	v_and_b32_sdwa v45, v40, v121 dst_sel:DWORD dst_unused:UNUSED_PAD src0_sel:WORD_1 src1_sel:DWORD
	v_cvt_pk_fp8_f32 v61, v40, v42
	v_and_b32_sdwa v46, v43, v121 dst_sel:DWORD dst_unused:UNUSED_PAD src0_sel:WORD_1 src1_sel:DWORD
	v_and_b32_sdwa v47, v42, v121 dst_sel:DWORD dst_unused:UNUSED_PAD src0_sel:WORD_1 src1_sel:DWORD
	v_and_b32_sdwa v44, v41, v121 dst_sel:DWORD dst_unused:UNUSED_PAD src0_sel:WORD_1 src1_sel:DWORD
	v_add3_u32 v40, v40, v45, s51
	v_add3_u32 v45, v43, v46, s51
	v_add3_u32 v42, v42, v47, s51
	v_cvt_pk_fp8_f32 v61, v41, v43 op_sel:[0,0,1]
	v_add3_u32 v44, v41, v44, s51
	v_and_b32_e32 v45, 0xffff0000, v45
	v_and_b32_e32 v42, 0xffff0000, v42
	v_or_b32_sdwa v41, v45, v44 dst_sel:DWORD dst_unused:UNUSED_PAD src0_sel:DWORD src1_sel:WORD_1
	v_or_b32_sdwa v40, v42, v40 dst_sel:DWORD dst_unused:UNUSED_PAD src0_sel:DWORD src1_sel:WORD_1
	global_store_dwordx2 v[94:95], v[40:41], off offset:2560
	global_store_dword v[92:93], v61, off offset:1280
	v_lshl_add_u64 v[44:45], s[16:17], 0, v[78:79]
	global_load_dwordx4 v[40:43], v[88:89], off
	v_lshl_add_u64 v[48:49], s[14:15], 0, v[78:79]
	global_load_dwordx4 v[44:47], v[44:45], off
	v_mov_b32_e32 v52, v36
	global_load_dwordx4 v[48:51], v[48:49], off
	v_mov_b32_e32 v53, v38
	v_mov_b32_e32 v38, v37
	v_pk_mul_f32 v[36:37], v[52:53], v[60:61] op_sel_hi:[1,0]
	v_pk_mul_f32 v[38:39], v[38:39], v[60:61] op_sel_hi:[1,0]
	v_mov_b32_e32 v58, v97
	s_waitcnt vmcnt(2)
	v_mov_b32_e32 v52, v40
	v_mov_b32_e32 v53, v42
	s_waitcnt vmcnt(1)
	v_mov_b32_e32 v54, v44
	v_mov_b32_e32 v55, v46
	v_mov_b32_e32 v42, v41
	v_mov_b32_e32 v46, v45
	s_waitcnt vmcnt(0)
	v_mov_b32_e32 v56, v48
	v_mov_b32_e32 v57, v50
	v_mov_b32_e32 v50, v49
	v_pk_mul_f32 v[36:37], v[36:37], v[52:53]
	v_pk_add_f32 v[40:41], v[54:55], 1.0 op_sel_hi:[1,0]
	v_pk_mul_f32 v[38:39], v[38:39], v[42:43]
	v_pk_add_f32 v[42:43], v[46:47], 1.0 op_sel_hi:[1,0]
	v_pk_fma_f32 v[36:37], v[36:37], v[40:41], v[56:57]
	v_pk_fma_f32 v[38:39], v[38:39], v[42:43], v[50:51]
	v_and_b32_sdwa v41, v36, v121 dst_sel:DWORD dst_unused:UNUSED_PAD src0_sel:WORD_1 src1_sel:DWORD
	v_cvt_pk_fp8_f32 v58, v36, v38
	v_and_b32_sdwa v42, v39, v121 dst_sel:DWORD dst_unused:UNUSED_PAD src0_sel:WORD_1 src1_sel:DWORD
	v_and_b32_sdwa v43, v38, v121 dst_sel:DWORD dst_unused:UNUSED_PAD src0_sel:WORD_1 src1_sel:DWORD
	v_and_b32_sdwa v40, v37, v121 dst_sel:DWORD dst_unused:UNUSED_PAD src0_sel:WORD_1 src1_sel:DWORD
	v_add3_u32 v36, v36, v41, s51
	v_add3_u32 v41, v39, v42, s51
	v_add3_u32 v38, v38, v43, s51
	v_cvt_pk_fp8_f32 v58, v37, v39 op_sel:[0,0,1]
	v_add3_u32 v40, v37, v40, s51
	v_and_b32_e32 v41, 0xffff0000, v41
	v_and_b32_e32 v38, 0xffff0000, v38
	v_or_b32_sdwa v37, v41, v40 dst_sel:DWORD dst_unused:UNUSED_PAD src0_sel:DWORD src1_sel:WORD_1
	v_or_b32_sdwa v36, v38, v36 dst_sel:DWORD dst_unused:UNUSED_PAD src0_sel:DWORD src1_sel:WORD_1
	global_store_dwordx2 v[94:95], v[36:37], off offset:3072
	global_store_dword v[92:93], v58, off offset:1536
	v_lshl_add_u64 v[36:37], s[16:17], 0, v[80:81]
	global_load_dwordx4 v[98:101], v[90:91], off
	global_load_dwordx4 v[102:105], v[36:37], off
	v_lshl_add_u64 v[36:37], s[14:15], 0, v[80:81]
	global_load_dwordx4 v[106:109], v[36:37], off
	v_mov_b32_e32 v36, v0
	v_mov_b32_e32 v37, v2
	v_mov_b32_e32 v2, v1
	v_pk_mul_f32 v[110:111], v[36:37], v[60:61] op_sel_hi:[1,0]
	v_pk_mul_f32 v[112:113], v[2:3], v[60:61] op_sel_hi:[1,0]
	v_mov_b64_e32 v[0:1], v[20:21]
	v_mov_b64_e32 v[38:39], v[26:27]
	v_mov_b64_e32 v[42:43], v[30:31]
	v_mov_b64_e32 v[46:47], v[34:35]
	v_mov_b64_e32 v[50:51], v[6:7]
	v_mov_b64_e32 v[54:55], v[10:11]
	v_mov_b64_e32 v[58:59], v[14:15]
	v_mov_b64_e32 v[62:63], v[18:19]
	v_mov_b64_e32 v[2:3], v[22:23]
	v_mov_b64_e32 v[36:37], v[24:25]
	v_mov_b64_e32 v[40:41], v[28:29]
	v_mov_b64_e32 v[44:45], v[32:33]
	v_mov_b64_e32 v[48:49], v[4:5]
	v_mov_b64_e32 v[52:53], v[8:9]
	v_mov_b64_e32 v[56:57], v[12:13]
	v_mov_b64_e32 v[60:61], v[16:17]
	s_mov_b32 s14, s20
	s_waitcnt vmcnt(2)
	v_mov_b32_e32 v114, v98
	v_mov_b32_e32 v115, v100
	s_waitcnt vmcnt(1)
	v_mov_b32_e32 v116, v102
	v_mov_b32_e32 v117, v104
	v_mov_b32_e32 v100, v99
	v_mov_b32_e32 v104, v103
	s_waitcnt vmcnt(0)
	v_mov_b32_e32 v118, v106
	v_mov_b32_e32 v119, v108
	v_mov_b32_e32 v108, v107
	v_pk_mul_f32 v[98:99], v[110:111], v[114:115]
	v_pk_add_f32 v[102:103], v[116:117], 1.0 op_sel_hi:[1,0]
	v_pk_mul_f32 v[100:101], v[112:113], v[100:101]
	v_pk_add_f32 v[104:105], v[104:105], 1.0 op_sel_hi:[1,0]
	v_pk_fma_f32 v[98:99], v[98:99], v[102:103], v[118:119]
	v_pk_fma_f32 v[100:101], v[100:101], v[104:105], v[108:109]
	v_and_b32_sdwa v103, v98, v121 dst_sel:DWORD dst_unused:UNUSED_PAD src0_sel:WORD_1 src1_sel:DWORD
	v_cvt_pk_fp8_f32 v120, v98, v100
	v_and_b32_sdwa v104, v101, v121 dst_sel:DWORD dst_unused:UNUSED_PAD src0_sel:WORD_1 src1_sel:DWORD
	v_and_b32_sdwa v105, v100, v121 dst_sel:DWORD dst_unused:UNUSED_PAD src0_sel:WORD_1 src1_sel:DWORD
	v_and_b32_sdwa v102, v99, v121 dst_sel:DWORD dst_unused:UNUSED_PAD src0_sel:WORD_1 src1_sel:DWORD
	v_add3_u32 v98, v98, v103, s51
	v_add3_u32 v103, v101, v104, s51
	v_add3_u32 v100, v100, v105, s51
	v_cvt_pk_fp8_f32 v120, v99, v101 op_sel:[0,0,1]
	v_add3_u32 v102, v99, v102, s51
	v_and_b32_e32 v103, 0xffff0000, v103
	v_and_b32_e32 v100, 0xffff0000, v100
	v_or_b32_sdwa v99, v103, v102 dst_sel:DWORD dst_unused:UNUSED_PAD src0_sel:DWORD src1_sel:WORD_1
	v_or_b32_sdwa v98, v100, v98 dst_sel:DWORD dst_unused:UNUSED_PAD src0_sel:DWORD src1_sel:WORD_1
	global_store_dwordx2 v[94:95], v[98:99], off offset:3584
	global_store_dword v[92:93], v120, off offset:1792
	s_cbranch_vccz .LBB0_244

.LBB0_743:
	s_waitcnt vmcnt(0)
	v_lshlrev_b32_e32 v12, 16, v11
	v_and_b32_e32 v13, 0xffff0000, v11
	v_pk_mul_f32 v[26:27], v[12:13], v[12:13]
	s_waitcnt vmcnt(10)
	v_lshlrev_b32_e32 v30, 16, v10
	v_add_f32_e32 v11, v26, v27
	v_and_b32_e32 v31, 0xffff0000, v10
	v_pk_mul_f32 v[32:33], v[30:31], v[30:31]
	s_ashr_i32 s3, s2, 31
	v_add_f32_e32 v10, v32, v33
	s_waitcnt lgkmcnt(0)
	s_nop 1
	v_add_f32_dpp v11, v11, v11 quad_perm:[1,0,3,2] row_mask:0xf bank_mask:0xf
	s_lshl_b64 s[12:13], s[2:3], 10
	s_mov_b32 s2, 0x358637bd
	v_lshl_add_u64 v[28:29], s[8:9], 0, v[96:97]
	s_add_i32 s5, s5, s54
	s_waitcnt lgkmcnt(0)
	s_nop 1
	v_add_f32_dpp v11, v11, v11 quad_perm:[2,3,0,1] row_mask:0xf bank_mask:0xf
	s_add_i32 s16, s16, s97
	s_waitcnt lgkmcnt(0)
	s_nop 1
	v_add_f32_dpp v11, v11, v11 row_half_mirror row_mask:0xf bank_mask:0xf
	s_waitcnt lgkmcnt(0)
	s_nop 1
	v_add_f32_dpp v11, v11, v11 row_mirror row_mask:0xf bank_mask:0xf
	v_mov_b32_e32 v25, v11
	s_waitcnt lgkmcnt(0)
	s_nop 1
	v_permlane16_swap_b32_e32 v11, v25
	v_add_f32_e32 v11, v11, v25
	v_mov_b32_e32 v27, v11
	s_nop 1
	v_permlane32_swap_b32_e32 v11, v27
	s_waitcnt lgkmcnt(0)
	s_nop 1
	v_add_f32_dpp v10, v10, v10 quad_perm:[1,0,3,2] row_mask:0xf bank_mask:0xf
	s_waitcnt lgkmcnt(0)
	s_nop 1
	v_add_f32_dpp v10, v10, v10 quad_perm:[2,3,0,1] row_mask:0xf bank_mask:0xf
	s_waitcnt lgkmcnt(0)
	s_nop 1
	v_add_f32_dpp v10, v10, v10 row_half_mirror row_mask:0xf bank_mask:0xf
	s_waitcnt lgkmcnt(0)
	s_nop 1
	v_add_f32_dpp v10, v10, v10 row_mirror row_mask:0xf bank_mask:0xf
	v_mov_b32_e32 v25, v10
	s_waitcnt lgkmcnt(0)
	s_nop 1
	v_permlane16_swap_b32_e32 v10, v25
	v_add_f32_e32 v10, v10, v25
	v_mov_b32_e32 v26, v10
	s_nop 1
	v_permlane32_swap_b32_e32 v10, v26
	v_pk_add_f32 v[26:27], v[10:11], v[26:27]
	v_mov_b64_e32 v[10:11], s[2:3]
	v_pk_fma_f32 v[26:27], v[26:27], s[60:61], v[10:11] op_sel_hi:[1,0,0]
	s_nop 0
	v_mul_f32_e32 v25, 0x4b800000, v27
	v_cmp_gt_f32_e64 s[2:3], s33, v27
	v_cmp_gt_f32_e32 vcc, s33, v26
	s_nop 0
	v_cndmask_b32_e64 v25, v27, v25, s[2:3]
	v_rsq_f32_e32 v25, v25
	s_nop 0
	v_mul_f32_e32 v27, 0x45800000, v25
	v_cndmask_b32_e64 v25, v25, v27, s[2:3]
	v_mul_f32_e32 v13, v25, v13
	v_mul_f32_e32 v12, v25, v12
	v_mul_f32_e32 v13, v5, v13
	v_mul_f32_e32 v12, v4, v12
	s_waitcnt vmcnt(0)
	v_mul_f32_e32 v25, v8, v13
	v_mul_f32_e32 v13, v9, v13
	v_fmac_f32_e32 v25, v9, v12
	v_fma_f32 v12, v8, v12, -v13
	v_bfe_u32 v13, v12, 16, 1
	v_add3_u32 v12, v12, v13, s51
	v_bfe_u32 v13, v25, 16, 1
	v_lshrrev_b32_e32 v12, 16, v12
	v_add3_u32 v13, v25, v13, s51
	s_mov_b32 s2, 0x6a858000
	v_and_or_b32 v25, v13, s48, v12
	v_add_co_u32_e64 v12, s[2:3], s2, v28
	s_nop 1
	v_addc_co_u32_e64 v13, s[2:3], 0, v29, s[2:3]
	global_store_dword v[12:13], v25, off
	v_mul_f32_e32 v25, 0x4b800000, v26
	v_cndmask_b32_e32 v25, v26, v25, vcc
	v_rsq_f32_e32 v25, v25
	s_nop 0
	v_mul_f32_e32 v26, 0x45800000, v25
	v_cndmask_b32_e32 v25, v25, v26, vcc
	v_mul_f32_e32 v26, v25, v30
	v_mul_f32_e32 v25, v25, v31
	v_mul_f32_e32 v25, v5, v25
	v_mul_f32_e32 v26, v4, v26
	v_mul_f32_e32 v27, v8, v25
	v_mul_f32_e32 v25, v9, v25
	v_fma_f32 v25, v8, v26, -v25
	v_fmac_f32_e32 v27, v9, v26
	v_bfe_u32 v26, v25, 16, 1
	v_add3_u32 v25, v25, v26, s51
	v_bfe_u32 v26, v27, 16, 1
	v_lshrrev_b32_e32 v25, 16, v25
	v_add3_u32 v26, v27, v26, s51
	v_and_or_b32 v25, v26, s48, v25
	v_lshlrev_b32_e32 v26, 16, v24
	v_and_b32_e32 v27, 0xffff0000, v24
	global_store_dword v[12:13], v25, off offset:256
	v_pk_mul_f32 v[24:25], v[26:27], v[26:27]
	v_lshlrev_b32_e32 v30, 16, v23
	v_add_f32_e32 v24, v24, v25
	v_and_b32_e32 v31, 0xffff0000, v23
	v_pk_mul_f32 v[32:33], v[30:31], v[30:31]
	s_waitcnt lgkmcnt(0)
	s_nop 1
	v_add_f32_dpp v24, v24, v24 quad_perm:[1,0,3,2] row_mask:0xf bank_mask:0xf
	v_add_f32_e32 v23, v32, v33
	s_waitcnt lgkmcnt(0)
	s_nop 1
	v_add_f32_dpp v24, v24, v24 quad_perm:[2,3,0,1] row_mask:0xf bank_mask:0xf
	s_waitcnt lgkmcnt(0)
	s_nop 1
	v_add_f32_dpp v24, v24, v24 row_half_mirror row_mask:0xf bank_mask:0xf
	s_waitcnt lgkmcnt(0)
	s_nop 1
	v_add_f32_dpp v24, v24, v24 row_mirror row_mask:0xf bank_mask:0xf
	v_mov_b32_e32 v25, v24
	s_waitcnt lgkmcnt(0)
	s_nop 1
	v_permlane16_swap_b32_e32 v24, v25
	v_add_f32_e32 v25, v24, v25
	v_mov_b32_e32 v29, v25
	s_nop 1
	v_permlane32_swap_b32_e32 v25, v29
	s_waitcnt lgkmcnt(0)
	s_nop 1
	v_add_f32_dpp v23, v23, v23 quad_perm:[1,0,3,2] row_mask:0xf bank_mask:0xf
	s_waitcnt lgkmcnt(0)
	s_nop 1
	v_add_f32_dpp v23, v23, v23 quad_perm:[2,3,0,1] row_mask:0xf bank_mask:0xf
	s_waitcnt lgkmcnt(0)
	s_nop 1
	v_add_f32_dpp v23, v23, v23 row_half_mirror row_mask:0xf bank_mask:0xf
	s_waitcnt lgkmcnt(0)
	s_nop 1
	v_add_f32_dpp v23, v23, v23 row_mirror row_mask:0xf bank_mask:0xf
	v_mov_b32_e32 v24, v23
	s_waitcnt lgkmcnt(0)
	s_nop 1
	v_permlane16_swap_b32_e32 v23, v24
	v_add_f32_e32 v24, v23, v24
	v_mov_b32_e32 v28, v24
	s_nop 1
	v_permlane32_swap_b32_e32 v24, v28
	v_pk_add_f32 v[24:25], v[24:25], v[28:29]
	v_lshlrev_b32_e32 v28, 16, v21
	v_pk_fma_f32 v[24:25], v[24:25], s[60:61], v[10:11] op_sel_hi:[1,0,0]
	v_and_b32_e32 v29, 0xffff0000, v21
	v_mul_f32_e32 v23, 0x4b800000, v25
	v_cmp_gt_f32_e64 s[2:3], s33, v25
	v_cmp_gt_f32_e32 vcc, s33, v24
	s_nop 0
	v_cndmask_b32_e64 v23, v25, v23, s[2:3]
	v_rsq_f32_e32 v23, v23
	s_nop 0
	v_mul_f32_e32 v25, 0x45800000, v23
	v_cndmask_b32_e64 v23, v23, v25, s[2:3]
	v_mul_f32_e32 v25, v23, v26
	v_mul_f32_e32 v23, v23, v27
	v_mul_f32_e32 v23, v5, v23
	v_mul_f32_e32 v25, v4, v25
	v_mul_f32_e32 v26, v8, v23
	v_mul_f32_e32 v23, v9, v23
	v_fma_f32 v23, v8, v25, -v23
	v_fmac_f32_e32 v26, v9, v25
	v_bfe_u32 v25, v23, 16, 1
	v_add3_u32 v23, v23, v25, s51
	v_bfe_u32 v25, v26, 16, 1
	v_lshrrev_b32_e32 v23, 16, v23
	v_add3_u32 v25, v26, v25, s51
	v_and_or_b32 v23, v25, s48, v23
	global_store_dword v[12:13], v23, off offset:512
	v_mul_f32_e32 v23, 0x4b800000, v24
	v_cndmask_b32_e32 v23, v24, v23, vcc
	v_rsq_f32_e32 v23, v23
	s_nop 0
	v_mul_f32_e32 v24, 0x45800000, v23
	v_cndmask_b32_e32 v23, v23, v24, vcc
	v_mul_f32_e32 v24, v23, v30
	v_mul_f32_e32 v23, v23, v31
	v_mul_f32_e32 v23, v5, v23
	v_mul_f32_e32 v24, v4, v24
	v_mul_f32_e32 v25, v8, v23
	v_mul_f32_e32 v23, v9, v23
	v_fma_f32 v23, v8, v24, -v23
	v_fmac_f32_e32 v25, v9, v24
	v_bfe_u32 v24, v23, 16, 1
	v_add3_u32 v23, v23, v24, s51
	v_bfe_u32 v24, v25, 16, 1
	v_lshrrev_b32_e32 v23, 16, v23
	v_add3_u32 v24, v25, v24, s51
	v_and_or_b32 v23, v24, s48, v23
	v_lshlrev_b32_e32 v24, 16, v22
	v_and_b32_e32 v25, 0xffff0000, v22
	global_store_dword v[12:13], v23, off offset:768
	v_pk_mul_f32 v[22:23], v[24:25], v[24:25]
	v_pk_mul_f32 v[30:31], v[28:29], v[28:29]
	v_add_f32_e32 v22, v22, v23
	v_add_f32_e32 v21, v30, v31
	s_waitcnt lgkmcnt(0)
	s_nop 1
	v_add_f32_dpp v22, v22, v22 quad_perm:[1,0,3,2] row_mask:0xf bank_mask:0xf
	s_waitcnt lgkmcnt(0)
	s_nop 1
	v_add_f32_dpp v22, v22, v22 quad_perm:[2,3,0,1] row_mask:0xf bank_mask:0xf
	s_waitcnt lgkmcnt(0)
	s_nop 1
	v_add_f32_dpp v22, v22, v22 row_half_mirror row_mask:0xf bank_mask:0xf
	s_waitcnt lgkmcnt(0)
	s_nop 1
	v_add_f32_dpp v22, v22, v22 row_mirror row_mask:0xf bank_mask:0xf
	v_mov_b32_e32 v23, v22
	s_waitcnt lgkmcnt(0)
	s_nop 1
	v_permlane16_swap_b32_e32 v22, v23
	v_add_f32_e32 v23, v22, v23
	v_mov_b32_e32 v27, v23
	s_nop 1
	v_permlane32_swap_b32_e32 v23, v27
	s_waitcnt lgkmcnt(0)
	s_nop 1
	v_add_f32_dpp v21, v21, v21 quad_perm:[1,0,3,2] row_mask:0xf bank_mask:0xf
	s_waitcnt lgkmcnt(0)
	s_nop 1
	v_add_f32_dpp v21, v21, v21 quad_perm:[2,3,0,1] row_mask:0xf bank_mask:0xf
	s_waitcnt lgkmcnt(0)
	s_nop 1
	v_add_f32_dpp v21, v21, v21 row_half_mirror row_mask:0xf bank_mask:0xf
	s_waitcnt lgkmcnt(0)
	s_nop 1
	v_add_f32_dpp v21, v21, v21 row_mirror row_mask:0xf bank_mask:0xf
	v_mov_b32_e32 v22, v21
	s_waitcnt lgkmcnt(0)
	s_nop 1
	v_permlane16_swap_b32_e32 v21, v22
	v_add_f32_e32 v22, v21, v22
	v_mov_b32_e32 v26, v22
	s_nop 1
	v_permlane32_swap_b32_e32 v22, v26
	v_pk_add_f32 v[22:23], v[22:23], v[26:27]
	v_lshlrev_b32_e32 v26, 16, v19
	v_pk_fma_f32 v[22:23], v[22:23], s[60:61], v[10:11] op_sel_hi:[1,0,0]
	v_and_b32_e32 v27, 0xffff0000, v19
	v_mul_f32_e32 v21, 0x4b800000, v23
	v_cmp_gt_f32_e64 s[2:3], s33, v23
	v_cmp_gt_f32_e32 vcc, s33, v22
	s_nop 0
	v_cndmask_b32_e64 v21, v23, v21, s[2:3]
	v_rsq_f32_e32 v21, v21
	s_nop 0
	v_mul_f32_e32 v23, 0x45800000, v21
	v_cndmask_b32_e64 v21, v21, v23, s[2:3]
	v_mul_f32_e32 v23, v21, v24
	v_mul_f32_e32 v21, v21, v25
	v_mul_f32_e32 v21, v5, v21
	v_mul_f32_e32 v23, v4, v23
	v_mul_f32_e32 v24, v8, v21
	v_mul_f32_e32 v21, v9, v21
	v_fma_f32 v21, v8, v23, -v21
	v_fmac_f32_e32 v24, v9, v23
	v_bfe_u32 v23, v21, 16, 1
	v_add3_u32 v21, v21, v23, s51
	v_bfe_u32 v23, v24, 16, 1
	v_lshrrev_b32_e32 v21, 16, v21
	v_add3_u32 v23, v24, v23, s51
	v_and_or_b32 v21, v23, s48, v21
	global_store_dword v[12:13], v21, off offset:1024
	v_mul_f32_e32 v21, 0x4b800000, v22
	v_cndmask_b32_e32 v21, v22, v21, vcc
	v_rsq_f32_e32 v21, v21
	s_nop 0
	v_mul_f32_e32 v22, 0x45800000, v21
	v_cndmask_b32_e32 v21, v21, v22, vcc
	v_mul_f32_e32 v22, v21, v28
	v_mul_f32_e32 v21, v21, v29
	v_mul_f32_e32 v21, v5, v21
	v_mul_f32_e32 v22, v4, v22
	v_mul_f32_e32 v23, v8, v21
	v_mul_f32_e32 v21, v9, v21
	v_fma_f32 v21, v8, v22, -v21
	v_fmac_f32_e32 v23, v9, v22
	v_bfe_u32 v22, v21, 16, 1
	v_add3_u32 v21, v21, v22, s51
	v_bfe_u32 v22, v23, 16, 1
	v_lshrrev_b32_e32 v21, 16, v21
	v_add3_u32 v22, v23, v22, s51
	v_and_or_b32 v21, v22, s48, v21
	v_lshlrev_b32_e32 v22, 16, v20
	v_and_b32_e32 v23, 0xffff0000, v20
	global_store_dword v[12:13], v21, off offset:1280
	v_pk_mul_f32 v[20:21], v[22:23], v[22:23]
	v_pk_mul_f32 v[28:29], v[26:27], v[26:27]
	v_add_f32_e32 v20, v20, v21
	v_add_f32_e32 v19, v28, v29
	s_waitcnt lgkmcnt(0)
	s_nop 1
	v_add_f32_dpp v20, v20, v20 quad_perm:[1,0,3,2] row_mask:0xf bank_mask:0xf
	s_waitcnt lgkmcnt(0)
	s_nop 1
	v_add_f32_dpp v20, v20, v20 quad_perm:[2,3,0,1] row_mask:0xf bank_mask:0xf
	s_waitcnt lgkmcnt(0)
	s_nop 1
	v_add_f32_dpp v20, v20, v20 row_half_mirror row_mask:0xf bank_mask:0xf
	s_waitcnt lgkmcnt(0)
	s_nop 1
	v_add_f32_dpp v20, v20, v20 row_mirror row_mask:0xf bank_mask:0xf
	v_mov_b32_e32 v21, v20
	s_waitcnt lgkmcnt(0)
	s_nop 1
	v_permlane16_swap_b32_e32 v20, v21
	v_add_f32_e32 v21, v20, v21
	v_mov_b32_e32 v25, v21
	s_nop 1
	v_permlane32_swap_b32_e32 v21, v25
	s_waitcnt lgkmcnt(0)
	s_nop 1
	v_add_f32_dpp v19, v19, v19 quad_perm:[1,0,3,2] row_mask:0xf bank_mask:0xf
	s_waitcnt lgkmcnt(0)
	s_nop 1
	v_add_f32_dpp v19, v19, v19 quad_perm:[2,3,0,1] row_mask:0xf bank_mask:0xf
	s_waitcnt lgkmcnt(0)
	s_nop 1
	v_add_f32_dpp v19, v19, v19 row_half_mirror row_mask:0xf bank_mask:0xf
	s_waitcnt lgkmcnt(0)
	s_nop 1
	v_add_f32_dpp v19, v19, v19 row_mirror row_mask:0xf bank_mask:0xf
	v_mov_b32_e32 v20, v19
	s_waitcnt lgkmcnt(0)
	s_nop 1
	v_permlane16_swap_b32_e32 v19, v20
	v_add_f32_e32 v20, v19, v20
	v_mov_b32_e32 v24, v20
	s_nop 1
	v_permlane32_swap_b32_e32 v20, v24
	v_pk_add_f32 v[20:21], v[20:21], v[24:25]
	v_lshlrev_b32_e32 v24, 16, v17
	v_pk_fma_f32 v[20:21], v[20:21], s[60:61], v[10:11] op_sel_hi:[1,0,0]
	v_and_b32_e32 v25, 0xffff0000, v17
	v_mul_f32_e32 v19, 0x4b800000, v21
	v_cmp_gt_f32_e64 s[2:3], s33, v21
	v_cmp_gt_f32_e32 vcc, s33, v20
	s_nop 0
	v_cndmask_b32_e64 v19, v21, v19, s[2:3]
	v_rsq_f32_e32 v19, v19
	s_nop 0
	v_mul_f32_e32 v21, 0x45800000, v19
	v_cndmask_b32_e64 v19, v19, v21, s[2:3]
	v_mul_f32_e32 v21, v19, v22
	v_mul_f32_e32 v19, v19, v23
	v_mul_f32_e32 v19, v5, v19
	v_mul_f32_e32 v21, v4, v21
	v_mul_f32_e32 v22, v8, v19
	v_mul_f32_e32 v19, v9, v19
	v_fma_f32 v19, v8, v21, -v19
	v_fmac_f32_e32 v22, v9, v21
	v_bfe_u32 v21, v19, 16, 1
	v_add3_u32 v19, v19, v21, s51
	v_bfe_u32 v21, v22, 16, 1
	v_lshrrev_b32_e32 v19, 16, v19
	v_add3_u32 v21, v22, v21, s51
	v_and_or_b32 v19, v21, s48, v19
	global_store_dword v[12:13], v19, off offset:1536
	v_mul_f32_e32 v19, 0x4b800000, v20
	v_cndmask_b32_e32 v19, v20, v19, vcc
	v_rsq_f32_e32 v19, v19
	v_lshl_add_u64 v[22:23], v[6:7], 0, s[12:13]
	v_mul_f32_e32 v20, 0x45800000, v19
	v_cndmask_b32_e32 v19, v19, v20, vcc
	v_mul_f32_e32 v20, v19, v26
	v_mul_f32_e32 v19, v19, v27
	v_mul_f32_e32 v19, v5, v19
	v_mul_f32_e32 v20, v4, v20
	v_mul_f32_e32 v21, v8, v19
	v_mul_f32_e32 v19, v9, v19
	v_fma_f32 v19, v8, v20, -v19
	v_fmac_f32_e32 v21, v9, v20
	v_bfe_u32 v20, v19, 16, 1
	v_add3_u32 v19, v19, v20, s51
	v_bfe_u32 v20, v21, 16, 1
	v_lshrrev_b32_e32 v19, 16, v19
	v_add3_u32 v20, v21, v20, s51
	v_and_or_b32 v19, v20, s48, v19
	global_store_dword v[12:13], v19, off offset:1792
	v_lshlrev_b32_e32 v12, 16, v18
	v_and_b32_e32 v13, 0xffff0000, v18
	v_pk_mul_f32 v[18:19], v[12:13], v[12:13]
	v_pk_mul_f32 v[26:27], v[24:25], v[24:25]
	v_add_f32_e32 v18, v18, v19
	v_add_f32_e32 v17, v26, v27
	s_waitcnt lgkmcnt(0)
	s_nop 1
	v_add_f32_dpp v18, v18, v18 quad_perm:[1,0,3,2] row_mask:0xf bank_mask:0xf
	s_waitcnt lgkmcnt(0)
	s_nop 1
	v_add_f32_dpp v18, v18, v18 quad_perm:[2,3,0,1] row_mask:0xf bank_mask:0xf
	s_waitcnt lgkmcnt(0)
	s_nop 1
	v_add_f32_dpp v18, v18, v18 row_half_mirror row_mask:0xf bank_mask:0xf
	s_waitcnt lgkmcnt(0)
	s_nop 1
	v_add_f32_dpp v18, v18, v18 row_mirror row_mask:0xf bank_mask:0xf
	v_mov_b32_e32 v19, v18
	s_waitcnt lgkmcnt(0)
	s_nop 1
	v_permlane16_swap_b32_e32 v18, v19
	v_add_f32_e32 v19, v18, v19
	v_mov_b32_e32 v21, v19
	s_nop 1
	v_permlane32_swap_b32_e32 v19, v21
	s_waitcnt lgkmcnt(0)
	s_nop 1
	v_add_f32_dpp v17, v17, v17 quad_perm:[1,0,3,2] row_mask:0xf bank_mask:0xf
	s_waitcnt lgkmcnt(0)
	s_nop 1
	v_add_f32_dpp v17, v17, v17 quad_perm:[2,3,0,1] row_mask:0xf bank_mask:0xf
	s_waitcnt lgkmcnt(0)
	s_nop 1
	v_add_f32_dpp v17, v17, v17 row_half_mirror row_mask:0xf bank_mask:0xf
	s_waitcnt lgkmcnt(0)
	s_nop 1
	v_add_f32_dpp v17, v17, v17 row_mirror row_mask:0xf bank_mask:0xf
	v_mov_b32_e32 v18, v17
	s_waitcnt lgkmcnt(0)
	s_nop 1
	v_permlane16_swap_b32_e32 v17, v18
	v_add_f32_e32 v18, v17, v18
	v_mov_b32_e32 v20, v18
	s_nop 1
	v_permlane32_swap_b32_e32 v18, v20
	v_pk_add_f32 v[18:19], v[18:19], v[20:21]
	s_nop 0
	v_pk_fma_f32 v[10:11], v[18:19], s[60:61], v[10:11] op_sel_hi:[1,0,0]
	s_nop 0
	v_mul_f32_e32 v17, 0x4b800000, v11
	v_cmp_gt_f32_e64 s[2:3], s33, v11
	v_cmp_gt_f32_e32 vcc, s33, v10
	s_nop 0
	v_cndmask_b32_e64 v11, v11, v17, s[2:3]
	v_rsq_f32_e32 v11, v11
	s_nop 0
	v_mul_f32_e32 v17, 0x45800000, v11
	v_cndmask_b32_e64 v11, v11, v17, s[2:3]
	v_mul_f32_e32 v12, v11, v12
	v_mul_f32_e32 v11, v11, v13
	v_mul_f32_e32 v11, v3, v11
	v_mul_f32_e32 v12, v2, v12
	v_mul_f32_e32 v13, v8, v11
	v_mul_f32_e32 v11, v9, v11
	v_fma_f32 v11, v8, v12, -v11
	v_fmac_f32_e32 v13, v9, v12
	v_bfe_u32 v12, v11, 16, 1
	v_add3_u32 v11, v11, v12, s51
	v_bfe_u32 v12, v13, 16, 1
	v_lshrrev_b32_e32 v11, 16, v11
	v_add3_u32 v12, v13, v12, s51
	v_and_or_b32 v11, v12, s48, v11
	global_store_dword v[22:23], v11, off
	v_mul_f32_e32 v11, 0x4b800000, v10
	v_cndmask_b32_e32 v10, v10, v11, vcc
	v_rsq_f32_e32 v10, v10
	v_readlane_b32 s2, v255, 11
	s_add_u32 s8, s8, s2
	s_mul_hi_i32 s2, s54, 0xa00
	v_mul_f32_e32 v11, 0x45800000, v10
	v_cndmask_b32_e32 v10, v10, v11, vcc
	v_mul_f32_e32 v11, v10, v24
	v_mul_f32_e32 v10, v10, v25
	v_mul_f32_e32 v10, v3, v10
	v_mul_f32_e32 v11, v2, v11
	v_mul_f32_e32 v12, v8, v10
	v_fmac_f32_e32 v12, v9, v11
	v_mul_f32_e32 v9, v9, v10
	v_fma_f32 v8, v8, v11, -v9
	v_bfe_u32 v9, v8, 16, 1
	s_addc_u32 s9, s9, s2
	v_readlane_b32 s2, v255, 12
	v_add3_u32 v8, v8, v9, s51
	v_bfe_u32 v9, v12, 16, 1
	s_add_u32 s10, s10, s2
	s_mul_hi_i32 s2, s54, 0x6c00
	v_lshrrev_b32_e32 v8, 16, v8
	v_add3_u32 v9, v12, v9, s51
	s_addc_u32 s11, s11, s2
	v_and_or_b32 v8, v9, s48, v8
	s_cmpk_gt_i32 s5, 0x23ff
	global_store_dword v[22:23], v8, off offset:256
	global_store_dword v[22:23], v15, off offset:512
	global_store_dword v[22:23], v16, off offset:768
	s_cbranch_scc1 .LBB0_750

.LBB0_882:
	s_nop 3
	v_max_f32_e32 v170, v1, v1
	v_max_f32_e32 v171, v0, v0
	v_max_f32_e32 v170, v171, v170
	v_max_f32_e32 v171, v3, v3
	v_max_f32_e32 v172, v2, v2
	v_max_f32_e32 v171, v172, v171
	v_max_f32_e32 v172, v7, v7
	v_max_f32_e32 v173, v6, v6
	v_max_f32_e32 v172, v173, v172
	v_max3_f32 v172, v4, v5, v172
	v_max3_f32 v170, v170, v171, v172
	v_mov_b32_e32 v171, v170
	s_waitcnt lgkmcnt(0)
	s_nop 1
	v_permlane16_swap_b32_e32 v170, v171
	v_max_f32_e32 v171, v171, v171
	v_max_f32_e32 v170, v170, v171
	v_mov_b32_e32 v171, v170
	s_nop 1
	v_permlane32_swap_b32_e32 v170, v171
	v_max3_f32 v170, v237, v170, v171
	v_cmp_eq_f32_e32 vcc, v170, v237
	s_cmp_eq_u64 vcc, exec
	s_cbranch_scc1 .LBB0_884
	v_sub_f32_e32 v171, v237, v170
	v_exp_f32_e32 v172, v171
	v_mov_b32_e32 v237, v170
	v_mul_f32_e32 v233, v233, v172
	v_pk_mul_f32 v[100:101], v[100:101], v[172:173] op_sel_hi:[1,0]
	v_pk_mul_f32 v[98:99], v[98:99], v[172:173] op_sel_hi:[1,0]
	v_pk_mul_f32 v[104:105], v[104:105], v[172:173] op_sel_hi:[1,0]
	v_pk_mul_f32 v[102:103], v[102:103], v[172:173] op_sel_hi:[1,0]
	v_pk_mul_f32 v[94:95], v[94:95], v[172:173] op_sel_hi:[1,0]
	v_pk_mul_f32 v[92:93], v[92:93], v[172:173] op_sel_hi:[1,0]
	v_pk_mul_f32 v[90:91], v[90:91], v[172:173] op_sel_hi:[1,0]
	v_pk_mul_f32 v[88:89], v[88:89], v[172:173] op_sel_hi:[1,0]

.LBB0_889:
	s_nop 0
	v_max_f32_e32 v170, v1, v1
	v_max_f32_e32 v171, v0, v0
	v_max_f32_e32 v170, v171, v170
	v_max_f32_e32 v171, v3, v3
	v_max_f32_e32 v172, v2, v2
	v_max_f32_e32 v171, v172, v171
	v_max_f32_e32 v172, v7, v7
	v_max_f32_e32 v173, v6, v6
	v_max_f32_e32 v172, v173, v172
	v_max3_f32 v172, v4, v5, v172
	v_max3_f32 v170, v170, v171, v172
	v_mov_b32_e32 v171, v170
	s_waitcnt lgkmcnt(0)
	s_nop 1
	v_permlane16_swap_b32_e32 v170, v171
	v_max_f32_e32 v171, v171, v171
	v_max_f32_e32 v170, v170, v171
	v_mov_b32_e32 v171, v170
	s_nop 1
	v_permlane32_swap_b32_e32 v170, v171
	v_max3_f32 v170, v236, v170, v171
	v_cmp_eq_f32_e32 vcc, v170, v236
	s_cmp_eq_u64 vcc, exec
	s_cbranch_scc1 .LBB0_891
	v_sub_f32_e32 v171, v236, v170
	v_exp_f32_e32 v172, v171
	v_mov_b32_e32 v236, v170
	v_mul_f32_e32 v232, v232, v172
	v_pk_mul_f32 v[54:55], v[54:55], v[172:173] op_sel_hi:[1,0]
	v_pk_mul_f32 v[52:53], v[52:53], v[172:173] op_sel_hi:[1,0]
	v_pk_mul_f32 v[50:51], v[50:51], v[172:173] op_sel_hi:[1,0]
	v_pk_mul_f32 v[48:49], v[48:49], v[172:173] op_sel_hi:[1,0]
	v_pk_mul_f32 v[46:47], v[46:47], v[172:173] op_sel_hi:[1,0]
	v_pk_mul_f32 v[44:45], v[44:45], v[172:173] op_sel_hi:[1,0]
	v_pk_mul_f32 v[42:43], v[42:43], v[172:173] op_sel_hi:[1,0]
	v_pk_mul_f32 v[40:41], v[40:41], v[172:173] op_sel_hi:[1,0]

.LBB0_895:
	s_nop 3
	v_max_f32_e32 v170, v1, v1
	v_max_f32_e32 v171, v0, v0
	v_max_f32_e32 v170, v171, v170
	v_max_f32_e32 v171, v3, v3
	v_max_f32_e32 v172, v2, v2
	v_max_f32_e32 v171, v172, v171
	v_max_f32_e32 v172, v7, v7
	v_max_f32_e32 v173, v6, v6
	v_max_f32_e32 v172, v173, v172
	v_max3_f32 v172, v4, v5, v172
	v_max3_f32 v170, v170, v171, v172
	v_mov_b32_e32 v171, v170
	s_waitcnt lgkmcnt(0)
	s_nop 1
	v_permlane16_swap_b32_e32 v170, v171
	v_max_f32_e32 v171, v171, v171
	v_max_f32_e32 v170, v170, v171
	v_mov_b32_e32 v171, v170
	s_nop 1
	v_permlane32_swap_b32_e32 v170, v171
	v_max3_f32 v177, v235, v170, v171
	v_cmp_eq_f32_e32 vcc, v177, v235
	s_cmp_eq_u64 vcc, exec
	s_cbranch_scc1 .LBB0_897
	v_sub_f32_e32 v170, v235, v177
	v_exp_f32_e32 v170, v170
	v_mov_b32_e32 v235, v177
	v_mul_f32_e32 v231, v231, v170
	v_pk_mul_f32 v[38:39], v[38:39], v[170:171] op_sel_hi:[1,0]
	v_pk_mul_f32 v[36:37], v[36:37], v[170:171] op_sel_hi:[1,0]
	v_pk_mul_f32 v[34:35], v[34:35], v[170:171] op_sel_hi:[1,0]
	v_pk_mul_f32 v[32:33], v[32:33], v[170:171] op_sel_hi:[1,0]
	v_pk_mul_f32 v[30:31], v[30:31], v[170:171] op_sel_hi:[1,0]
	v_pk_mul_f32 v[28:29], v[28:29], v[170:171] op_sel_hi:[1,0]
	v_pk_mul_f32 v[26:27], v[26:27], v[170:171] op_sel_hi:[1,0]
	v_pk_mul_f32 v[24:25], v[24:25], v[170:171] op_sel_hi:[1,0]

.LBB0_902:
	s_nop 3
	v_max_f32_e32 v154, v1, v1
	v_max_f32_e32 v155, v0, v0
	v_max_f32_e32 v154, v155, v154
	v_max_f32_e32 v155, v3, v3
	v_max_f32_e32 v156, v2, v2
	v_max_f32_e32 v155, v156, v155
	v_max_f32_e32 v156, v7, v7
	v_max_f32_e32 v157, v6, v6
	v_max_f32_e32 v156, v157, v156
	v_max3_f32 v156, v4, v5, v156
	v_max3_f32 v154, v154, v155, v156
	v_mov_b32_e32 v155, v154
	s_waitcnt lgkmcnt(0)
	s_nop 1
	v_permlane16_swap_b32_e32 v154, v155
	v_max_f32_e32 v155, v155, v155
	v_max_f32_e32 v154, v154, v155
	v_mov_b32_e32 v155, v154
	s_nop 1
	v_permlane32_swap_b32_e32 v154, v155
	v_max3_f32 v154, v234, v154, v155
	v_cmp_eq_f32_e32 vcc, v154, v234
	s_cmp_eq_u64 vcc, exec
	s_cbranch_scc1 .LBB0_904
	v_sub_f32_e32 v155, v234, v154
	v_exp_f32_e32 v156, v155
	v_mov_b32_e32 v234, v154
	v_mul_f32_e32 v230, v230, v156
	v_pk_mul_f32 v[22:23], v[22:23], v[156:157] op_sel_hi:[1,0]
	v_pk_mul_f32 v[20:21], v[20:21], v[156:157] op_sel_hi:[1,0]
	v_pk_mul_f32 v[18:19], v[18:19], v[156:157] op_sel_hi:[1,0]
	v_pk_mul_f32 v[16:17], v[16:17], v[156:157] op_sel_hi:[1,0]
	v_pk_mul_f32 v[14:15], v[14:15], v[156:157] op_sel_hi:[1,0]
	v_pk_mul_f32 v[12:13], v[12:13], v[156:157] op_sel_hi:[1,0]
	v_pk_mul_f32 v[10:11], v[10:11], v[156:157] op_sel_hi:[1,0]
	v_pk_mul_f32 v[8:9], v[8:9], v[156:157] op_sel_hi:[1,0]

.LBB0_1534:
	v_mul_f32_e32 v64, v61, v61
	v_mul_f32_e32 v65, v57, v57
	v_fmac_f32_e32 v64, v60, v60
	v_fmac_f32_e32 v65, v56, v56
	v_fmac_f32_e32 v64, v62, v62
	v_fmac_f32_e32 v65, v58, v58
	v_fmac_f32_e32 v64, v63, v63
	v_fmac_f32_e32 v65, v59, v59
	v_add_f32_e32 v64, v65, v64
	v_mul_f32_e32 v65, v53, v53
	v_fmac_f32_e32 v65, v52, v52
	v_fmac_f32_e32 v65, v54, v54
	v_fmac_f32_e32 v65, v55, v55
	v_add_f32_e32 v64, v65, v64
	v_mul_f32_e32 v65, v49, v49
	v_fmac_f32_e32 v65, v48, v48
	v_fmac_f32_e32 v65, v50, v50
	v_fmac_f32_e32 v65, v51, v51
	v_add_f32_e32 v64, v65, v64
	v_mul_f32_e32 v65, v45, v45
	v_fmac_f32_e32 v65, v44, v44
	v_fmac_f32_e32 v65, v46, v46
	v_fmac_f32_e32 v65, v47, v47
	v_add_f32_e32 v64, v65, v64
	v_mul_f32_e32 v65, v41, v41
	v_fmac_f32_e32 v65, v40, v40
	v_fmac_f32_e32 v65, v42, v42
	v_fmac_f32_e32 v65, v43, v43
	v_add_f32_e32 v64, v65, v64
	v_mul_f32_e32 v65, v5, v5
	v_fmac_f32_e32 v65, v4, v4
	v_fmac_f32_e32 v65, v6, v6
	v_fmac_f32_e32 v65, v7, v7
	v_add_f32_e32 v64, v65, v64
	v_mul_f32_e32 v65, v1, v1
	v_fmac_f32_e32 v65, v0, v0
	v_fmac_f32_e32 v65, v2, v2
	v_fmac_f32_e32 v65, v3, v3
	v_add_f32_e32 v64, v65, v64
	s_min_i32 s5, s10, 0x2000
	s_ashr_i32 s5, s5, 11
	s_mul_hi_i32 s10, s5, 0xc000
	s_mul_i32 s5, s5, 0xc000
	s_waitcnt lgkmcnt(0)
	s_nop 1
	v_add_f32_dpp v64, v64, v64 quad_perm:[1,0,3,2] row_mask:0xf bank_mask:0xf
	s_add_u32 s5, s55, s5
	s_addc_u32 s13, s69, s10
	s_add_u32 s10, s5, 0x8000
	s_addc_u32 s11, s13, 0
	s_waitcnt lgkmcnt(0)
	s_nop 1
	v_add_f32_dpp v64, v64, v64 quad_perm:[2,3,0,1] row_mask:0xf bank_mask:0xf
	s_add_u32 s12, s5, 0x6000
	s_addc_u32 s13, s13, 0
	v_mov_b32_e32 v122, v60
	v_mov_b32_e32 v123, v62
	s_waitcnt lgkmcnt(0)
	s_nop 1
	v_add_f32_dpp v64, v64, v64 row_half_mirror row_mask:0xf bank_mask:0xf
	v_mov_b32_e32 v62, v61
	v_mov_b32_e32 v93, 1
	v_mov_b32_e32 v217, 1
	s_waitcnt lgkmcnt(0)
	s_nop 1
	v_add_f32_dpp v64, v64, v64 row_mirror row_mask:0xf bank_mask:0xf
	v_mov_b32_e32 v65, v64
	s_waitcnt lgkmcnt(0)
	s_nop 1
	v_permlane16_swap_b32_e32 v64, v65
	v_add_f32_e32 v64, v64, v65
	v_mov_b32_e32 v65, v64
	s_nop 1
	v_permlane32_swap_b32_e32 v64, v65
	v_add_f32_e32 v64, v64, v65
	v_mov_b32_e32 v65, 0x358637bd
	v_fmamk_f32 v64, v64, 0x3a000000, v65
	v_cmp_gt_f32_e32 vcc, s33, v64
	v_mul_f32_e32 v65, 0x4b800000, v64
	s_nop 0
	v_cndmask_b32_e32 v64, v64, v65, vcc
	v_rsq_f32_e32 v64, v64
	s_nop 0
	v_mul_f32_e32 v65, 0x45800000, v64
	v_cndmask_b32_e32 v100, v64, v65, vcc
	global_load_dwordx4 v[64:67], v[78:79], off
	global_load_dwordx4 v[68:71], v96, s[10:11]
	global_load_dwordx4 v[72:75], v96, s[12:13]
	v_pk_mul_f32 v[122:123], v[122:123], v[100:101] op_sel_hi:[1,0]
	v_pk_mul_f32 v[60:61], v[62:63], v[100:101] op_sel_hi:[1,0]
	s_and_b64 vcc, exec, s[8:9]
	s_waitcnt vmcnt(2)
	v_mov_b32_e32 v124, v64
	v_mov_b32_e32 v125, v66
	v_pk_mul_f32 v[122:123], v[124:125], v[122:123]
	s_waitcnt vmcnt(1)
	v_mov_b32_e32 v125, v70
	v_mov_b32_e32 v66, v65
	v_mov_b32_e32 v70, v69
	v_mov_b32_e32 v124, v68
	s_waitcnt vmcnt(0)
	v_mov_b32_e32 v127, v74
	v_pk_mul_f32 v[60:61], v[66:67], v[60:61]
	v_pk_add_f32 v[62:63], v[70:71], 1.0 op_sel_hi:[1,0]
	v_mov_b32_e32 v74, v73
	v_pk_add_f32 v[124:125], v[124:125], 1.0 op_sel_hi:[1,0]
	v_mov_b32_e32 v126, v72
	v_pk_fma_f32 v[60:61], v[62:63], v[60:61], v[74:75]
	v_pk_fma_f32 v[122:123], v[124:125], v[122:123], v[126:127]
	v_and_b32_sdwa v64, v61, v93 dst_sel:DWORD dst_unused:UNUSED_PAD src0_sel:WORD_1 src1_sel:DWORD
	v_and_b32_sdwa v65, v60, v93 dst_sel:DWORD dst_unused:UNUSED_PAD src0_sel:WORD_1 src1_sel:DWORD
	v_and_b32_sdwa v62, v123, v93 dst_sel:DWORD dst_unused:UNUSED_PAD src0_sel:WORD_1 src1_sel:DWORD
	v_and_b32_sdwa v63, v122, v93 dst_sel:DWORD dst_unused:UNUSED_PAD src0_sel:WORD_1 src1_sel:DWORD
	v_add3_u32 v61, v61, v64, s51
	v_add3_u32 v60, v60, v65, s51
	v_add3_u32 v63, v122, v63, s51
	v_add3_u32 v62, v123, v62, s51
	v_and_b32_e32 v61, 0xffff0000, v61
	v_and_b32_e32 v60, 0xffff0000, v60
	v_or_b32_sdwa v61, v61, v62 dst_sel:DWORD dst_unused:UNUSED_PAD src0_sel:DWORD src1_sel:WORD_1
	v_or_b32_sdwa v60, v60, v63 dst_sel:DWORD dst_unused:UNUSED_PAD src0_sel:DWORD src1_sel:WORD_1
	global_store_dwordx2 v[98:99], v[60:61], off
	global_load_dwordx4 v[60:63], v[78:79], off offset:1024
	s_nop 0
	global_load_dwordx4 v[64:67], v81, s[10:11]
	global_load_dwordx4 v[68:71], v81, s[12:13]
	v_mov_b32_e32 v72, v56
	v_mov_b32_e32 v73, v58
	v_pk_mul_f32 v[72:73], v[72:73], v[100:101] op_sel_hi:[1,0]
	v_mov_b32_e32 v58, v57
	v_pk_mul_f32 v[56:57], v[58:59], v[100:101] op_sel_hi:[1,0]
	s_waitcnt vmcnt(2)
	v_mov_b32_e32 v74, v60
	v_mov_b32_e32 v75, v62
	v_pk_mul_f32 v[72:73], v[74:75], v[72:73]
	s_waitcnt vmcnt(1)
	v_mov_b32_e32 v75, v66
	v_mov_b32_e32 v62, v61
	v_mov_b32_e32 v66, v65
	v_mov_b32_e32 v74, v64
	s_waitcnt vmcnt(0)
	v_mov_b32_e32 v123, v70
	v_pk_mul_f32 v[56:57], v[62:63], v[56:57]
	v_pk_add_f32 v[58:59], v[66:67], 1.0 op_sel_hi:[1,0]
	v_mov_b32_e32 v70, v69
	v_pk_add_f32 v[74:75], v[74:75], 1.0 op_sel_hi:[1,0]
	v_mov_b32_e32 v122, v68
	v_pk_fma_f32 v[56:57], v[58:59], v[56:57], v[70:71]
	v_pk_fma_f32 v[72:73], v[74:75], v[72:73], v[122:123]
	v_and_b32_sdwa v60, v57, v93 dst_sel:DWORD dst_unused:UNUSED_PAD src0_sel:WORD_1 src1_sel:DWORD
	v_and_b32_sdwa v61, v56, v93 dst_sel:DWORD dst_unused:UNUSED_PAD src0_sel:WORD_1 src1_sel:DWORD
	v_and_b32_sdwa v58, v73, v93 dst_sel:DWORD dst_unused:UNUSED_PAD src0_sel:WORD_1 src1_sel:DWORD
	v_and_b32_sdwa v59, v72, v93 dst_sel:DWORD dst_unused:UNUSED_PAD src0_sel:WORD_1 src1_sel:DWORD
	v_add3_u32 v57, v57, v60, s51
	v_add3_u32 v56, v56, v61, s51
	v_add3_u32 v59, v72, v59, s51
	v_add3_u32 v58, v73, v58, s51
	v_and_b32_e32 v57, 0xffff0000, v57
	v_and_b32_e32 v56, 0xffff0000, v56
	v_or_b32_sdwa v57, v57, v58 dst_sel:DWORD dst_unused:UNUSED_PAD src0_sel:DWORD src1_sel:WORD_1
	v_or_b32_sdwa v56, v56, v59 dst_sel:DWORD dst_unused:UNUSED_PAD src0_sel:DWORD src1_sel:WORD_1
	global_store_dwordx2 v[98:99], v[56:57], off offset:512
	global_load_dwordx4 v[56:59], v[78:79], off offset:2048
	s_nop 0
	global_load_dwordx4 v[60:63], v85, s[10:11]
	global_load_dwordx4 v[64:67], v85, s[12:13]
	v_mov_b32_e32 v68, v52
	v_mov_b32_e32 v69, v54
	v_pk_mul_f32 v[68:69], v[68:69], v[100:101] op_sel_hi:[1,0]
	v_mov_b32_e32 v54, v53
	v_pk_mul_f32 v[52:53], v[54:55], v[100:101] op_sel_hi:[1,0]
	s_waitcnt vmcnt(2)
	v_mov_b32_e32 v70, v56
	v_mov_b32_e32 v71, v58
	v_pk_mul_f32 v[68:69], v[70:71], v[68:69]
	s_waitcnt vmcnt(1)
	v_mov_b32_e32 v71, v62
	v_mov_b32_e32 v58, v57
	v_mov_b32_e32 v62, v61
	v_mov_b32_e32 v70, v60
	s_waitcnt vmcnt(0)
	v_mov_b32_e32 v73, v66
	v_pk_mul_f32 v[52:53], v[58:59], v[52:53]
	v_pk_add_f32 v[54:55], v[62:63], 1.0 op_sel_hi:[1,0]
	v_mov_b32_e32 v66, v65
	v_pk_add_f32 v[70:71], v[70:71], 1.0 op_sel_hi:[1,0]
	v_mov_b32_e32 v72, v64
	v_pk_fma_f32 v[52:53], v[54:55], v[52:53], v[66:67]
	v_pk_fma_f32 v[68:69], v[70:71], v[68:69], v[72:73]
	v_and_b32_sdwa v56, v53, v93 dst_sel:DWORD dst_unused:UNUSED_PAD src0_sel:WORD_1 src1_sel:DWORD
	v_and_b32_sdwa v57, v52, v93 dst_sel:DWORD dst_unused:UNUSED_PAD src0_sel:WORD_1 src1_sel:DWORD
	v_and_b32_sdwa v54, v69, v93 dst_sel:DWORD dst_unused:UNUSED_PAD src0_sel:WORD_1 src1_sel:DWORD
	v_and_b32_sdwa v55, v68, v93 dst_sel:DWORD dst_unused:UNUSED_PAD src0_sel:WORD_1 src1_sel:DWORD
	v_add3_u32 v53, v53, v56, s51
	v_add3_u32 v52, v52, v57, s51
	v_add3_u32 v55, v68, v55, s51
	v_add3_u32 v54, v69, v54, s51
	v_and_b32_e32 v53, 0xffff0000, v53
	v_and_b32_e32 v52, 0xffff0000, v52
	v_or_b32_sdwa v53, v53, v54 dst_sel:DWORD dst_unused:UNUSED_PAD src0_sel:DWORD src1_sel:WORD_1
	v_or_b32_sdwa v52, v52, v55 dst_sel:DWORD dst_unused:UNUSED_PAD src0_sel:DWORD src1_sel:WORD_1
	global_store_dwordx2 v[98:99], v[52:53], off offset:1024
	global_load_dwordx4 v[52:55], v[78:79], off offset:3072
	s_nop 0
	global_load_dwordx4 v[56:59], v89, s[10:11]
	global_load_dwordx4 v[60:63], v89, s[12:13]
	v_mov_b32_e32 v64, v48
	v_mov_b32_e32 v65, v50
	v_pk_mul_f32 v[64:65], v[64:65], v[100:101] op_sel_hi:[1,0]
	v_mov_b32_e32 v50, v49
	v_pk_mul_f32 v[48:49], v[50:51], v[100:101] op_sel_hi:[1,0]
	s_waitcnt vmcnt(2)
	v_mov_b32_e32 v66, v52
	v_mov_b32_e32 v67, v54
	v_pk_mul_f32 v[64:65], v[64:65], v[66:67]
	s_waitcnt vmcnt(1)
	v_mov_b32_e32 v67, v58
	v_mov_b32_e32 v54, v53
	v_mov_b32_e32 v58, v57
	v_mov_b32_e32 v66, v56
	s_waitcnt vmcnt(0)
	v_mov_b32_e32 v69, v62
	v_pk_mul_f32 v[48:49], v[48:49], v[54:55]
	v_pk_add_f32 v[50:51], v[58:59], 1.0 op_sel_hi:[1,0]
	v_mov_b32_e32 v62, v61
	v_pk_add_f32 v[66:67], v[66:67], 1.0 op_sel_hi:[1,0]
	v_mov_b32_e32 v68, v60
	v_pk_fma_f32 v[48:49], v[48:49], v[50:51], v[62:63]
	v_pk_fma_f32 v[64:65], v[64:65], v[66:67], v[68:69]
	v_and_b32_sdwa v52, v49, v93 dst_sel:DWORD dst_unused:UNUSED_PAD src0_sel:WORD_1 src1_sel:DWORD
	v_and_b32_sdwa v53, v48, v93 dst_sel:DWORD dst_unused:UNUSED_PAD src0_sel:WORD_1 src1_sel:DWORD
	v_and_b32_sdwa v50, v65, v93 dst_sel:DWORD dst_unused:UNUSED_PAD src0_sel:WORD_1 src1_sel:DWORD
	v_and_b32_sdwa v51, v64, v93 dst_sel:DWORD dst_unused:UNUSED_PAD src0_sel:WORD_1 src1_sel:DWORD
	v_add3_u32 v49, v49, v52, s51
	v_add3_u32 v48, v48, v53, s51
	v_add3_u32 v51, v64, v51, s51
	v_add3_u32 v50, v65, v50, s51
	v_and_b32_e32 v49, 0xffff0000, v49
	v_and_b32_e32 v48, 0xffff0000, v48
	v_or_b32_sdwa v49, v49, v50 dst_sel:DWORD dst_unused:UNUSED_PAD src0_sel:DWORD src1_sel:WORD_1
	v_or_b32_sdwa v48, v48, v51 dst_sel:DWORD dst_unused:UNUSED_PAD src0_sel:DWORD src1_sel:WORD_1
	global_store_dwordx2 v[98:99], v[48:49], off offset:1536
	global_load_dwordx4 v[48:51], v[82:83], off
	s_nop 0
	global_load_dwordx4 v[52:55], v80, s[10:11]
	global_load_dwordx4 v[56:59], v80, s[12:13]
	v_mov_b32_e32 v60, v44
	v_mov_b32_e32 v61, v46
	v_pk_mul_f32 v[60:61], v[60:61], v[100:101] op_sel_hi:[1,0]
	v_mov_b32_e32 v46, v45
	v_pk_mul_f32 v[44:45], v[46:47], v[100:101] op_sel_hi:[1,0]
	s_waitcnt vmcnt(2)
	v_mov_b32_e32 v62, v48
	v_mov_b32_e32 v63, v50
	v_pk_mul_f32 v[60:61], v[60:61], v[62:63]
	s_waitcnt vmcnt(1)
	v_mov_b32_e32 v63, v54
	v_mov_b32_e32 v50, v49
	v_mov_b32_e32 v54, v53
	v_mov_b32_e32 v62, v52
	s_waitcnt vmcnt(0)
	v_mov_b32_e32 v65, v58
	v_pk_mul_f32 v[44:45], v[44:45], v[50:51]
	v_pk_add_f32 v[46:47], v[54:55], 1.0 op_sel_hi:[1,0]
	v_mov_b32_e32 v58, v57
	v_pk_add_f32 v[62:63], v[62:63], 1.0 op_sel_hi:[1,0]
	v_mov_b32_e32 v64, v56
	v_pk_fma_f32 v[44:45], v[44:45], v[46:47], v[58:59]
	v_pk_fma_f32 v[60:61], v[60:61], v[62:63], v[64:65]
	v_and_b32_sdwa v48, v45, v93 dst_sel:DWORD dst_unused:UNUSED_PAD src0_sel:WORD_1 src1_sel:DWORD
	v_and_b32_sdwa v49, v44, v93 dst_sel:DWORD dst_unused:UNUSED_PAD src0_sel:WORD_1 src1_sel:DWORD
	v_and_b32_sdwa v46, v61, v93 dst_sel:DWORD dst_unused:UNUSED_PAD src0_sel:WORD_1 src1_sel:DWORD
	v_and_b32_sdwa v47, v60, v93 dst_sel:DWORD dst_unused:UNUSED_PAD src0_sel:WORD_1 src1_sel:DWORD
	v_add3_u32 v45, v45, v48, s51
	v_add3_u32 v44, v44, v49, s51
	v_add3_u32 v47, v60, v47, s51
	v_add3_u32 v46, v61, v46, s51
	v_and_b32_e32 v45, 0xffff0000, v45
	v_and_b32_e32 v44, 0xffff0000, v44
	v_or_b32_sdwa v45, v45, v46 dst_sel:DWORD dst_unused:UNUSED_PAD src0_sel:DWORD src1_sel:WORD_1
	v_or_b32_sdwa v44, v44, v47 dst_sel:DWORD dst_unused:UNUSED_PAD src0_sel:DWORD src1_sel:WORD_1
	global_store_dwordx2 v[98:99], v[44:45], off offset:2048
	global_load_dwordx4 v[44:47], v[86:87], off
	s_nop 0
	global_load_dwordx4 v[48:51], v84, s[10:11]
	global_load_dwordx4 v[52:55], v84, s[12:13]
	v_mov_b32_e32 v56, v40
	v_mov_b32_e32 v57, v42
	v_pk_mul_f32 v[56:57], v[56:57], v[100:101] op_sel_hi:[1,0]
	v_mov_b32_e32 v42, v41
	v_pk_mul_f32 v[40:41], v[42:43], v[100:101] op_sel_hi:[1,0]
	s_waitcnt vmcnt(2)
	v_mov_b32_e32 v58, v44
	v_mov_b32_e32 v59, v46
	v_pk_mul_f32 v[56:57], v[56:57], v[58:59]
	s_waitcnt vmcnt(1)
	v_mov_b32_e32 v59, v50
	v_mov_b32_e32 v46, v45
	v_mov_b32_e32 v50, v49
	v_mov_b32_e32 v58, v48
	s_waitcnt vmcnt(0)
	v_mov_b32_e32 v61, v54
	v_pk_mul_f32 v[40:41], v[40:41], v[46:47]
	v_pk_add_f32 v[42:43], v[50:51], 1.0 op_sel_hi:[1,0]
	v_mov_b32_e32 v54, v53
	v_pk_add_f32 v[58:59], v[58:59], 1.0 op_sel_hi:[1,0]
	v_mov_b32_e32 v60, v52
	v_pk_fma_f32 v[40:41], v[40:41], v[42:43], v[54:55]
	v_pk_fma_f32 v[56:57], v[56:57], v[58:59], v[60:61]
	v_and_b32_sdwa v44, v41, v93 dst_sel:DWORD dst_unused:UNUSED_PAD src0_sel:WORD_1 src1_sel:DWORD
	v_and_b32_sdwa v45, v40, v93 dst_sel:DWORD dst_unused:UNUSED_PAD src0_sel:WORD_1 src1_sel:DWORD
	v_and_b32_sdwa v42, v57, v93 dst_sel:DWORD dst_unused:UNUSED_PAD src0_sel:WORD_1 src1_sel:DWORD
	v_and_b32_sdwa v43, v56, v93 dst_sel:DWORD dst_unused:UNUSED_PAD src0_sel:WORD_1 src1_sel:DWORD
	v_add3_u32 v41, v41, v44, s51
	v_add3_u32 v40, v40, v45, s51
	v_add3_u32 v43, v56, v43, s51
	v_add3_u32 v42, v57, v42, s51
	v_and_b32_e32 v41, 0xffff0000, v41
	v_and_b32_e32 v40, 0xffff0000, v40
	v_or_b32_sdwa v41, v41, v42 dst_sel:DWORD dst_unused:UNUSED_PAD src0_sel:DWORD src1_sel:WORD_1
	v_or_b32_sdwa v40, v40, v43 dst_sel:DWORD dst_unused:UNUSED_PAD src0_sel:DWORD src1_sel:WORD_1
	global_store_dwordx2 v[98:99], v[40:41], off offset:2560
	global_load_dwordx4 v[40:43], v[90:91], off
	s_nop 0
	global_load_dwordx4 v[44:47], v88, s[10:11]
	global_load_dwordx4 v[48:51], v88, s[12:13]
	v_mov_b32_e32 v52, v4
	v_mov_b32_e32 v53, v6
	v_pk_mul_f32 v[52:53], v[52:53], v[100:101] op_sel_hi:[1,0]
	v_mov_b32_e32 v6, v5
	v_pk_mul_f32 v[4:5], v[6:7], v[100:101] op_sel_hi:[1,0]
	v_mov_b64_e32 v[62:63], v[22:23]
	v_mov_b64_e32 v[60:61], v[20:21]
	s_waitcnt vmcnt(2)
	v_mov_b32_e32 v54, v40
	v_mov_b32_e32 v55, v42
	v_pk_mul_f32 v[52:53], v[52:53], v[54:55]
	s_waitcnt vmcnt(1)
	v_mov_b32_e32 v55, v46
	v_mov_b32_e32 v42, v41
	v_mov_b32_e32 v46, v45
	v_mov_b32_e32 v54, v44
	s_waitcnt vmcnt(0)
	v_mov_b32_e32 v57, v50
	v_pk_mul_f32 v[4:5], v[4:5], v[42:43]
	v_pk_add_f32 v[6:7], v[46:47], 1.0 op_sel_hi:[1,0]
	v_mov_b32_e32 v50, v49
	v_pk_add_f32 v[54:55], v[54:55], 1.0 op_sel_hi:[1,0]
	v_mov_b32_e32 v56, v48
	v_pk_fma_f32 v[4:5], v[4:5], v[6:7], v[50:51]
	v_pk_fma_f32 v[52:53], v[52:53], v[54:55], v[56:57]
	v_and_b32_sdwa v40, v5, v93 dst_sel:DWORD dst_unused:UNUSED_PAD src0_sel:WORD_1 src1_sel:DWORD
	v_and_b32_sdwa v41, v4, v93 dst_sel:DWORD dst_unused:UNUSED_PAD src0_sel:WORD_1 src1_sel:DWORD
	v_and_b32_sdwa v6, v53, v93 dst_sel:DWORD dst_unused:UNUSED_PAD src0_sel:WORD_1 src1_sel:DWORD
	v_and_b32_sdwa v7, v52, v93 dst_sel:DWORD dst_unused:UNUSED_PAD src0_sel:WORD_1 src1_sel:DWORD
	v_add3_u32 v5, v5, v40, s51
	v_add3_u32 v4, v4, v41, s51
	v_add3_u32 v7, v52, v7, s51
	v_add3_u32 v6, v53, v6, s51
	v_and_b32_e32 v5, 0xffff0000, v5
	v_and_b32_e32 v4, 0xffff0000, v4
	v_or_b32_sdwa v5, v5, v6 dst_sel:DWORD dst_unused:UNUSED_PAD src0_sel:DWORD src1_sel:WORD_1
	v_or_b32_sdwa v4, v4, v7 dst_sel:DWORD dst_unused:UNUSED_PAD src0_sel:DWORD src1_sel:WORD_1
	global_store_dwordx2 v[98:99], v[4:5], off offset:3072
	global_load_dwordx4 v[4:7], v[94:95], off
	s_nop 0
	global_load_dwordx4 v[40:43], v92, s[10:11]
	global_load_dwordx4 v[44:47], v92, s[12:13]
	v_mov_b32_e32 v48, v0
	v_mov_b32_e32 v49, v2
	v_pk_mul_f32 v[48:49], v[48:49], v[100:101] op_sel_hi:[1,0]
	v_mov_b32_e32 v2, v1
	v_pk_mul_f32 v[0:1], v[2:3], v[100:101] op_sel_hi:[1,0]
	v_readlane_b32 s10, v255, 40
	v_readlane_b32 s11, v255, 41
	v_mov_b64_e32 v[58:59], v[18:19]
	v_mov_b64_e32 v[56:57], v[16:17]
	s_waitcnt vmcnt(2)
	v_mov_b32_e32 v50, v4
	v_mov_b32_e32 v51, v6
	v_pk_mul_f32 v[48:49], v[48:49], v[50:51]
	s_waitcnt vmcnt(1)
	v_mov_b32_e32 v51, v42
	v_mov_b32_e32 v6, v5
	v_mov_b32_e32 v42, v41
	v_mov_b32_e32 v50, v40
	s_waitcnt vmcnt(0)
	v_mov_b32_e32 v53, v46
	v_pk_mul_f32 v[0:1], v[0:1], v[6:7]
	v_pk_add_f32 v[2:3], v[42:43], 1.0 op_sel_hi:[1,0]
	v_mov_b32_e32 v46, v45
	v_pk_add_f32 v[50:51], v[50:51], 1.0 op_sel_hi:[1,0]
	v_mov_b32_e32 v52, v44
	v_pk_fma_f32 v[0:1], v[0:1], v[2:3], v[46:47]
	v_pk_fma_f32 v[48:49], v[48:49], v[50:51], v[52:53]
	v_and_b32_sdwa v4, v1, v93 dst_sel:DWORD dst_unused:UNUSED_PAD src0_sel:WORD_1 src1_sel:DWORD
	v_and_b32_sdwa v5, v0, v93 dst_sel:DWORD dst_unused:UNUSED_PAD src0_sel:WORD_1 src1_sel:DWORD
	v_and_b32_sdwa v2, v49, v93 dst_sel:DWORD dst_unused:UNUSED_PAD src0_sel:WORD_1 src1_sel:DWORD
	v_and_b32_sdwa v3, v48, v93 dst_sel:DWORD dst_unused:UNUSED_PAD src0_sel:WORD_1 src1_sel:DWORD
	v_add3_u32 v1, v1, v4, s51
	v_add3_u32 v0, v0, v5, s51
	v_add3_u32 v3, v48, v3, s51
	v_add3_u32 v2, v49, v2, s51
	v_and_b32_e32 v1, 0xffff0000, v1
	v_and_b32_e32 v0, 0xffff0000, v0
	v_or_b32_sdwa v1, v1, v2 dst_sel:DWORD dst_unused:UNUSED_PAD src0_sel:DWORD src1_sel:WORD_1
	v_or_b32_sdwa v0, v0, v3 dst_sel:DWORD dst_unused:UNUSED_PAD src0_sel:DWORD src1_sel:WORD_1
	global_store_dwordx2 v[98:99], v[0:1], off offset:3584
	v_mov_b64_e32 v[0:1], v[24:25]
	v_mov_b64_e32 v[4:5], v[28:29]
	v_mov_b64_e32 v[42:43], v[34:35]
	v_mov_b64_e32 v[46:47], v[38:39]
	v_mov_b64_e32 v[50:51], v[10:11]
	v_mov_b64_e32 v[54:55], v[14:15]
	v_lshl_add_u64 v[98:99], v[98:99], 0, s[10:11]
	v_mov_b64_e32 v[2:3], v[26:27]
	v_mov_b64_e32 v[6:7], v[30:31]
	v_mov_b64_e32 v[40:41], v[32:33]
	v_mov_b64_e32 v[44:45], v[36:37]
	v_mov_b64_e32 v[48:49], v[8:9]
	v_mov_b64_e32 v[52:53], v[12:13]
	s_mov_b32 s10, s4
	s_cbranch_vccnz .LBB0_1537

.LBB0_1547:
	v_mul_f32_e32 v64, v61, v61
	v_mul_f32_e32 v65, v57, v57
	v_fmac_f32_e32 v64, v60, v60
	v_fmac_f32_e32 v65, v56, v56
	v_fmac_f32_e32 v64, v62, v62
	v_fmac_f32_e32 v65, v58, v58
	v_fmac_f32_e32 v64, v63, v63
	v_fmac_f32_e32 v65, v59, v59
	v_add_f32_e32 v64, v64, v65
	v_mul_f32_e32 v65, v53, v53
	v_fmac_f32_e32 v65, v52, v52
	v_fmac_f32_e32 v65, v54, v54
	v_fmac_f32_e32 v65, v55, v55
	v_add_f32_e32 v64, v64, v65
	v_mul_f32_e32 v65, v49, v49
	v_fmac_f32_e32 v65, v48, v48
	v_fmac_f32_e32 v65, v50, v50
	v_fmac_f32_e32 v65, v51, v51
	v_add_f32_e32 v64, v64, v65
	v_mul_f32_e32 v65, v45, v45
	v_fmac_f32_e32 v65, v44, v44
	v_fmac_f32_e32 v65, v46, v46
	v_fmac_f32_e32 v65, v47, v47
	v_add_f32_e32 v64, v64, v65
	v_mul_f32_e32 v65, v41, v41
	v_fmac_f32_e32 v65, v40, v40
	v_fmac_f32_e32 v65, v42, v42
	v_fmac_f32_e32 v65, v43, v43
	v_add_f32_e32 v64, v64, v65
	v_mul_f32_e32 v65, v37, v37
	v_fmac_f32_e32 v65, v36, v36
	v_fmac_f32_e32 v65, v38, v38
	v_fmac_f32_e32 v65, v39, v39
	v_add_f32_e32 v64, v64, v65
	v_mul_f32_e32 v65, v33, v33
	v_fmac_f32_e32 v65, v32, v32
	v_fmac_f32_e32 v65, v34, v34
	v_fmac_f32_e32 v65, v35, v35
	v_add_f32_e32 v64, v64, v65
	s_min_i32 s6, s6, 0x2000
	s_ashr_i32 s6, s6, 11
	s_mul_hi_i32 s7, s6, 0xc000
	s_mul_i32 s6, s6, 0xc000
	s_waitcnt lgkmcnt(0)
	s_nop 1
	v_add_f32_dpp v64, v64, v64 quad_perm:[1,0,3,2] row_mask:0xf bank_mask:0xf
	s_add_u32 s8, s55, s6
	s_addc_u32 s9, s69, s7
	s_add_u32 s6, s8, 0x8000
	s_addc_u32 s7, s9, 0
	s_waitcnt lgkmcnt(0)
	s_nop 1
	v_add_f32_dpp v64, v64, v64 quad_perm:[2,3,0,1] row_mask:0xf bank_mask:0xf
	s_add_u32 s8, s8, 0x6000
	s_addc_u32 s9, s9, 0
	s_waitcnt lgkmcnt(0)
	s_nop 1
	v_add_f32_dpp v64, v64, v64 row_half_mirror row_mask:0xf bank_mask:0xf
	s_waitcnt lgkmcnt(0)
	s_nop 1
	v_add_f32_dpp v64, v64, v64 row_mirror row_mask:0xf bank_mask:0xf
	v_mov_b32_e32 v65, v64
	s_waitcnt lgkmcnt(0)
	s_nop 1
	v_permlane16_swap_b32_e32 v64, v65
	v_add_f32_e32 v64, v64, v65
	v_mov_b32_e32 v65, v64
	s_nop 1
	v_permlane32_swap_b32_e32 v64, v65
	v_add_f32_e32 v64, v64, v65
	v_mov_b32_e32 v65, 0x358637bd
	v_fmamk_f32 v64, v64, 0x3a000000, v65
	v_cmp_gt_f32_e32 vcc, s33, v64
	v_mul_f32_e32 v65, 0x4b800000, v64
	s_nop 0
	v_cndmask_b32_e32 v64, v64, v65, vcc
	v_rsq_f32_e32 v64, v64
	s_nop 0
	v_mul_f32_e32 v65, 0x45800000, v64
	v_cndmask_b32_e32 v85, v64, v65, vcc
	global_load_dwordx4 v[104:107], v[68:69], off
	global_load_dwordx4 v[108:111], v96, s[6:7]
	global_load_dwordx4 v[64:67], v96, s[8:9]
	v_mul_f32_e32 v60, v60, v85
	v_mul_f32_e32 v61, v61, v85
	v_mul_f32_e32 v56, v56, v85
	v_mul_f32_e32 v52, v52, v85
	v_mul_f32_e32 v48, v48, v85
	v_mul_f32_e32 v44, v44, v85
	v_mul_f32_e32 v40, v40, v85
	v_mul_f32_e32 v36, v36, v85
	v_mul_f32_e32 v32, v32, v85
	s_waitcnt vmcnt(2)
	v_mul_f32_e32 v60, v104, v60
	s_waitcnt vmcnt(1)
	v_add_f32_e32 v81, 1.0, v108
	s_waitcnt vmcnt(0)
	v_fma_f32 v60, v81, v60, v64
	v_mul_f32_e32 v61, v105, v61
	v_add_f32_e32 v64, 1.0, v109
	v_fma_f32 v89, v64, v61, v65
	v_mul_f32_e32 v61, v62, v85
	v_mul_f32_e32 v61, v106, v61
	v_add_f32_e32 v62, 1.0, v110
	v_fma_f32 v93, v62, v61, v66
	v_mul_f32_e32 v61, v63, v85
	v_mul_f32_e32 v61, v107, v61
	v_add_f32_e32 v62, 1.0, v111
	v_fmac_f32_e32 v67, v62, v61
	v_mov_b32_e32 v61, v97
	v_cvt_pk_fp8_f32 v61, v60, v89
	v_lshl_add_u32 v81, v75, 2, v71
	v_cvt_pk_fp8_f32 v61, v93, v67 op_sel:[0,0,1]
	global_store_dword v[102:103], v61, off
	ds_read_b128 v[104:107], v81
	ds_read_b128 v[108:111], v81 offset:16
	s_waitcnt lgkmcnt(1)
	v_fma_f32 v75, v104, v60, 0
	s_waitcnt lgkmcnt(0)
	v_fma_f32 v63, v108, v60, 0
	v_fma_f32 v66, v105, v60, 0
	v_fma_f32 v62, v109, v60, 0
	v_fma_f32 v65, v106, v60, 0
	v_fma_f32 v61, v110, v60, 0
	v_fma_f32 v64, v107, v60, 0
	v_fma_f32 v60, v111, v60, 0
	ds_read_b128 v[104:107], v81 offset:2048
	ds_read_b128 v[108:111], v81 offset:2064
	s_waitcnt lgkmcnt(1)
	v_fmac_f32_e32 v75, v104, v89
	s_waitcnt lgkmcnt(0)
	v_fmac_f32_e32 v63, v108, v89
	v_fmac_f32_e32 v66, v105, v89
	v_fmac_f32_e32 v62, v109, v89
	v_fmac_f32_e32 v65, v106, v89
	v_fmac_f32_e32 v61, v110, v89
	v_fmac_f32_e32 v64, v107, v89
	v_fmac_f32_e32 v60, v111, v89
	ds_read_b128 v[104:107], v81 offset:4096
	ds_read_b128 v[108:111], v81 offset:4112
	s_waitcnt lgkmcnt(1)
	v_fmac_f32_e32 v75, v104, v93
	s_waitcnt lgkmcnt(0)
	v_fmac_f32_e32 v63, v108, v93
	v_fmac_f32_e32 v66, v105, v93
	v_fmac_f32_e32 v62, v109, v93
	v_fmac_f32_e32 v65, v106, v93
	v_fmac_f32_e32 v61, v110, v93
	v_fmac_f32_e32 v64, v107, v93
	v_fmac_f32_e32 v60, v111, v93
	ds_read_b128 v[104:107], v81 offset:6144
	ds_read_b128 v[108:111], v81 offset:6160
	s_waitcnt lgkmcnt(1)
	v_fmac_f32_e32 v75, v67, v104
	s_waitcnt lgkmcnt(0)
	v_fmac_f32_e32 v63, v67, v108
	v_fmac_f32_e32 v66, v67, v105
	v_fmac_f32_e32 v62, v67, v109
	v_fmac_f32_e32 v65, v67, v106
	v_fmac_f32_e32 v61, v67, v110
	v_fmac_f32_e32 v64, v67, v107
	v_fmac_f32_e32 v60, v67, v111
	global_load_dwordx4 v[104:107], v[72:73], off
	global_load_dwordx4 v[108:111], v70, s[6:7]
	global_load_dwordx4 v[112:115], v70, s[8:9]
	s_waitcnt vmcnt(2)
	v_mul_f32_e32 v56, v56, v104
	s_waitcnt vmcnt(1)
	v_add_f32_e32 v67, 1.0, v108
	s_waitcnt vmcnt(0)
	v_fma_f32 v67, v56, v67, v112
	v_mul_f32_e32 v56, v57, v85
	v_mul_f32_e32 v56, v56, v105
	v_add_f32_e32 v57, 1.0, v109
	v_fma_f32 v89, v56, v57, v113
	v_mul_f32_e32 v56, v58, v85
	v_mul_f32_e32 v56, v56, v106
	v_add_f32_e32 v57, 1.0, v110
	v_fma_f32 v93, v56, v57, v114
	v_mul_f32_e32 v56, v59, v85
	v_mul_f32_e32 v56, v56, v107
	v_add_f32_e32 v57, 1.0, v111
	v_fmac_f32_e32 v115, v56, v57
	v_mov_b32_e32 v56, v97
	v_cvt_pk_fp8_f32 v56, v67, v89
	v_cvt_pk_fp8_f32 v56, v93, v115 op_sel:[0,0,1]
	global_store_dword v[102:103], v56, off offset:256
	ds_read_b128 v[56:59], v81 offset:8192
	ds_read_b128 v[104:107], v81 offset:8208
	s_waitcnt lgkmcnt(1)
	v_fmac_f32_e32 v75, v67, v56
	s_waitcnt lgkmcnt(0)
	v_fmac_f32_e32 v63, v67, v104
	v_fmac_f32_e32 v66, v67, v57
	v_fmac_f32_e32 v62, v67, v105
	v_fmac_f32_e32 v65, v67, v58
	v_fmac_f32_e32 v61, v67, v106
	v_fmac_f32_e32 v64, v67, v59
	v_fmac_f32_e32 v60, v67, v107
	ds_read_b128 v[56:59], v81 offset:10240
	ds_read_b128 v[104:107], v81 offset:10256
	s_waitcnt lgkmcnt(1)
	v_fmac_f32_e32 v75, v89, v56
	s_waitcnt lgkmcnt(0)
	v_fmac_f32_e32 v63, v89, v104
	v_fmac_f32_e32 v66, v89, v57
	v_fmac_f32_e32 v62, v89, v105
	v_fmac_f32_e32 v65, v89, v58
	v_fmac_f32_e32 v61, v89, v106
	v_fmac_f32_e32 v64, v89, v59
	v_fmac_f32_e32 v60, v89, v107
	ds_read_b128 v[56:59], v81 offset:12288
	ds_read_b128 v[104:107], v81 offset:12304
	s_waitcnt lgkmcnt(1)
	v_fmac_f32_e32 v75, v93, v56
	s_waitcnt lgkmcnt(0)
	v_fmac_f32_e32 v63, v93, v104
	v_fmac_f32_e32 v66, v93, v57
	v_fmac_f32_e32 v62, v93, v105
	v_fmac_f32_e32 v65, v93, v58
	v_fmac_f32_e32 v61, v93, v106
	v_fmac_f32_e32 v64, v93, v59
	v_fmac_f32_e32 v60, v93, v107
	ds_read_b128 v[56:59], v81 offset:14336
	ds_read_b128 v[104:107], v81 offset:14352
	s_waitcnt lgkmcnt(1)
	v_fmac_f32_e32 v75, v115, v56
	s_waitcnt lgkmcnt(0)
	v_fmac_f32_e32 v63, v115, v104
	v_fmac_f32_e32 v66, v115, v57
	v_fmac_f32_e32 v62, v115, v105
	v_fmac_f32_e32 v65, v115, v58
	v_fmac_f32_e32 v61, v115, v106
	v_fmac_f32_e32 v64, v115, v59
	v_fmac_f32_e32 v60, v115, v107
	global_load_dwordx4 v[56:59], v[78:79], off
	global_load_dwordx4 v[104:107], v74, s[6:7]
	global_load_dwordx4 v[108:111], v74, s[8:9]
	s_waitcnt vmcnt(2)
	v_mul_f32_e32 v52, v52, v56
	s_waitcnt vmcnt(1)
	v_add_f32_e32 v56, 1.0, v104
	s_waitcnt vmcnt(0)
	v_fma_f32 v67, v52, v56, v108
	v_mul_f32_e32 v52, v53, v85
	v_mul_f32_e32 v52, v52, v57
	v_add_f32_e32 v53, 1.0, v105
	v_fma_f32 v89, v52, v53, v109
	v_mul_f32_e32 v52, v54, v85
	v_mul_f32_e32 v52, v52, v58
	v_add_f32_e32 v53, 1.0, v106
	v_fma_f32 v93, v52, v53, v110
	v_mul_f32_e32 v52, v55, v85
	v_mul_f32_e32 v52, v52, v59
	v_add_f32_e32 v53, 1.0, v107
	v_fmac_f32_e32 v111, v52, v53
	v_mov_b32_e32 v52, v97
	v_cvt_pk_fp8_f32 v52, v67, v89
	v_cvt_pk_fp8_f32 v52, v93, v111 op_sel:[0,0,1]
	global_store_dword v[102:103], v52, off offset:512
	ds_read_b128 v[52:55], v81 offset:16384
	ds_read_b128 v[56:59], v81 offset:16400
	s_waitcnt lgkmcnt(1)
	v_fmac_f32_e32 v75, v67, v52
	s_waitcnt lgkmcnt(0)
	v_fmac_f32_e32 v63, v67, v56
	v_fmac_f32_e32 v66, v67, v53
	v_fmac_f32_e32 v62, v67, v57
	v_fmac_f32_e32 v65, v67, v54
	v_fmac_f32_e32 v61, v67, v58
	v_fmac_f32_e32 v64, v67, v55
	v_fmac_f32_e32 v60, v67, v59
	ds_read_b128 v[52:55], v81 offset:18432
	ds_read_b128 v[56:59], v81 offset:18448
	s_waitcnt lgkmcnt(1)
	v_fmac_f32_e32 v75, v89, v52
	s_waitcnt lgkmcnt(0)
	v_fmac_f32_e32 v63, v89, v56
	v_fmac_f32_e32 v66, v89, v53
	v_fmac_f32_e32 v62, v89, v57
	v_fmac_f32_e32 v65, v89, v54
	v_fmac_f32_e32 v61, v89, v58
	v_fmac_f32_e32 v64, v89, v55
	v_fmac_f32_e32 v60, v89, v59
	ds_read_b128 v[52:55], v81 offset:20480
	ds_read_b128 v[56:59], v81 offset:20496
	s_waitcnt lgkmcnt(1)
	v_fmac_f32_e32 v75, v93, v52
	s_waitcnt lgkmcnt(0)
	v_fmac_f32_e32 v63, v93, v56
	v_fmac_f32_e32 v66, v93, v53
	v_fmac_f32_e32 v62, v93, v57
	v_fmac_f32_e32 v65, v93, v54
	v_fmac_f32_e32 v61, v93, v58
	v_fmac_f32_e32 v64, v93, v55
	v_fmac_f32_e32 v60, v93, v59
	ds_read_b128 v[52:55], v81 offset:22528
	ds_read_b128 v[56:59], v81 offset:22544
	s_waitcnt lgkmcnt(1)
	v_fmac_f32_e32 v75, v111, v52
	s_waitcnt lgkmcnt(0)
	v_fmac_f32_e32 v63, v111, v56
	v_fmac_f32_e32 v66, v111, v53
	v_fmac_f32_e32 v62, v111, v57
	v_fmac_f32_e32 v65, v111, v54
	v_fmac_f32_e32 v61, v111, v58
	v_fmac_f32_e32 v64, v111, v55
	v_fmac_f32_e32 v60, v111, v59
	global_load_dwordx4 v[52:55], v[82:83], off
	global_load_dwordx4 v[56:59], v80, s[6:7]
	global_load_dwordx4 v[104:107], v80, s[8:9]
	s_waitcnt vmcnt(2)
	v_mul_f32_e32 v48, v48, v52
	s_waitcnt vmcnt(1)
	v_add_f32_e32 v52, 1.0, v56
	s_waitcnt vmcnt(0)
	v_fma_f32 v56, v48, v52, v104
	v_mul_f32_e32 v48, v49, v85
	v_mul_f32_e32 v48, v48, v53
	v_add_f32_e32 v49, 1.0, v57
	v_fma_f32 v57, v48, v49, v105
	v_mul_f32_e32 v48, v50, v85
	v_mul_f32_e32 v48, v48, v54
	v_add_f32_e32 v49, 1.0, v58
	v_fma_f32 v58, v48, v49, v106
	v_mul_f32_e32 v48, v51, v85
	v_mul_f32_e32 v48, v48, v55
	v_add_f32_e32 v49, 1.0, v59
	v_fmac_f32_e32 v107, v48, v49
	v_mov_b32_e32 v48, v97
	v_cvt_pk_fp8_f32 v48, v56, v57
	v_cvt_pk_fp8_f32 v48, v58, v107 op_sel:[0,0,1]
	global_store_dword v[102:103], v48, off offset:768
	ds_read_b128 v[48:51], v81 offset:24576
	ds_read_b128 v[52:55], v81 offset:24592
	s_waitcnt lgkmcnt(1)
	v_fmac_f32_e32 v75, v56, v48
	s_waitcnt lgkmcnt(0)
	v_fmac_f32_e32 v63, v56, v52
	v_fmac_f32_e32 v66, v56, v49
	v_fmac_f32_e32 v62, v56, v53
	v_fmac_f32_e32 v65, v56, v50
	v_fmac_f32_e32 v61, v56, v54
	v_fmac_f32_e32 v64, v56, v51
	v_fmac_f32_e32 v60, v56, v55
	ds_read_b128 v[48:51], v81 offset:26624
	ds_read_b128 v[52:55], v81 offset:26640
	s_waitcnt lgkmcnt(1)
	v_fmac_f32_e32 v75, v57, v48
	s_waitcnt lgkmcnt(0)
	v_fmac_f32_e32 v63, v57, v52
	v_fmac_f32_e32 v66, v57, v49
	v_fmac_f32_e32 v62, v57, v53
	v_fmac_f32_e32 v65, v57, v50
	v_fmac_f32_e32 v61, v57, v54
	v_fmac_f32_e32 v64, v57, v51
	v_fmac_f32_e32 v60, v57, v55
	ds_read_b128 v[48:51], v81 offset:28672
	ds_read_b128 v[52:55], v81 offset:28688
	s_waitcnt lgkmcnt(1)
	v_fmac_f32_e32 v75, v58, v48
	s_waitcnt lgkmcnt(0)
	v_fmac_f32_e32 v63, v58, v52
	v_fmac_f32_e32 v66, v58, v49
	v_fmac_f32_e32 v62, v58, v53
	v_fmac_f32_e32 v65, v58, v50
	v_fmac_f32_e32 v61, v58, v54
	v_fmac_f32_e32 v64, v58, v51
	v_fmac_f32_e32 v60, v58, v55
	ds_read_b128 v[48:51], v81 offset:30720
	ds_read_b128 v[52:55], v81 offset:30736
	s_waitcnt lgkmcnt(1)
	v_fmac_f32_e32 v75, v107, v48
	s_waitcnt lgkmcnt(0)
	v_fmac_f32_e32 v63, v107, v52
	v_fmac_f32_e32 v66, v107, v49
	v_fmac_f32_e32 v62, v107, v53
	v_fmac_f32_e32 v65, v107, v50
	v_fmac_f32_e32 v61, v107, v54
	v_fmac_f32_e32 v64, v107, v51
	v_fmac_f32_e32 v60, v107, v55
	global_load_dwordx4 v[48:51], v[86:87], off
	global_load_dwordx4 v[52:55], v84, s[6:7]
	global_load_dwordx4 v[56:59], v84, s[8:9]
	s_waitcnt vmcnt(2)
	v_mul_f32_e32 v44, v44, v48
	s_waitcnt vmcnt(1)
	v_add_f32_e32 v48, 1.0, v52
	s_waitcnt vmcnt(0)
	v_fma_f32 v52, v44, v48, v56
	v_mul_f32_e32 v44, v45, v85
	v_mul_f32_e32 v44, v44, v49
	v_add_f32_e32 v45, 1.0, v53
	v_fma_f32 v53, v44, v45, v57
	v_mul_f32_e32 v44, v46, v85
	v_mul_f32_e32 v44, v44, v50
	v_add_f32_e32 v45, 1.0, v54
	v_fma_f32 v54, v44, v45, v58
	v_mul_f32_e32 v44, v47, v85
	v_mul_f32_e32 v44, v44, v51
	v_add_f32_e32 v45, 1.0, v55
	v_fmac_f32_e32 v59, v44, v45
	v_mov_b32_e32 v44, v97
	v_cvt_pk_fp8_f32 v44, v52, v53
	v_cvt_pk_fp8_f32 v44, v54, v59 op_sel:[0,0,1]
	global_store_dword v[102:103], v44, off offset:1024
	ds_read_b128 v[44:47], v81 offset:32768
	ds_read_b128 v[48:51], v81 offset:32784
	s_waitcnt lgkmcnt(1)
	v_fmac_f32_e32 v75, v52, v44
	s_waitcnt lgkmcnt(0)
	v_fmac_f32_e32 v63, v52, v48
	v_fmac_f32_e32 v66, v52, v45
	v_fmac_f32_e32 v62, v52, v49
	v_fmac_f32_e32 v65, v52, v46
	v_fmac_f32_e32 v61, v52, v50
	v_fmac_f32_e32 v64, v52, v47
	v_fmac_f32_e32 v60, v52, v51
	ds_read_b128 v[44:47], v81 offset:34816
	ds_read_b128 v[48:51], v81 offset:34832
	s_waitcnt lgkmcnt(1)
	v_fmac_f32_e32 v75, v53, v44
	s_waitcnt lgkmcnt(0)
	v_fmac_f32_e32 v63, v53, v48
	v_fmac_f32_e32 v66, v53, v45
	v_fmac_f32_e32 v62, v53, v49
	v_fmac_f32_e32 v65, v53, v46
	v_fmac_f32_e32 v61, v53, v50
	v_fmac_f32_e32 v64, v53, v47
	v_fmac_f32_e32 v60, v53, v51
	ds_read_b128 v[44:47], v81 offset:36864
	ds_read_b128 v[48:51], v81 offset:36880
	s_waitcnt lgkmcnt(1)
	v_fmac_f32_e32 v75, v54, v44
	s_waitcnt lgkmcnt(0)
	v_fmac_f32_e32 v63, v54, v48
	v_fmac_f32_e32 v66, v54, v45
	v_fmac_f32_e32 v62, v54, v49
	v_fmac_f32_e32 v65, v54, v46
	v_fmac_f32_e32 v61, v54, v50
	v_fmac_f32_e32 v64, v54, v47
	v_fmac_f32_e32 v60, v54, v51
	ds_read_b128 v[44:47], v81 offset:38912
	ds_read_b128 v[48:51], v81 offset:38928
	s_waitcnt lgkmcnt(1)
	v_fmac_f32_e32 v75, v59, v44
	s_waitcnt lgkmcnt(0)
	v_fmac_f32_e32 v63, v59, v48
	v_fmac_f32_e32 v66, v59, v45
	v_fmac_f32_e32 v62, v59, v49
	v_fmac_f32_e32 v65, v59, v46
	v_fmac_f32_e32 v61, v59, v50
	v_fmac_f32_e32 v64, v59, v47
	v_fmac_f32_e32 v60, v59, v51
	global_load_dwordx4 v[48:51], v[90:91], off
	global_load_dwordx4 v[52:55], v88, s[6:7]
	global_load_dwordx4 v[44:47], v88, s[8:9]
	s_waitcnt vmcnt(2)
	v_mul_f32_e32 v40, v40, v48
	s_waitcnt vmcnt(1)
	v_add_f32_e32 v48, 1.0, v52
	s_waitcnt vmcnt(0)
	v_fma_f32 v44, v40, v48, v44
	v_mul_f32_e32 v40, v41, v85
	v_mul_f32_e32 v40, v40, v49
	v_add_f32_e32 v41, 1.0, v53
	v_fma_f32 v45, v40, v41, v45
	v_mul_f32_e32 v40, v42, v85
	v_mul_f32_e32 v40, v40, v50
	v_add_f32_e32 v41, 1.0, v54
	v_fma_f32 v46, v40, v41, v46
	v_mul_f32_e32 v40, v43, v85
	v_mul_f32_e32 v40, v40, v51
	v_add_f32_e32 v41, 1.0, v55
	v_fmac_f32_e32 v47, v40, v41
	v_mov_b32_e32 v40, v97
	v_cvt_pk_fp8_f32 v40, v44, v45
	v_cvt_pk_fp8_f32 v40, v46, v47 op_sel:[0,0,1]
	global_store_dword v[102:103], v40, off offset:1280
	ds_read_b128 v[40:43], v81 offset:40960
	ds_read_b128 v[48:51], v81 offset:40976
	s_waitcnt lgkmcnt(1)
	v_fmac_f32_e32 v75, v44, v40
	s_waitcnt lgkmcnt(0)
	v_fmac_f32_e32 v63, v44, v48
	v_fmac_f32_e32 v66, v44, v41
	v_fmac_f32_e32 v62, v44, v49
	v_fmac_f32_e32 v65, v44, v42
	v_fmac_f32_e32 v61, v44, v50
	v_fmac_f32_e32 v64, v44, v43
	v_fmac_f32_e32 v60, v44, v51
	ds_read_b128 v[40:43], v81 offset:43008
	ds_read_b128 v[48:51], v81 offset:43024
	s_waitcnt lgkmcnt(1)
	v_fmac_f32_e32 v75, v45, v40
	s_waitcnt lgkmcnt(0)
	v_fmac_f32_e32 v63, v45, v48
	v_fmac_f32_e32 v66, v45, v41
	v_fmac_f32_e32 v62, v45, v49
	v_fmac_f32_e32 v65, v45, v42
	v_fmac_f32_e32 v61, v45, v50
	v_fmac_f32_e32 v64, v45, v43
	v_fmac_f32_e32 v60, v45, v51
	ds_read_b128 v[40:43], v81 offset:45056
	ds_read_b128 v[48:51], v81 offset:45072
	s_waitcnt lgkmcnt(1)
	v_fmac_f32_e32 v75, v46, v40
	s_waitcnt lgkmcnt(0)
	v_fmac_f32_e32 v63, v46, v48
	v_fmac_f32_e32 v66, v46, v41
	v_fmac_f32_e32 v62, v46, v49
	v_fmac_f32_e32 v65, v46, v42
	v_fmac_f32_e32 v61, v46, v50
	v_fmac_f32_e32 v64, v46, v43
	v_fmac_f32_e32 v60, v46, v51
	ds_read_b128 v[40:43], v81 offset:47104
	ds_read_b128 v[48:51], v81 offset:47120
	s_waitcnt lgkmcnt(1)
	v_fmac_f32_e32 v75, v47, v40
	s_waitcnt lgkmcnt(0)
	v_fmac_f32_e32 v63, v47, v48
	v_fmac_f32_e32 v66, v47, v41
	v_fmac_f32_e32 v62, v47, v49
	v_fmac_f32_e32 v65, v47, v42
	v_fmac_f32_e32 v61, v47, v50
	v_fmac_f32_e32 v64, v47, v43
	v_fmac_f32_e32 v60, v47, v51
	global_load_dwordx4 v[44:47], v[94:95], off
	global_load_dwordx4 v[48:51], v92, s[6:7]
	global_load_dwordx4 v[40:43], v92, s[8:9]
	s_waitcnt vmcnt(2)
	v_mul_f32_e32 v36, v36, v44
	s_waitcnt vmcnt(1)
	v_add_f32_e32 v44, 1.0, v48
	s_waitcnt vmcnt(0)
	v_fma_f32 v40, v36, v44, v40
	v_mul_f32_e32 v36, v37, v85
	v_mul_f32_e32 v36, v36, v45
	v_add_f32_e32 v37, 1.0, v49
	v_fma_f32 v41, v36, v37, v41
	v_mul_f32_e32 v36, v38, v85
	v_mul_f32_e32 v36, v36, v46
	v_add_f32_e32 v37, 1.0, v50
	v_fma_f32 v42, v36, v37, v42
	v_mul_f32_e32 v36, v39, v85
	v_mul_f32_e32 v36, v36, v47
	v_add_f32_e32 v37, 1.0, v51
	v_fmac_f32_e32 v43, v36, v37
	v_mov_b32_e32 v36, v97
	v_cvt_pk_fp8_f32 v36, v40, v41
	v_cvt_pk_fp8_f32 v36, v42, v43 op_sel:[0,0,1]
	global_store_dword v[102:103], v36, off offset:1536
	ds_read_b128 v[36:39], v81 offset:49152
	ds_read_b128 v[44:47], v81 offset:49168
	s_waitcnt lgkmcnt(1)
	v_fmac_f32_e32 v75, v40, v36
	s_waitcnt lgkmcnt(0)
	v_fmac_f32_e32 v63, v40, v44
	v_fmac_f32_e32 v66, v40, v37
	v_fmac_f32_e32 v62, v40, v45
	v_fmac_f32_e32 v65, v40, v38
	v_fmac_f32_e32 v61, v40, v46
	v_fmac_f32_e32 v64, v40, v39
	v_fmac_f32_e32 v60, v40, v47
	ds_read_b128 v[36:39], v81 offset:51200
	ds_read_b128 v[44:47], v81 offset:51216
	s_waitcnt lgkmcnt(1)
	v_fmac_f32_e32 v75, v41, v36
	s_waitcnt lgkmcnt(0)
	v_fmac_f32_e32 v63, v41, v44
	v_fmac_f32_e32 v66, v41, v37
	v_fmac_f32_e32 v62, v41, v45
	v_fmac_f32_e32 v65, v41, v38
	v_fmac_f32_e32 v61, v41, v46
	v_fmac_f32_e32 v64, v41, v39
	v_fmac_f32_e32 v60, v41, v47
	ds_read_b128 v[36:39], v81 offset:53248
	ds_read_b128 v[44:47], v81 offset:53264
	s_waitcnt lgkmcnt(1)
	v_fmac_f32_e32 v75, v42, v36
	s_waitcnt lgkmcnt(0)
	v_fmac_f32_e32 v63, v42, v44
	v_fmac_f32_e32 v66, v42, v37
	v_fmac_f32_e32 v62, v42, v45
	v_fmac_f32_e32 v65, v42, v38
	v_fmac_f32_e32 v61, v42, v46
	v_fmac_f32_e32 v64, v42, v39
	v_fmac_f32_e32 v60, v42, v47
	ds_read_b128 v[36:39], v81 offset:55296
	ds_read_b128 v[44:47], v81 offset:55312
	s_waitcnt lgkmcnt(1)
	v_fmac_f32_e32 v75, v43, v36
	s_waitcnt lgkmcnt(0)
	v_fmac_f32_e32 v63, v43, v44
	v_fmac_f32_e32 v66, v43, v37
	v_fmac_f32_e32 v62, v43, v45
	v_fmac_f32_e32 v65, v43, v38
	v_fmac_f32_e32 v61, v43, v46
	v_fmac_f32_e32 v64, v43, v39
	v_fmac_f32_e32 v60, v43, v47
	global_load_dwordx4 v[40:43], v[100:101], off
	global_load_dwordx4 v[44:47], v98, s[6:7]
	global_load_dwordx4 v[36:39], v98, s[8:9]
	s_waitcnt vmcnt(2)
	v_mul_f32_e32 v32, v32, v40
	s_waitcnt vmcnt(1)
	v_add_f32_e32 v40, 1.0, v44
	s_waitcnt vmcnt(0)
	v_fma_f32 v36, v32, v40, v36
	v_mul_f32_e32 v32, v33, v85
	v_mul_f32_e32 v32, v32, v41
	v_add_f32_e32 v33, 1.0, v45
	v_fma_f32 v33, v32, v33, v37
	v_mul_f32_e32 v32, v34, v85
	v_mul_f32_e32 v32, v32, v42
	v_add_f32_e32 v34, 1.0, v46
	v_fma_f32 v32, v32, v34, v38
	v_mul_f32_e32 v34, v35, v85
	v_mul_f32_e32 v34, v34, v43
	v_add_f32_e32 v35, 1.0, v47
	v_fmac_f32_e32 v39, v34, v35
	v_mov_b32_e32 v34, v97
	v_cvt_pk_fp8_f32 v34, v36, v33
	v_cvt_pk_fp8_f32 v34, v32, v39 op_sel:[0,0,1]
	global_store_dword v[102:103], v34, off offset:1792
	ds_read_b128 v[40:43], v81 offset:57344
	ds_read_b128 v[44:47], v81 offset:57360
	s_waitcnt lgkmcnt(1)
	v_fmac_f32_e32 v75, v36, v40
	s_waitcnt lgkmcnt(0)
	v_fmac_f32_e32 v63, v36, v44
	v_fmac_f32_e32 v66, v36, v41
	v_fmac_f32_e32 v62, v36, v45
	v_fmac_f32_e32 v65, v36, v42
	v_fmac_f32_e32 v61, v36, v46
	v_fmac_f32_e32 v64, v36, v43
	v_fmac_f32_e32 v60, v36, v47
	ds_read_b128 v[34:37], v81 offset:59392
	ds_read_b128 v[40:43], v81 offset:59408
	s_waitcnt lgkmcnt(1)
	v_fmac_f32_e32 v75, v33, v34
	s_waitcnt lgkmcnt(0)
	v_fmac_f32_e32 v63, v33, v40
	v_fmac_f32_e32 v66, v33, v35
	v_fmac_f32_e32 v62, v33, v41
	v_fmac_f32_e32 v65, v33, v36
	v_fmac_f32_e32 v61, v33, v42
	v_fmac_f32_e32 v64, v33, v37
	v_fmac_f32_e32 v60, v33, v43
	ds_read_b128 v[34:37], v81 offset:61440
	ds_read_b128 v[40:43], v81 offset:61456
	s_waitcnt lgkmcnt(1)
	v_fmac_f32_e32 v75, v32, v34
	s_waitcnt lgkmcnt(0)
	v_fmac_f32_e32 v63, v32, v40
	v_fmac_f32_e32 v66, v32, v35
	v_fmac_f32_e32 v62, v32, v41
	v_fmac_f32_e32 v65, v32, v36
	v_fmac_f32_e32 v61, v32, v42
	v_fmac_f32_e32 v64, v32, v37
	v_fmac_f32_e32 v60, v32, v43
	ds_read_b128 v[40:43], v81 offset:63488
	ds_read_b128 v[32:35], v81 offset:63504
	s_waitcnt lgkmcnt(1)
	v_fmac_f32_e32 v75, v39, v40
	s_waitcnt lgkmcnt(0)
	v_fmac_f32_e32 v63, v39, v32
	v_fmac_f32_e32 v65, v39, v42
	v_fmac_f32_e32 v61, v39, v34
	v_fmac_f32_e32 v66, v39, v41
	s_waitcnt lgkmcnt(3)
	s_nop 1
	v_add_f32_dpp v32, v75, v75 quad_perm:[1,0,3,2] row_mask:0xf bank_mask:0xf
	s_waitcnt lgkmcnt(2)
	s_nop 1
	v_add_f32_dpp v36, v65, v65 quad_perm:[1,0,3,2] row_mask:0xf bank_mask:0xf
	s_waitcnt lgkmcnt(1)
	s_nop 1
	v_add_f32_dpp v40, v63, v63 quad_perm:[1,0,3,2] row_mask:0xf bank_mask:0xf
	s_waitcnt lgkmcnt(0)
	s_nop 1
	v_add_f32_dpp v44, v61, v61 quad_perm:[1,0,3,2] row_mask:0xf bank_mask:0xf
	v_fmac_f32_e32 v62, v39, v33
	v_fmac_f32_e32 v64, v39, v43
	s_waitcnt lgkmcnt(3)
	s_nop 1
	v_add_f32_dpp v32, v32, v32 quad_perm:[2,3,0,1] row_mask:0xf bank_mask:0xf
	s_waitcnt lgkmcnt(2)
	s_nop 1
	v_add_f32_dpp v36, v36, v36 quad_perm:[2,3,0,1] row_mask:0xf bank_mask:0xf
	s_waitcnt lgkmcnt(1)
	s_nop 1
	v_add_f32_dpp v40, v40, v40 quad_perm:[2,3,0,1] row_mask:0xf bank_mask:0xf
	s_waitcnt lgkmcnt(0)
	s_nop 1
	v_add_f32_dpp v44, v44, v44 quad_perm:[2,3,0,1] row_mask:0xf bank_mask:0xf
	v_fmac_f32_e32 v60, v39, v35
	s_waitcnt lgkmcnt(3)
	s_nop 1
	v_add_f32_dpp v32, v32, v32 row_half_mirror row_mask:0xf bank_mask:0xf
	s_waitcnt lgkmcnt(2)
	s_nop 1
	v_add_f32_dpp v36, v36, v36 row_half_mirror row_mask:0xf bank_mask:0xf
	s_waitcnt lgkmcnt(1)
	s_nop 1
	v_add_f32_dpp v40, v40, v40 row_half_mirror row_mask:0xf bank_mask:0xf
	s_waitcnt lgkmcnt(0)
	s_nop 1
	v_add_f32_dpp v44, v44, v44 row_half_mirror row_mask:0xf bank_mask:0xf
	s_waitcnt lgkmcnt(3)
	s_nop 1
	v_add_f32_dpp v32, v32, v32 row_mirror row_mask:0xf bank_mask:0xf
	s_waitcnt lgkmcnt(2)
	s_nop 1
	v_add_f32_dpp v36, v36, v36 row_mirror row_mask:0xf bank_mask:0xf
	s_waitcnt lgkmcnt(1)
	s_nop 1
	v_add_f32_dpp v40, v40, v40 row_mirror row_mask:0xf bank_mask:0xf
	s_waitcnt lgkmcnt(0)
	s_nop 1
	v_add_f32_dpp v44, v44, v44 row_mirror row_mask:0xf bank_mask:0xf
	v_mov_b32_e32 v33, v32
	v_mov_b32_e32 v37, v36
	v_mov_b32_e32 v41, v40
	v_mov_b32_e32 v45, v44
	s_waitcnt lgkmcnt(3)
	s_nop 1
	v_permlane16_swap_b32_e32 v32, v33
	v_add_f32_e32 v32, v32, v33
	s_waitcnt lgkmcnt(3)
	s_nop 1
	v_permlane16_swap_b32_e32 v36, v37
	v_add_f32_e32 v36, v36, v37
	s_waitcnt lgkmcnt(3)
	s_nop 1
	v_permlane16_swap_b32_e32 v40, v41
	v_add_f32_e32 v40, v40, v41
	s_waitcnt lgkmcnt(3)
	s_nop 1
	v_permlane16_swap_b32_e32 v44, v45
	v_add_f32_e32 v44, v44, v45
	s_waitcnt lgkmcnt(3)
	s_nop 1
	v_add_f32_dpp v33, v66, v66 quad_perm:[1,0,3,2] row_mask:0xf bank_mask:0xf
	s_waitcnt lgkmcnt(2)
	s_nop 1
	v_add_f32_dpp v37, v64, v64 quad_perm:[1,0,3,2] row_mask:0xf bank_mask:0xf
	s_waitcnt lgkmcnt(1)
	s_nop 1
	v_add_f32_dpp v41, v62, v62 quad_perm:[1,0,3,2] row_mask:0xf bank_mask:0xf
	s_waitcnt lgkmcnt(1)
	s_nop 1
	v_add_f32_dpp v45, v60, v60 quad_perm:[1,0,3,2] row_mask:0xf bank_mask:0xf
	s_waitcnt lgkmcnt(3)
	s_nop 1
	v_add_f32_dpp v33, v33, v33 quad_perm:[2,3,0,1] row_mask:0xf bank_mask:0xf
	s_waitcnt lgkmcnt(3)
	s_nop 1
	v_add_f32_dpp v37, v37, v37 quad_perm:[2,3,0,1] row_mask:0xf bank_mask:0xf
	s_waitcnt lgkmcnt(2)
	s_nop 1
	v_add_f32_dpp v41, v41, v41 quad_perm:[2,3,0,1] row_mask:0xf bank_mask:0xf
	s_waitcnt lgkmcnt(1)
	s_nop 1
	v_add_f32_dpp v45, v45, v45 quad_perm:[2,3,0,1] row_mask:0xf bank_mask:0xf
	s_waitcnt lgkmcnt(3)
	s_nop 1
	v_add_f32_dpp v33, v33, v33 row_half_mirror row_mask:0xf bank_mask:0xf
	s_waitcnt lgkmcnt(3)
	s_nop 1
	v_add_f32_dpp v37, v37, v37 row_half_mirror row_mask:0xf bank_mask:0xf
	s_waitcnt lgkmcnt(2)
	s_nop 1
	v_add_f32_dpp v41, v41, v41 row_half_mirror row_mask:0xf bank_mask:0xf
	s_waitcnt lgkmcnt(1)
	s_nop 1
	v_add_f32_dpp v45, v45, v45 row_half_mirror row_mask:0xf bank_mask:0xf
	s_waitcnt lgkmcnt(3)
	s_nop 1
	v_add_f32_dpp v33, v33, v33 row_mirror row_mask:0xf bank_mask:0xf
	v_mov_b32_e32 v35, v33
	s_waitcnt lgkmcnt(3)
	s_nop 1
	v_add_f32_dpp v37, v37, v37 row_mirror row_mask:0xf bank_mask:0xf
	s_waitcnt lgkmcnt(2)
	s_nop 1
	v_add_f32_dpp v41, v41, v41 row_mirror row_mask:0xf bank_mask:0xf
	s_waitcnt lgkmcnt(1)
	s_nop 1
	v_add_f32_dpp v45, v45, v45 row_mirror row_mask:0xf bank_mask:0xf
	v_mov_b32_e32 v39, v37
	v_mov_b32_e32 v43, v41
	v_mov_b32_e32 v47, v45
	s_waitcnt lgkmcnt(3)
	s_nop 1
	v_permlane16_swap_b32_e32 v33, v35
	v_add_f32_e32 v33, v33, v35
	v_mov_b32_e32 v34, v32
	s_waitcnt lgkmcnt(2)
	s_nop 1
	v_permlane16_swap_b32_e32 v37, v39
	v_add_f32_e32 v37, v37, v39
	s_waitcnt lgkmcnt(1)
	s_nop 1
	v_permlane16_swap_b32_e32 v41, v43
	v_add_f32_e32 v41, v41, v43
	s_waitcnt lgkmcnt(0)
	s_nop 1
	v_permlane16_swap_b32_e32 v45, v47
	v_add_f32_e32 v45, v45, v47
	v_mov_b32_e32 v35, v33
	v_mov_b32_e32 v38, v36
	v_mov_b32_e32 v39, v37
	v_mov_b32_e32 v42, v40
	v_mov_b32_e32 v43, v41
	v_mov_b32_e32 v46, v44
	v_mov_b32_e32 v47, v45
	v_permlane32_swap_b32_e32 v32, v34
	v_permlane32_swap_b32_e32 v33, v35
	v_permlane32_swap_b32_e32 v36, v38
	v_permlane32_swap_b32_e32 v37, v39
	v_permlane32_swap_b32_e32 v40, v42
	v_permlane32_swap_b32_e32 v41, v43
	v_permlane32_swap_b32_e32 v44, v46
	v_permlane32_swap_b32_e32 v45, v47
	s_and_saveexec_b64 s[26:27], s[4:5]
	s_cbranch_execz .LBB0_1544
	v_readlane_b32 s80, v254, 23
	v_readlane_b32 s84, v254, 27
	v_readlane_b32 s85, v254, 28
	v_readlane_b32 s86, v254, 29
	v_readlane_b32 s87, v254, 30
	v_readlane_b32 s88, v254, 31
	v_readlane_b32 s89, v254, 32
	v_readlane_b32 s90, v254, 33
	v_readlane_b32 s91, v254, 34
	v_readlane_b32 s92, v254, 35
	v_readlane_b32 s93, v254, 36
	v_readlane_b32 s94, v254, 37
	v_readlane_b32 s95, v254, 38
	s_mov_b64 s[8:9], s[84:85]
	s_mov_b64 s[14:15], s[90:91]
	global_load_dwordx4 v[48:51], v97, s[14:15]
	global_load_dwordx4 v[52:55], v97, s[14:15] offset:16
	v_pk_add_f32 v[32:33], v[32:33], v[34:35]
	v_pk_add_f32 v[34:35], v[36:37], v[38:39]
	v_pk_add_f32 v[40:41], v[40:41], v[42:43]
	v_pk_add_f32 v[42:43], v[44:45], v[46:47]
	s_mov_b64 s[10:11], s[86:87]
	s_mov_b64 s[12:13], s[88:89]
	s_mov_b64 s[16:17], s[92:93]
	s_mov_b64 s[18:19], s[94:95]
	s_ashr_i32 s21, s20, 31
	v_readlane_b32 s81, v254, 24
	v_readlane_b32 s82, v254, 25
	v_readlane_b32 s83, v254, 26
	s_waitcnt vmcnt(1)
	v_pk_add_f32 v[38:39], v[32:33], v[48:49]
	s_nop 0
	v_cmp_gt_f32_e32 vcc, v39, v38
	v_pk_add_f32 v[36:37], v[34:35], v[50:51]
	s_waitcnt vmcnt(0)
	v_pk_add_f32 v[34:35], v[40:41], v[52:53]
	v_cndmask_b32_e32 v41, v38, v39, vcc
	v_cndmask_b32_e64 v40, 0, 1, vcc
	v_cmp_ngt_f32_e32 vcc, v36, v41
	v_pk_add_f32 v[32:33], v[42:43], v[54:55]
	s_nop 0
	v_cndmask_b32_e32 v40, 2, v40, vcc
	v_cmp_eq_u32_e32 vcc, 1, v40
	s_nop 1
	v_cndmask_b32_e32 v41, v38, v39, vcc
	v_cmp_eq_u32_e32 vcc, 2, v40
	s_nop 1
	v_cndmask_b32_e32 v41, v41, v36, vcc
	v_cmp_eq_u32_e32 vcc, 3, v40
	s_nop 1
	v_cndmask_b32_e32 v41, v41, v37, vcc
	v_cmp_eq_u32_e32 vcc, 4, v40
	s_nop 1
	v_cndmask_b32_e32 v41, v41, v34, vcc
	v_cmp_eq_u32_e32 vcc, 5, v40
	s_nop 1
	v_cndmask_b32_e32 v41, v41, v35, vcc
	v_cmp_eq_u32_e32 vcc, 6, v40
	s_nop 1
	v_cndmask_b32_e32 v41, v41, v32, vcc
	v_cmp_eq_u32_e32 vcc, 7, v40
	s_nop 1
	v_cndmask_b32_e32 v41, v41, v33, vcc
	v_cmp_ngt_f32_e32 vcc, v37, v41
	s_nop 1
	v_cndmask_b32_e32 v40, 3, v40, vcc
	v_cmp_eq_u32_e32 vcc, 1, v40
	s_nop 1
	v_cndmask_b32_e32 v41, v38, v39, vcc
	v_cmp_eq_u32_e32 vcc, 2, v40
	s_nop 1
	v_cndmask_b32_e32 v41, v41, v36, vcc
	v_cmp_eq_u32_e32 vcc, 3, v40
	s_nop 1
	v_cndmask_b32_e32 v41, v41, v37, vcc
	v_cmp_eq_u32_e32 vcc, 4, v40
	s_nop 1
	v_cndmask_b32_e32 v41, v41, v34, vcc
	v_cmp_eq_u32_e32 vcc, 5, v40
	s_nop 1
	v_cndmask_b32_e32 v41, v41, v35, vcc
	v_cmp_eq_u32_e32 vcc, 6, v40
	s_nop 1
	v_cndmask_b32_e32 v41, v41, v32, vcc
	v_cmp_eq_u32_e32 vcc, 7, v40
	s_nop 1
	v_cndmask_b32_e32 v41, v41, v33, vcc
	v_cmp_ngt_f32_e32 vcc, v34, v41
	s_nop 1
	v_cndmask_b32_e32 v40, 4, v40, vcc
	v_cmp_eq_u32_e32 vcc, 1, v40
	s_nop 1
	v_cndmask_b32_e32 v41, v38, v39, vcc
	v_cmp_eq_u32_e32 vcc, 2, v40
	s_nop 1
	v_cndmask_b32_e32 v41, v41, v36, vcc
	v_cmp_eq_u32_e32 vcc, 3, v40
	s_nop 1
	v_cndmask_b32_e32 v41, v41, v37, vcc
	v_cmp_eq_u32_e32 vcc, 4, v40
	s_nop 1
	v_cndmask_b32_e32 v41, v41, v34, vcc
	v_cmp_eq_u32_e32 vcc, 5, v40
	s_nop 1
	v_cndmask_b32_e32 v41, v41, v35, vcc
	v_cmp_eq_u32_e32 vcc, 6, v40
	s_nop 1
	v_cndmask_b32_e32 v41, v41, v32, vcc
	v_cmp_eq_u32_e32 vcc, 7, v40
	s_nop 1
	v_cndmask_b32_e32 v41, v41, v33, vcc
	v_cmp_ngt_f32_e32 vcc, v35, v41
	s_nop 1
	v_cndmask_b32_e32 v40, 5, v40, vcc
	v_cmp_eq_u32_e32 vcc, 1, v40
	s_nop 1
	v_cndmask_b32_e32 v41, v38, v39, vcc
	v_cmp_eq_u32_e32 vcc, 2, v40
	s_nop 1
	v_cndmask_b32_e32 v41, v41, v36, vcc
	v_cmp_eq_u32_e32 vcc, 3, v40
	s_nop 1
	v_cndmask_b32_e32 v41, v41, v37, vcc
	v_cmp_eq_u32_e32 vcc, 4, v40
	s_nop 1
	v_cndmask_b32_e32 v41, v41, v34, vcc
	v_cmp_eq_u32_e32 vcc, 5, v40
	s_nop 1
	v_cndmask_b32_e32 v41, v41, v35, vcc
	v_cmp_eq_u32_e32 vcc, 6, v40
	s_nop 1
	v_cndmask_b32_e32 v41, v41, v32, vcc
	v_cmp_eq_u32_e32 vcc, 7, v40
	s_nop 1
	v_cndmask_b32_e32 v41, v41, v33, vcc
	v_cmp_gt_f32_e32 vcc, v32, v41
	s_nop 1
	v_cndmask_b32_e64 v40, v40, 6, vcc
	v_cmp_eq_u32_e64 s[6:7], 1, v40
	s_nop 1
	v_cndmask_b32_e64 v41, v38, v39, s[6:7]
	v_cmp_eq_u32_e64 s[6:7], 2, v40
	s_nop 1
	v_cndmask_b32_e64 v41, v41, v36, s[6:7]
	v_cmp_eq_u32_e64 s[6:7], 3, v40
	s_nop 1
	v_cndmask_b32_e64 v41, v41, v37, s[6:7]
	v_cmp_eq_u32_e64 s[6:7], 4, v40
	s_nop 1
	v_cndmask_b32_e64 v41, v41, v34, s[6:7]
	v_cmp_eq_u32_e64 s[6:7], 5, v40
	s_nop 1
	v_cndmask_b32_e64 v41, v41, v35, s[6:7]
	v_cmp_eq_u32_e64 s[6:7], 6, v40
	s_nop 1
	v_cndmask_b32_e64 v41, v41, v32, s[6:7]
	v_cmp_eq_u32_e64 s[6:7], 7, v40
	s_nop 1
	v_cndmask_b32_e64 v41, v41, v33, s[6:7]
	v_cmp_ngt_f32_e64 s[6:7], v33, v41
	s_and_b64 vcc, s[6:7], vcc
	s_nop 0
	v_cndmask_b32_e64 v40, 7, v40, s[6:7]
	v_cmp_eq_u32_e64 s[8:9], 0, v40
	s_nop 1
	v_cndmask_b32_e64 v41, 0, -1, s[8:9]
	v_cmp_eq_u32_e64 s[10:11], 1, v41
	s_nop 1
	v_cndmask_b32_e64 v42, v38, v39, s[10:11]
	v_cmp_eq_u32_e64 s[10:11], 2, v41
	s_nop 1
	v_cndmask_b32_e64 v42, v42, v36, s[10:11]
	v_cmp_eq_u32_e64 s[10:11], 3, v41
	s_nop 1
	v_cndmask_b32_e64 v42, v42, v37, s[10:11]
	v_cmp_eq_u32_e64 s[10:11], 4, v41
	s_nop 1
	v_cndmask_b32_e64 v42, v42, v34, s[10:11]
	v_cmp_eq_u32_e64 s[10:11], 5, v41
	s_nop 1
	v_cndmask_b32_e64 v42, v42, v35, s[10:11]
	v_cmp_eq_u32_e64 s[10:11], 6, v41
	s_nop 1
	v_cndmask_b32_e64 v42, v42, v32, s[10:11]
	v_cmp_eq_u32_e64 s[10:11], 7, v41
	s_nop 1
	v_cndmask_b32_e64 v42, v42, v33, s[10:11]
	v_cmp_gt_f32_e64 s[10:11], v39, v42
	s_or_b64 s[8:9], s[8:9], s[10:11]
	v_cndmask_b32_e64 v41, v41, 1, s[8:9]
	v_cmp_ne_u32_e64 s[8:9], 1, v40
	s_nop 1
	v_cndmask_b32_e64 v42, 0, v41, s[8:9]
	v_cmp_eq_u32_e64 s[10:11], 1, v42
	v_cmp_gt_i32_e64 s[8:9], 0, v42
	s_nop 0
	v_cndmask_b32_e64 v43, v38, v39, s[10:11]
	v_cmp_eq_u32_e64 s[10:11], 2, v42
	s_nop 1
	v_cndmask_b32_e64 v43, v43, v36, s[10:11]
	v_cmp_eq_u32_e64 s[10:11], 3, v42
	s_nop 1
	v_cndmask_b32_e64 v43, v43, v37, s[10:11]
	v_cmp_eq_u32_e64 s[10:11], 4, v42
	s_nop 1
	v_cndmask_b32_e64 v43, v43, v34, s[10:11]
	v_cmp_eq_u32_e64 s[10:11], 5, v42
	s_nop 1
	v_cndmask_b32_e64 v43, v43, v35, s[10:11]
	v_cmp_eq_u32_e64 s[10:11], 6, v42
	s_nop 1
	v_cndmask_b32_e64 v43, v43, v32, s[10:11]
	v_cmp_eq_u32_e64 s[10:11], 7, v42
	s_nop 1
	v_cndmask_b32_e64 v43, v43, v33, s[10:11]
	v_cmp_gt_f32_e64 s[10:11], v36, v43
	s_or_b64 s[8:9], s[8:9], s[10:11]
	v_cndmask_b32_e64 v42, v42, 2, s[8:9]
	v_cmp_eq_u32_e64 s[8:9], 2, v40
	s_nop 1
	v_cndmask_b32_e64 v41, v42, v41, s[8:9]
	v_cmp_eq_u32_e64 s[12:13], 1, v41
	v_cmp_gt_i32_e64 s[10:11], 0, v41
	s_nop 0
	v_cndmask_b32_e64 v43, v38, v39, s[12:13]
	v_cmp_eq_u32_e64 s[12:13], 2, v41
	s_nop 1
	v_cndmask_b32_e64 v43, v43, v36, s[12:13]
	v_cmp_eq_u32_e64 s[12:13], 3, v41
	s_nop 1
	v_cndmask_b32_e64 v43, v43, v37, s[12:13]
	v_cmp_eq_u32_e64 s[12:13], 4, v41
	s_nop 1
	v_cndmask_b32_e64 v43, v43, v34, s[12:13]
	v_cmp_eq_u32_e64 s[12:13], 5, v41
	s_nop 1
	v_cndmask_b32_e64 v43, v43, v35, s[12:13]
	v_cmp_eq_u32_e64 s[12:13], 6, v41
	s_nop 1
	v_cndmask_b32_e64 v43, v43, v32, s[12:13]
	v_cmp_eq_u32_e64 s[12:13], 7, v41
	s_nop 1
	v_cndmask_b32_e64 v43, v43, v33, s[12:13]
	v_cmp_gt_f32_e64 s[12:13], v37, v43
	s_or_b64 s[10:11], s[10:11], s[12:13]
	v_cndmask_b32_e64 v41, v41, 3, s[10:11]
	v_cmp_eq_u32_e64 s[10:11], 3, v40
	s_nop 1
	v_cndmask_b32_e64 v42, v41, v42, s[10:11]
	v_cmp_eq_u32_e64 s[14:15], 1, v42
	v_cmp_gt_i32_e64 s[12:13], 0, v42
	s_nop 0
	v_cndmask_b32_e64 v43, v38, v39, s[14:15]
	v_cmp_eq_u32_e64 s[14:15], 2, v42
	s_nop 1
	v_cndmask_b32_e64 v43, v43, v36, s[14:15]
	v_cmp_eq_u32_e64 s[14:15], 3, v42
	s_nop 1
	v_cndmask_b32_e64 v43, v43, v37, s[14:15]
	v_cmp_eq_u32_e64 s[14:15], 4, v42
	s_nop 1
	v_cndmask_b32_e64 v43, v43, v34, s[14:15]
	v_cmp_eq_u32_e64 s[14:15], 5, v42
	s_nop 1
	v_cndmask_b32_e64 v43, v43, v35, s[14:15]
	v_cmp_eq_u32_e64 s[14:15], 6, v42
	s_nop 1
	v_cndmask_b32_e64 v43, v43, v32, s[14:15]
	v_cmp_eq_u32_e64 s[14:15], 7, v42
	s_nop 1
	v_cndmask_b32_e64 v43, v43, v33, s[14:15]
	v_cmp_gt_f32_e64 s[14:15], v34, v43
	s_or_b64 s[12:13], s[12:13], s[14:15]
	v_cndmask_b32_e64 v42, v42, 4, s[12:13]
	v_cmp_eq_u32_e64 s[12:13], 4, v40
	s_nop 1
	v_cndmask_b32_e64 v41, v42, v41, s[12:13]
	v_cmp_eq_u32_e64 s[16:17], 1, v41
	v_cmp_gt_i32_e64 s[14:15], 0, v41
	s_nop 0
	v_cndmask_b32_e64 v43, v38, v39, s[16:17]
	v_cmp_eq_u32_e64 s[16:17], 2, v41
	s_nop 1
	v_cndmask_b32_e64 v43, v43, v36, s[16:17]
	v_cmp_eq_u32_e64 s[16:17], 3, v41
	s_nop 1
	v_cndmask_b32_e64 v43, v43, v37, s[16:17]
	v_cmp_eq_u32_e64 s[16:17], 4, v41
	s_nop 1
	v_cndmask_b32_e64 v43, v43, v34, s[16:17]
	v_cmp_eq_u32_e64 s[16:17], 5, v41
	s_nop 1
	v_cndmask_b32_e64 v43, v43, v35, s[16:17]
	v_cmp_eq_u32_e64 s[16:17], 6, v41
	s_nop 1
	v_cndmask_b32_e64 v43, v43, v32, s[16:17]
	v_cmp_eq_u32_e64 s[16:17], 7, v41
	s_nop 1
	v_cndmask_b32_e64 v43, v43, v33, s[16:17]
	v_cmp_gt_f32_e64 s[16:17], v35, v43
	s_or_b64 s[14:15], s[14:15], s[16:17]
	v_cndmask_b32_e64 v41, v41, 5, s[14:15]
	v_cmp_eq_u32_e64 s[14:15], 5, v40
	s_nop 1
	v_cndmask_b32_e64 v41, v41, v42, s[14:15]
	v_cmp_eq_u32_e64 s[18:19], 1, v41
	v_cmp_gt_i32_e64 s[16:17], 0, v41
	s_nop 0
	v_cndmask_b32_e64 v42, v38, v39, s[18:19]
	v_cmp_eq_u32_e64 s[18:19], 2, v41
	s_nop 1
	v_cndmask_b32_e64 v42, v42, v36, s[18:19]
	v_cmp_eq_u32_e64 s[18:19], 3, v41
	s_nop 1
	v_cndmask_b32_e64 v42, v42, v37, s[18:19]
	v_cmp_eq_u32_e64 s[18:19], 4, v41
	s_nop 1
	v_cndmask_b32_e64 v42, v42, v34, s[18:19]
	v_cmp_eq_u32_e64 s[18:19], 5, v41
	s_nop 1
	v_cndmask_b32_e64 v42, v42, v35, s[18:19]
	v_cmp_eq_u32_e64 s[18:19], 6, v41
	s_nop 1
	v_cndmask_b32_e64 v42, v42, v32, s[18:19]
	v_cmp_eq_u32_e64 s[18:19], 7, v41
	s_nop 1
	v_cndmask_b32_e64 v42, v42, v33, s[18:19]
	v_cmp_gt_f32_e64 s[18:19], v32, v42
	s_or_b64 s[16:17], s[16:17], s[18:19]
	v_cndmask_b32_e64 v42, v41, 6, s[16:17]
	v_cndmask_b32_e32 v41, v42, v41, vcc
	v_cmp_eq_u32_e64 s[16:17], 1, v41
	v_cmp_gt_i32_e32 vcc, 0, v41
	s_nop 0
	v_cndmask_b32_e64 v43, v38, v39, s[16:17]
	v_cmp_eq_u32_e64 s[16:17], 2, v41
	s_nop 1
	v_cndmask_b32_e64 v43, v43, v36, s[16:17]
	v_cmp_eq_u32_e64 s[16:17], 3, v41
	s_nop 1
	v_cndmask_b32_e64 v43, v43, v37, s[16:17]
	v_cmp_eq_u32_e64 s[16:17], 4, v41
	s_nop 1
	v_cndmask_b32_e64 v43, v43, v34, s[16:17]
	v_cmp_eq_u32_e64 s[16:17], 5, v41
	s_nop 1
	v_cndmask_b32_e64 v43, v43, v35, s[16:17]
	v_cmp_eq_u32_e64 s[16:17], 6, v41
	s_nop 1
	v_cndmask_b32_e64 v43, v43, v32, s[16:17]
	v_cmp_eq_u32_e64 s[16:17], 7, v41
	s_nop 1
	v_cndmask_b32_e64 v43, v43, v33, s[16:17]
	v_cmp_gt_f32_e64 s[16:17], v33, v43
	s_or_b64 s[16:17], vcc, s[16:17]
	s_nop 0
	v_cndmask_b32_e64 v41, v41, 7, s[16:17]
	v_cndmask_b32_e64 v41, v42, v41, s[6:7]
	v_cmp_eq_u32_e32 vcc, 1, v41
	s_mov_b32 s6, 0x3fb8aa3b
	s_nop 0
	v_cndmask_b32_e32 v42, v38, v39, vcc
	v_cmp_eq_u32_e32 vcc, 2, v41
	s_nop 1
	v_cndmask_b32_e32 v42, v42, v36, vcc
	v_cmp_eq_u32_e32 vcc, 3, v41
	s_nop 1
	v_cndmask_b32_e32 v42, v42, v37, vcc
	v_cmp_eq_u32_e32 vcc, 4, v41
	s_nop 1
	v_cndmask_b32_e32 v42, v42, v34, vcc
	v_cmp_eq_u32_e32 vcc, 5, v41
	s_nop 1
	v_cndmask_b32_e32 v42, v42, v35, vcc
	v_cmp_eq_u32_e32 vcc, 6, v41
	s_nop 1
	v_cndmask_b32_e32 v42, v42, v32, vcc
	v_cmp_eq_u32_e32 vcc, 7, v41
	s_nop 1
	v_cndmask_b32_e32 v42, v42, v33, vcc
	v_cmp_eq_u32_e32 vcc, 1, v40
	s_nop 1
	v_cndmask_b32_e32 v38, v38, v39, vcc
	v_cndmask_b32_e64 v36, v38, v36, s[8:9]
	v_cndmask_b32_e64 v36, v36, v37, s[10:11]
	v_cndmask_b32_e64 v34, v36, v34, s[12:13]
	v_cndmask_b32_e64 v34, v34, v35, s[14:15]
	v_cmp_eq_u32_e32 vcc, 6, v40
	s_nop 1
	v_cndmask_b32_e32 v32, v34, v32, vcc
	v_cmp_eq_u32_e32 vcc, 7, v40
	s_nop 1
	v_cndmask_b32_e32 v32, v32, v33, vcc
	v_sub_f32_e32 v32, v42, v32
	v_mul_f32_e32 v33, 0x3fb8aa3b, v32
	v_fma_f32 v34, v32, s6, -v33
	v_rndne_f32_e32 v35, v33
	v_fmac_f32_e32 v34, 0x32a5705f, v32
	v_sub_f32_e32 v33, v33, v35
	v_add_f32_e32 v33, v33, v34
	v_exp_f32_e32 v33, v33
	v_cvt_i32_f32_e32 v34, v35
	s_mov_b32 s6, 0xc2ce8ed0
	v_cmp_ngt_f32_e32 vcc, s6, v32
	s_mov_b32 s6, 0x42b17218
	v_ldexp_f32 v33, v33, v34
	v_cndmask_b32_e32 v33, 0, v33, vcc
	v_cmp_nlt_f32_e32 vcc, s6, v32
	v_mov_b32_e32 v32, 0x7f800000
	s_nop 0
	v_cndmask_b32_e32 v32, v32, v33, vcc
	v_add_f32_e32 v33, 1.0, v32
	v_div_scale_f32 v34, s[6:7], v33, v33, 1.0
	v_rcp_f32_e32 v35, v34
	s_lshl_b64 s[6:7], s[20:21], 2
	s_add_u32 s8, s28, s6
	s_addc_u32 s9, s29, s7
	v_fma_f32 v36, -v34, v35, 1.0
	v_fmac_f32_e32 v35, v36, v35
	v_div_scale_f32 v36, vcc, 1.0, v33, 1.0
	v_mul_f32_e32 v37, v36, v35
	v_fma_f32 v38, -v34, v37, v36
	v_fmac_f32_e32 v37, v38, v35
	s_add_i32 s10, s20, 1
	v_fma_f32 v34, -v34, v37, v36
	s_ashr_i32 s11, s10, 31
	v_div_fmas_f32 v34, v34, v35, v37
	s_add_u32 s6, s31, s6
	v_div_fixup_f32 v33, v34, v33, 1.0
	s_addc_u32 s7, s34, s7
	global_store_dword v97, v33, s[6:7]
	s_lshl_b64 s[6:7], s[10:11], 2
	s_add_u32 s6, s31, s6
	v_mul_f32_e32 v32, v32, v33
	s_addc_u32 s7, s34, s7
	global_store_dwordx2 v97, v[40:41], s[8:9]
	global_store_dword v97, v32, s[6:7]
	s_branch .LBB0_1544

.LBB0_1611:
	s_or_b64 exec, exec, s[12:13]
	v_cvt_f32_i32_e32 v0, v18
	v_cvt_f32_i32_e32 v1, v19
	s_waitcnt lgkmcnt(1)
	s_nop 1
	v_add_f32_dpp v0, v0, v0 quad_perm:[1,0,3,2] row_mask:0xf bank_mask:0xf
	s_waitcnt lgkmcnt(0)
	s_nop 1
	v_add_f32_dpp v1, v1, v1 quad_perm:[1,0,3,2] row_mask:0xf bank_mask:0xf
	s_waitcnt lgkmcnt(1)
	s_nop 1
	v_add_f32_dpp v0, v0, v0 quad_perm:[2,3,0,1] row_mask:0xf bank_mask:0xf
	s_waitcnt lgkmcnt(0)
	s_nop 1
	v_add_f32_dpp v1, v1, v1 quad_perm:[2,3,0,1] row_mask:0xf bank_mask:0xf
	s_waitcnt lgkmcnt(1)
	s_nop 1
	v_add_f32_dpp v0, v0, v0 row_half_mirror row_mask:0xf bank_mask:0xf
	s_waitcnt lgkmcnt(0)
	s_nop 1
	v_add_f32_dpp v1, v1, v1 row_half_mirror row_mask:0xf bank_mask:0xf
	s_waitcnt lgkmcnt(1)
	s_nop 1
	v_add_f32_dpp v18, v0, v0 row_mirror row_mask:0xf bank_mask:0xf
	s_waitcnt lgkmcnt(0)
	s_nop 1
	v_add_f32_dpp v1, v1, v1 row_mirror row_mask:0xf bank_mask:0xf
	v_mov_b32_e32 v19, v18
	s_waitcnt vmcnt(2)
	v_mov_b32_e32 v20, v1
	v_and_b32_e32 v0, 63, v17
	v_cmp_eq_u32_e32 vcc, 0, v0
	s_waitcnt lgkmcnt(1)
	s_nop 1
	v_permlane16_swap_b32_e32 v18, v19
	v_add_f32_e32 v18, v18, v19
	s_waitcnt lgkmcnt(0)
	s_nop 1
	v_permlane16_swap_b32_e32 v1, v20
	v_add_f32_e32 v1, v1, v20
	v_mov_b32_e32 v19, v18
	v_mov_b32_e32 v17, v1
	s_nop 0
	v_permlane32_swap_b32_e32 v18, v19
	v_permlane32_swap_b32_e32 v1, v17
	s_and_saveexec_b64 s[6:7], vcc
	s_cbranch_execz .LBB0_1620
	v_add_f32_e32 v18, v18, v19
	v_cvt_i32_f32_e32 v18, v18
	s_mov_b64 s[4:5], exec
	s_mov_b32 s12, 0

.LBB0_1620:
	s_or_b64 exec, exec, s[6:7]
	v_cvt_f32_i32_e32 v1, v15
	v_cvt_f32_i32_e32 v15, v16
	s_waitcnt lgkmcnt(1)
	s_nop 1
	v_add_f32_dpp v1, v1, v1 quad_perm:[1,0,3,2] row_mask:0xf bank_mask:0xf
	s_waitcnt lgkmcnt(0)
	s_nop 1
	v_add_f32_dpp v15, v15, v15 quad_perm:[1,0,3,2] row_mask:0xf bank_mask:0xf
	s_waitcnt lgkmcnt(1)
	s_nop 1
	v_add_f32_dpp v1, v1, v1 quad_perm:[2,3,0,1] row_mask:0xf bank_mask:0xf
	s_waitcnt lgkmcnt(0)
	s_nop 1
	v_add_f32_dpp v15, v15, v15 quad_perm:[2,3,0,1] row_mask:0xf bank_mask:0xf
	s_waitcnt lgkmcnt(1)
	s_nop 1
	v_add_f32_dpp v1, v1, v1 row_half_mirror row_mask:0xf bank_mask:0xf
	s_waitcnt lgkmcnt(0)
	s_nop 1
	v_add_f32_dpp v15, v15, v15 row_half_mirror row_mask:0xf bank_mask:0xf
	s_waitcnt lgkmcnt(1)
	s_nop 1
	v_add_f32_dpp v1, v1, v1 row_mirror row_mask:0xf bank_mask:0xf
	s_waitcnt lgkmcnt(0)
	s_nop 1
	v_add_f32_dpp v15, v15, v15 row_mirror row_mask:0xf bank_mask:0xf
	v_mov_b32_e32 v16, v1
	v_mov_b32_e32 v17, v15
	s_waitcnt lgkmcnt(1)
	s_nop 1
	v_permlane16_swap_b32_e32 v1, v16
	v_add_f32_e32 v16, v1, v16
	s_waitcnt lgkmcnt(0)
	s_nop 1
	v_permlane16_swap_b32_e32 v15, v17
	v_add_f32_e32 v1, v15, v17
	v_mov_b32_e32 v17, v16
	v_mov_b32_e32 v15, v1
	s_nop 0
	v_permlane32_swap_b32_e32 v16, v17
	v_permlane32_swap_b32_e32 v1, v15
	s_and_saveexec_b64 s[6:7], vcc
	s_cbranch_execz .LBB0_1629
	v_add_f32_e32 v16, v16, v17
	v_cvt_i32_f32_e32 v16, v16
	s_mov_b64 s[4:5], exec
	s_mov_b32 s12, 0

.LBB0_1629:
	s_or_b64 exec, exec, s[6:7]
	v_cvt_f32_i32_e32 v1, v13
	v_cvt_f32_i32_e32 v13, v14
	s_waitcnt lgkmcnt(1)
	s_nop 1
	v_add_f32_dpp v1, v1, v1 quad_perm:[1,0,3,2] row_mask:0xf bank_mask:0xf
	s_waitcnt lgkmcnt(0)
	s_nop 1
	v_add_f32_dpp v13, v13, v13 quad_perm:[1,0,3,2] row_mask:0xf bank_mask:0xf
	s_waitcnt lgkmcnt(1)
	s_nop 1
	v_add_f32_dpp v1, v1, v1 quad_perm:[2,3,0,1] row_mask:0xf bank_mask:0xf
	s_waitcnt lgkmcnt(0)
	s_nop 1
	v_add_f32_dpp v13, v13, v13 quad_perm:[2,3,0,1] row_mask:0xf bank_mask:0xf
	s_waitcnt lgkmcnt(1)
	s_nop 1
	v_add_f32_dpp v1, v1, v1 row_half_mirror row_mask:0xf bank_mask:0xf
	s_waitcnt lgkmcnt(0)
	s_nop 1
	v_add_f32_dpp v13, v13, v13 row_half_mirror row_mask:0xf bank_mask:0xf
	s_waitcnt lgkmcnt(1)
	s_nop 1
	v_add_f32_dpp v1, v1, v1 row_mirror row_mask:0xf bank_mask:0xf
	s_waitcnt lgkmcnt(0)
	s_nop 1
	v_add_f32_dpp v13, v13, v13 row_mirror row_mask:0xf bank_mask:0xf
	v_mov_b32_e32 v14, v1
	v_mov_b32_e32 v15, v13
	s_waitcnt lgkmcnt(1)
	s_nop 1
	v_permlane16_swap_b32_e32 v1, v14
	v_add_f32_e32 v14, v1, v14
	s_waitcnt lgkmcnt(0)
	s_nop 1
	v_permlane16_swap_b32_e32 v13, v15
	v_add_f32_e32 v1, v13, v15
	v_mov_b32_e32 v15, v14
	v_mov_b32_e32 v13, v1
	s_nop 0
	v_permlane32_swap_b32_e32 v14, v15
	v_permlane32_swap_b32_e32 v1, v13
	s_and_saveexec_b64 s[6:7], vcc
	s_cbranch_execz .LBB0_1638
	v_add_f32_e32 v14, v14, v15
	v_cvt_i32_f32_e32 v14, v14
	s_mov_b64 s[4:5], exec
	s_mov_b32 s12, 0

.LBB0_1638:
	s_or_b64 exec, exec, s[6:7]
	v_cvt_f32_i32_e32 v1, v11
	v_cvt_f32_i32_e32 v11, v12
	s_waitcnt lgkmcnt(1)
	s_nop 1
	v_add_f32_dpp v1, v1, v1 quad_perm:[1,0,3,2] row_mask:0xf bank_mask:0xf
	s_waitcnt lgkmcnt(0)
	s_nop 1
	v_add_f32_dpp v11, v11, v11 quad_perm:[1,0,3,2] row_mask:0xf bank_mask:0xf
	s_waitcnt lgkmcnt(1)
	s_nop 1
	v_add_f32_dpp v1, v1, v1 quad_perm:[2,3,0,1] row_mask:0xf bank_mask:0xf
	s_waitcnt lgkmcnt(0)
	s_nop 1
	v_add_f32_dpp v11, v11, v11 quad_perm:[2,3,0,1] row_mask:0xf bank_mask:0xf
	s_waitcnt lgkmcnt(1)
	s_nop 1
	v_add_f32_dpp v1, v1, v1 row_half_mirror row_mask:0xf bank_mask:0xf
	s_waitcnt lgkmcnt(0)
	s_nop 1
	v_add_f32_dpp v11, v11, v11 row_half_mirror row_mask:0xf bank_mask:0xf
	s_waitcnt lgkmcnt(1)
	s_nop 1
	v_add_f32_dpp v1, v1, v1 row_mirror row_mask:0xf bank_mask:0xf
	s_waitcnt lgkmcnt(0)
	s_nop 1
	v_add_f32_dpp v11, v11, v11 row_mirror row_mask:0xf bank_mask:0xf
	v_mov_b32_e32 v12, v1
	v_mov_b32_e32 v13, v11
	s_waitcnt lgkmcnt(1)
	s_nop 1
	v_permlane16_swap_b32_e32 v1, v12
	v_add_f32_e32 v12, v1, v12
	s_waitcnt lgkmcnt(0)
	s_nop 1
	v_permlane16_swap_b32_e32 v11, v13
	v_add_f32_e32 v1, v11, v13
	v_mov_b32_e32 v13, v12
	v_mov_b32_e32 v11, v1
	s_nop 0
	v_permlane32_swap_b32_e32 v12, v13
	v_permlane32_swap_b32_e32 v1, v11
	s_and_saveexec_b64 s[6:7], vcc
	s_cbranch_execz .LBB0_1647
	v_add_f32_e32 v12, v12, v13
	v_cvt_i32_f32_e32 v12, v12
	s_mov_b64 s[4:5], exec
	s_mov_b32 s12, 0

.LBB0_1647:
	s_or_b64 exec, exec, s[6:7]
	v_cvt_f32_i32_e32 v1, v9
	v_cvt_f32_i32_e32 v9, v10
	s_waitcnt lgkmcnt(1)
	s_nop 1
	v_add_f32_dpp v1, v1, v1 quad_perm:[1,0,3,2] row_mask:0xf bank_mask:0xf
	s_waitcnt lgkmcnt(0)
	s_nop 1
	v_add_f32_dpp v9, v9, v9 quad_perm:[1,0,3,2] row_mask:0xf bank_mask:0xf
	s_waitcnt lgkmcnt(1)
	s_nop 1
	v_add_f32_dpp v1, v1, v1 quad_perm:[2,3,0,1] row_mask:0xf bank_mask:0xf
	s_waitcnt lgkmcnt(0)
	s_nop 1
	v_add_f32_dpp v9, v9, v9 quad_perm:[2,3,0,1] row_mask:0xf bank_mask:0xf
	s_waitcnt lgkmcnt(1)
	s_nop 1
	v_add_f32_dpp v1, v1, v1 row_half_mirror row_mask:0xf bank_mask:0xf
	s_waitcnt lgkmcnt(0)
	s_nop 1
	v_add_f32_dpp v9, v9, v9 row_half_mirror row_mask:0xf bank_mask:0xf
	s_waitcnt lgkmcnt(1)
	s_nop 1
	v_add_f32_dpp v1, v1, v1 row_mirror row_mask:0xf bank_mask:0xf
	s_waitcnt lgkmcnt(0)
	s_nop 1
	v_add_f32_dpp v9, v9, v9 row_mirror row_mask:0xf bank_mask:0xf
	v_mov_b32_e32 v10, v1
	v_mov_b32_e32 v11, v9
	s_waitcnt lgkmcnt(1)
	s_nop 1
	v_permlane16_swap_b32_e32 v1, v10
	v_add_f32_e32 v10, v1, v10
	s_waitcnt lgkmcnt(0)
	s_nop 1
	v_permlane16_swap_b32_e32 v9, v11
	v_add_f32_e32 v1, v9, v11
	v_mov_b32_e32 v11, v10
	v_mov_b32_e32 v9, v1
	s_nop 0
	v_permlane32_swap_b32_e32 v10, v11
	v_permlane32_swap_b32_e32 v1, v9
	s_and_saveexec_b64 s[6:7], vcc
	s_cbranch_execz .LBB0_1656
	v_add_f32_e32 v10, v10, v11
	v_cvt_i32_f32_e32 v10, v10
	s_mov_b64 s[4:5], exec
	s_mov_b32 s12, 0

.LBB0_1656:
	s_or_b64 exec, exec, s[6:7]
	v_cvt_f32_i32_e32 v1, v7
	v_cvt_f32_i32_e32 v7, v8
	s_waitcnt lgkmcnt(1)
	s_nop 1
	v_add_f32_dpp v1, v1, v1 quad_perm:[1,0,3,2] row_mask:0xf bank_mask:0xf
	s_waitcnt lgkmcnt(0)
	s_nop 1
	v_add_f32_dpp v7, v7, v7 quad_perm:[1,0,3,2] row_mask:0xf bank_mask:0xf
	s_waitcnt lgkmcnt(1)
	s_nop 1
	v_add_f32_dpp v1, v1, v1 quad_perm:[2,3,0,1] row_mask:0xf bank_mask:0xf
	s_waitcnt lgkmcnt(0)
	s_nop 1
	v_add_f32_dpp v7, v7, v7 quad_perm:[2,3,0,1] row_mask:0xf bank_mask:0xf
	s_waitcnt lgkmcnt(1)
	s_nop 1
	v_add_f32_dpp v1, v1, v1 row_half_mirror row_mask:0xf bank_mask:0xf
	s_waitcnt lgkmcnt(0)
	s_nop 1
	v_add_f32_dpp v7, v7, v7 row_half_mirror row_mask:0xf bank_mask:0xf
	s_waitcnt lgkmcnt(1)
	s_nop 1
	v_add_f32_dpp v1, v1, v1 row_mirror row_mask:0xf bank_mask:0xf
	s_waitcnt lgkmcnt(0)
	s_nop 1
	v_add_f32_dpp v7, v7, v7 row_mirror row_mask:0xf bank_mask:0xf
	v_mov_b32_e32 v8, v1
	v_mov_b32_e32 v9, v7
	s_waitcnt lgkmcnt(1)
	s_nop 1
	v_permlane16_swap_b32_e32 v1, v8
	v_add_f32_e32 v8, v1, v8
	s_waitcnt lgkmcnt(0)
	s_nop 1
	v_permlane16_swap_b32_e32 v7, v9
	v_add_f32_e32 v1, v7, v9
	v_mov_b32_e32 v9, v8
	v_mov_b32_e32 v7, v1
	s_nop 0
	v_permlane32_swap_b32_e32 v8, v9
	v_permlane32_swap_b32_e32 v1, v7
	s_and_saveexec_b64 s[6:7], vcc
	s_cbranch_execz .LBB0_1665
	v_add_f32_e32 v8, v8, v9
	v_cvt_i32_f32_e32 v8, v8
	s_mov_b64 s[4:5], exec
	s_mov_b32 s12, 0

.LBB0_1665:
	s_or_b64 exec, exec, s[6:7]
	v_cvt_f32_i32_e32 v1, v5
	v_cvt_f32_i32_e32 v5, v6
	s_waitcnt lgkmcnt(1)
	s_nop 1
	v_add_f32_dpp v1, v1, v1 quad_perm:[1,0,3,2] row_mask:0xf bank_mask:0xf
	s_waitcnt lgkmcnt(0)
	s_nop 1
	v_add_f32_dpp v5, v5, v5 quad_perm:[1,0,3,2] row_mask:0xf bank_mask:0xf
	s_waitcnt lgkmcnt(1)
	s_nop 1
	v_add_f32_dpp v1, v1, v1 quad_perm:[2,3,0,1] row_mask:0xf bank_mask:0xf
	s_waitcnt lgkmcnt(0)
	s_nop 1
	v_add_f32_dpp v5, v5, v5 quad_perm:[2,3,0,1] row_mask:0xf bank_mask:0xf
	s_waitcnt lgkmcnt(1)
	s_nop 1
	v_add_f32_dpp v1, v1, v1 row_half_mirror row_mask:0xf bank_mask:0xf
	s_waitcnt lgkmcnt(0)
	s_nop 1
	v_add_f32_dpp v5, v5, v5 row_half_mirror row_mask:0xf bank_mask:0xf
	s_waitcnt lgkmcnt(1)
	s_nop 1
	v_add_f32_dpp v1, v1, v1 row_mirror row_mask:0xf bank_mask:0xf
	s_waitcnt lgkmcnt(0)
	s_nop 1
	v_add_f32_dpp v5, v5, v5 row_mirror row_mask:0xf bank_mask:0xf
	v_mov_b32_e32 v6, v1
	v_mov_b32_e32 v7, v5
	s_waitcnt lgkmcnt(1)
	s_nop 1
	v_permlane16_swap_b32_e32 v1, v6
	v_add_f32_e32 v6, v1, v6
	s_waitcnt lgkmcnt(0)
	s_nop 1
	v_permlane16_swap_b32_e32 v5, v7
	v_add_f32_e32 v1, v5, v7
	v_mov_b32_e32 v7, v6
	v_mov_b32_e32 v5, v1
	s_nop 0
	v_permlane32_swap_b32_e32 v6, v7
	v_permlane32_swap_b32_e32 v1, v5
	s_and_saveexec_b64 s[6:7], vcc
	s_cbranch_execz .LBB0_1674
	v_add_f32_e32 v6, v6, v7
	v_cvt_i32_f32_e32 v6, v6
	s_mov_b64 s[4:5], exec
	s_mov_b32 s12, 0

.LBB0_1674:
	s_or_b64 exec, exec, s[6:7]
	v_cvt_f32_i32_e32 v1, v3
	v_cvt_f32_i32_e32 v3, v4
	s_waitcnt lgkmcnt(1)
	s_nop 1
	v_add_f32_dpp v1, v1, v1 quad_perm:[1,0,3,2] row_mask:0xf bank_mask:0xf
	s_waitcnt lgkmcnt(0)
	s_nop 1
	v_add_f32_dpp v3, v3, v3 quad_perm:[1,0,3,2] row_mask:0xf bank_mask:0xf
	s_waitcnt lgkmcnt(1)
	s_nop 1
	v_add_f32_dpp v1, v1, v1 quad_perm:[2,3,0,1] row_mask:0xf bank_mask:0xf
	s_waitcnt lgkmcnt(0)
	s_nop 1
	v_add_f32_dpp v3, v3, v3 quad_perm:[2,3,0,1] row_mask:0xf bank_mask:0xf
	s_waitcnt lgkmcnt(1)
	s_nop 1
	v_add_f32_dpp v1, v1, v1 row_half_mirror row_mask:0xf bank_mask:0xf
	s_waitcnt lgkmcnt(0)
	s_nop 1
	v_add_f32_dpp v3, v3, v3 row_half_mirror row_mask:0xf bank_mask:0xf
	s_waitcnt lgkmcnt(1)
	s_nop 1
	v_add_f32_dpp v1, v1, v1 row_mirror row_mask:0xf bank_mask:0xf
	s_waitcnt lgkmcnt(0)
	s_nop 1
	v_add_f32_dpp v3, v3, v3 row_mirror row_mask:0xf bank_mask:0xf
	v_mov_b32_e32 v4, v1
	v_mov_b32_e32 v5, v3
	s_waitcnt lgkmcnt(1)
	s_nop 1
	v_permlane16_swap_b32_e32 v1, v4
	v_add_f32_e32 v4, v1, v4
	s_waitcnt lgkmcnt(0)
	s_nop 1
	v_permlane16_swap_b32_e32 v3, v5
	v_add_f32_e32 v1, v3, v5
	v_mov_b32_e32 v5, v4
	v_mov_b32_e32 v3, v1
	s_nop 0
	v_permlane32_swap_b32_e32 v4, v5
	v_permlane32_swap_b32_e32 v1, v3
	s_and_saveexec_b64 s[4:5], vcc
	s_cbranch_execz .LBB0_1683
	v_add_f32_e32 v4, v4, v5
	v_cvt_i32_f32_e32 v4, v4
	s_mov_b64 s[6:7], exec
	s_mov_b32 s12, 0

.LBB0_2114:
	s_andn2_b64 vcc, exec, s[4:5]
	s_mov_b32 s20, 25
	s_cbranch_vccnz .LBB0_2190
	v_mov_b32_e32 v0, v130
	s_barrier
	s_nop 0
	v_cmp_gt_i32_e32 vcc, 64, v0
	s_and_saveexec_b64 s[4:5], vcc
	s_cbranch_execz .LBB0_2120
	s_waitcnt vmcnt(0)
	v_mov_b32_e32 v7, 0x10000
	global_load_dword v140, v7, s[44:45] sc1
	global_load_dword v141, v7, s[44:45] offset:4 sc1
	global_load_dword v142, v7, s[44:45] offset:8 sc1
	global_load_dword v143, v7, s[44:45] offset:12 sc1
	global_load_dword v144, v7, s[44:45] offset:16 sc1
	global_load_dword v145, v7, s[44:45] offset:20 sc1
	global_load_dword v146, v7, s[44:45] offset:24 sc1
	global_load_dword v147, v7, s[44:45] offset:28 sc1
	v_mul_lo_u32 v1, v0, s96
	v_add_u32_e32 v1, s34, v1
	s_waitcnt vmcnt(7)
	v_readfirstlane_b32 s2, v140
	s_addk_i32 s2, 0xff
	s_ashr_i32 s3, s2, 31
	s_lshr_b32 s3, s3, 24
	s_add_i32 s2, s2, s3
	s_ashr_i32 s8, s2, 8
	s_waitcnt vmcnt(6)
	v_readfirstlane_b32 s2, v141
	s_addk_i32 s2, 0xff
	s_ashr_i32 s3, s2, 31
	s_lshr_b32 s3, s3, 24
	s_add_i32 s2, s2, s3
	s_ashr_i32 s2, s2, 8
	s_add_i32 s2, s2, s8
	s_waitcnt vmcnt(5)
	v_readfirstlane_b32 s3, v142
	s_addk_i32 s3, 0xff
	s_ashr_i32 s6, s3, 31
	s_lshr_b32 s6, s6, 24
	s_add_i32 s3, s3, s6
	s_ashr_i32 s9, s3, 8
	s_add_i32 s9, s9, s2
	s_waitcnt vmcnt(4)
	v_add_u32_e32 v2, 0xff, v143
	v_ashrrev_i32_e32 v3, 31, v2
	v_add_u32_sdwa v2, v2, v3 dst_sel:DWORD dst_unused:UNUSED_PAD src0_sel:DWORD src1_sel:BYTE_3
	v_ashrrev_i32_e32 v2, 8, v2
	v_add_u32_e32 v2, s9, v2
	s_waitcnt vmcnt(3)
	v_add_u32_e32 v3, 0xff, v144
	v_ashrrev_i32_e32 v4, 31, v3
	v_add_u32_sdwa v3, v3, v4 dst_sel:DWORD dst_unused:UNUSED_PAD src0_sel:DWORD src1_sel:BYTE_3
	v_ashrrev_i32_e32 v3, 8, v3
	v_add_u32_e32 v3, v3, v2
	s_waitcnt vmcnt(2)
	v_add_u32_e32 v4, 0xff, v145
	v_ashrrev_i32_e32 v5, 31, v4
	v_add_u32_sdwa v4, v4, v5 dst_sel:DWORD dst_unused:UNUSED_PAD src0_sel:DWORD src1_sel:BYTE_3
	v_ashrrev_i32_e32 v4, 8, v4
	v_add_u32_e32 v4, v4, v3
	s_waitcnt vmcnt(1)
	v_add_u32_e32 v5, 0xff, v146
	v_ashrrev_i32_e32 v6, 31, v5
	v_add_u32_sdwa v5, v5, v6 dst_sel:DWORD dst_unused:UNUSED_PAD src0_sel:DWORD src1_sel:BYTE_3
	v_ashrrev_i32_e32 v5, 8, v5
	v_add_u32_e32 v5, v5, v4
	s_waitcnt vmcnt(0)
	v_add_u32_e32 v6, 0xff, v147
	v_ashrrev_i32_e32 v7, 31, v6
	v_add_u32_sdwa v6, v6, v7 dst_sel:DWORD dst_unused:UNUSED_PAD src0_sel:DWORD src1_sel:BYTE_3
	v_ashrrev_i32_e32 v6, 8, v6
	v_add_u32_e32 v6, v6, v5
	v_min_i32_e32 v6, 0x48, v6
	v_mul_lo_u32 v6, v6, 44
	v_cmp_lt_i32_e32 vcc, v1, v6
	s_and_saveexec_b64 s[6:7], vcc
	s_cbranch_execz .LBB0_2118
	s_mov_b32 s3, 0x2e8ba2e9
	v_mul_hi_i32 v6, v1, s3
	v_lshrrev_b32_e32 v7, 31, v6
	v_ashrrev_i32_e32 v6, 3, v6
	v_add_u32_e32 v6, v6, v7
	v_cmp_le_i32_e64 s[2:3], s2, v6
	s_nop 1
	v_cndmask_b32_e64 v7, 0, 1, s[2:3]
	v_cmp_le_i32_e64 s[2:3], s8, v6
	s_nop 1
	v_cndmask_b32_e64 v8, 0, 1, s[2:3]
	v_cmp_le_i32_e64 s[2:3], s9, v6
	s_nop 1
	v_addc_co_u32_e64 v7, s[2:3], v7, v8, s[2:3]
	v_cmp_ge_i32_e64 s[2:3], v6, v2
	v_mov_b32_e32 v8, v97
	s_nop 0
	v_cndmask_b32_e64 v2, 0, 1, s[2:3]
	v_cmp_ge_i32_e64 s[2:3], v6, v3
	s_nop 1
	v_addc_co_u32_e64 v2, s[2:3], v7, v2, s[2:3]
	v_cmp_ge_i32_e64 s[2:3], v6, v4
	v_ashrrev_i32_e32 v7, 31, v6
	s_nop 0
	v_cndmask_b32_e64 v3, 0, 1, s[2:3]
	v_cmp_ge_i32_e64 s[2:3], v6, v5
	v_mov_b64_e32 v[4:5], s[44:45]
	s_nop 0
	v_addc_co_u32_e64 v9, s[2:3], v2, v3, s[2:3]
	v_mul_lo_u32 v2, v6, 44
	v_sub_u32_e32 v10, v1, v2
	v_lshlrev_b64 v[2:3], 19, v[6:7]
	v_lshl_add_u64 v[2:3], s[44:45], 0, v[2:3]
	s_mov_b64 s[2:3], 0x74f8000
	v_lshl_add_u64 v[2:3], v[2:3], 0, s[2:3]
	s_mov_b32 s2, 0x1600000
	v_ashrrev_i32_e32 v11, 31, v10
	v_mad_u64_u32 v[4:5], s[2:3], v9, s2, v[4:5]
	v_lshlrev_b64 v[12:13], 19, v[10:11]
	v_lshl_add_u64 v[4:5], v[4:5], 0, v[12:13]
	s_mov_b64 s[2:3], 0x41548000
	v_lshl_add_u32 v1, v0, 5, 0
	v_lshl_add_u64 v[4:5], v[4:5], 0, s[2:3]
	v_add_u32_e32 v1, 0x201c0, v1
	v_mov_b32_e32 v7, v10
	ds_write_b128 v1, v[2:5]
	ds_write_b128 v1, v[6:9] offset:16

.LBB0_2190:
	v_readlane_b32 s6, v254, 7
	v_readlane_b32 s7, v254, 8
	s_cmp_le_i32 s6, s20
	s_cselect_b64 s[4:5], -1, 0
	s_cmp_lt_i32 s20, s7
	s_cselect_b64 s[6:7], -1, 0
	s_and_b64 s[4:5], s[4:5], s[6:7]
	s_mov_b32 s2, s88
	s_andn2_b64 vcc, exec, s[4:5]
	v_mbcnt_lo_u32_b32 v0, -1, 0
	v_mbcnt_hi_u32_b32 v0, -1, v0
	s_cbranch_vccnz .LBB0_2239
	v_or_b32_e32 v0, s66, v0
	v_mov_b32_e32 v1, v0
	s_waitcnt vmcnt(0)
	s_barrier
	s_nop 0
	v_cmp_gt_i32_e32 vcc, 64, v1
	s_and_saveexec_b64 s[6:7], vcc
	s_cbranch_execz .LBB0_2196
	v_mov_b32_e32 v4, 0x10000
	global_load_dword v140, v4, s[44:45] sc1
	global_load_dword v141, v4, s[44:45] offset:4 sc1
	global_load_dword v142, v4, s[44:45] offset:8 sc1
	global_load_dword v143, v4, s[44:45] offset:12 sc1
	global_load_dword v144, v4, s[44:45] offset:16 sc1
	global_load_dword v145, v4, s[44:45] offset:20 sc1
	global_load_dword v146, v4, s[44:45] offset:24 sc1
	global_load_dword v147, v4, s[44:45] offset:28 sc1
	v_mul_lo_u32 v2, v1, s96
	v_add_u32_e32 v2, s2, v2
	v_readlane_b32 s16, v255, 10
	v_readlane_b32 s17, v255, 9
	s_waitcnt vmcnt(7)
	v_readfirstlane_b32 s2, v140
	s_addk_i32 s2, 0xff
	s_ashr_i32 s3, s2, 31
	s_lshr_b32 s3, s3, 24
	s_add_i32 s2, s2, s3
	s_ashr_i32 s10, s2, 8
	s_waitcnt vmcnt(6)
	v_readfirstlane_b32 s2, v141
	s_addk_i32 s2, 0xff
	s_ashr_i32 s3, s2, 31
	s_lshr_b32 s3, s3, 24
	s_add_i32 s2, s2, s3
	s_ashr_i32 s2, s2, 8
	s_add_i32 s2, s2, s10
	s_waitcnt vmcnt(5)
	v_readfirstlane_b32 s3, v142
	s_addk_i32 s3, 0xff
	s_ashr_i32 s8, s3, 31
	s_lshr_b32 s8, s8, 24
	s_add_i32 s3, s3, s8
	s_ashr_i32 s11, s3, 8
	s_add_i32 s11, s11, s2
	s_waitcnt vmcnt(4)
	v_readfirstlane_b32 s3, v143
	s_addk_i32 s3, 0xff
	s_ashr_i32 s8, s3, 31
	s_lshr_b32 s8, s8, 24
	s_add_i32 s3, s3, s8
	s_ashr_i32 s12, s3, 8
	s_add_i32 s12, s12, s11
	s_waitcnt vmcnt(3)
	v_readfirstlane_b32 s3, v144
	s_addk_i32 s3, 0xff
	s_ashr_i32 s8, s3, 31
	s_lshr_b32 s8, s8, 24
	s_add_i32 s3, s3, s8
	s_ashr_i32 s13, s3, 8
	s_add_i32 s13, s13, s12
	s_waitcnt vmcnt(2)
	v_readfirstlane_b32 s3, v145
	s_addk_i32 s3, 0xff
	s_ashr_i32 s8, s3, 31
	s_lshr_b32 s8, s8, 24
	s_add_i32 s3, s3, s8
	s_ashr_i32 s14, s3, 8
	s_add_i32 s14, s14, s13
	s_waitcnt vmcnt(1)
	v_readfirstlane_b32 s3, v146
	s_addk_i32 s3, 0xff
	s_ashr_i32 s8, s3, 31
	s_lshr_b32 s8, s8, 24
	s_add_i32 s3, s3, s8
	s_ashr_i32 s15, s3, 8
	s_add_i32 s15, s15, s14
	s_waitcnt vmcnt(0)
	v_readfirstlane_b32 s3, v147
	s_addk_i32 s3, 0xff
	s_ashr_i32 s8, s3, 31
	s_lshr_b32 s8, s8, 24
	s_add_i32 s3, s3, s8
	s_ashr_i32 s3, s3, 8
	s_add_i32 s3, s3, s15
	s_min_i32 s3, s3, 0x48
	s_lshl_b32 s3, s3, 3
	s_abs_i32 s9, s3
	s_mul_hi_u32 s16, s9, s16
	s_mul_i32 s16, s16, s17
	s_sub_i32 s9, s9, s16
	s_ashr_i32 s8, s3, 31
	s_sub_i32 s16, s9, s17
	s_cmp_ge_u32 s9, s17
	s_cselect_b32 s9, s16, s9
	s_sub_i32 s16, s9, s17
	s_cmp_ge_u32 s9, s17
	s_cselect_b32 s9, s16, s9
	s_xor_b32 s9, s9, s8
	s_sub_i32 s8, s8, s9
	s_add_i32 s3, s3, s8
	v_cmp_gt_i32_e32 vcc, s3, v2
	s_and_saveexec_b64 s[8:9], vcc
	s_cbranch_execz .LBB0_2194
	v_ashrrev_i32_e32 v3, 31, v2
	v_lshrrev_b32_e32 v3, 29, v3
	v_add_u32_e32 v3, v2, v3
	v_ashrrev_i32_e32 v4, 3, v3
	v_cmp_le_i32_e64 s[2:3], s2, v4
	v_and_b32_e32 v3, -8, v3
	s_nop 0
	v_cndmask_b32_e64 v5, 0, 1, s[2:3]
	v_cmp_le_i32_e64 s[2:3], s10, v4
	s_nop 1
	v_cndmask_b32_e64 v6, 0, 1, s[2:3]
	v_cmp_le_i32_e64 s[2:3], s11, v4
	s_nop 1
	v_addc_co_u32_e64 v5, s[2:3], v5, v6, s[2:3]
	v_cmp_le_i32_e64 s[2:3], s12, v4
	s_nop 1
	v_cndmask_b32_e64 v6, 0, 1, s[2:3]
	v_cmp_le_i32_e64 s[2:3], s13, v4
	s_nop 1
	v_addc_co_u32_e64 v5, s[2:3], v5, v6, s[2:3]
	v_cmp_le_i32_e64 s[2:3], s14, v4
	s_nop 1
	v_cndmask_b32_e64 v6, 0, 1, s[2:3]
	v_cmp_le_i32_e64 s[2:3], s15, v4
	s_nop 1
	v_addc_co_u32_e64 v7, s[2:3], v5, v6, s[2:3]
	v_sub_u32_e32 v5, v2, v3
	v_mov_b64_e32 v[2:3], s[44:45]
	v_mad_i64_i32 v[8:9], s[2:3], v4, s78, v[2:3]
	s_mov_b64 s[2:3], 0x27718000
	s_nop 0
	v_lshl_add_u64 v[8:9], v[8:9], 0, s[2:3]
	s_mov_b32 s2, 0xb00000
	v_mul_lo_u32 v10, v5, s78
	v_mad_u64_u32 v[2:3], s[2:3], v7, s2, v[2:3]
	v_ashrrev_i32_e32 v11, 31, v10
	v_lshl_add_u64 v[2:3], v[2:3], 0, v[10:11]
	s_mov_b64 s[2:3], 0x57548000
	v_lshl_add_u64 v[10:11], v[2:3], 0, s[2:3]
	v_lshl_add_u32 v2, v1, 5, 0
	v_add_u32_e32 v2, 0x201c0, v2
	v_mov_b32_e32 v6, v97
	ds_write_b128 v2, v[8:11]
	ds_write_b128 v2, v[4:7] offset:16

.LBB0_2212:
	s_mov_b32 s30, s88
	v_mov_b32_e32 v2, 0x10000
	v_mbcnt_lo_u32_b32 v0, -1, 0
	v_mbcnt_hi_u32_b32 v0, -1, v0
	global_load_dword v140, v2, s[44:45] sc1
	global_load_dword v141, v2, s[44:45] offset:4 sc1
	global_load_dword v142, v2, s[44:45] offset:8 sc1
	global_load_dword v143, v2, s[44:45] offset:12 sc1
	global_load_dword v144, v2, s[44:45] offset:16 sc1
	global_load_dword v145, v2, s[44:45] offset:20 sc1
	global_load_dword v146, v2, s[44:45] offset:24 sc1
	global_load_dword v147, v2, s[44:45] offset:28 sc1
	s_add_u32 s20, s44, 0x10000
	s_addc_u32 s21, s45, 0
	s_add_u32 s18, s44, 0x10004
	s_addc_u32 s19, s45, 0
	s_add_u32 s16, s44, 0x10008
	s_addc_u32 s17, s45, 0
	s_add_u32 s14, s44, 0x1000c
	s_addc_u32 s15, s45, 0
	s_add_u32 s12, s44, 0x10010
	s_addc_u32 s13, s45, 0
	s_add_u32 s10, s44, 0x10014
	s_addc_u32 s11, s45, 0
	s_add_u32 s8, s44, 0x10018
	v_or_b32_e32 v0, s66, v0
	s_addc_u32 s9, s45, 0
	s_add_u32 s2, s44, 0x1001c
	s_addc_u32 s3, s45, 0
	s_waitcnt vmcnt(7)
	v_readfirstlane_b32 s22, v140
	s_waitcnt vmcnt(6)
	v_readfirstlane_b32 s23, v141
	s_waitcnt vmcnt(5)
	v_readfirstlane_b32 s24, v142
	s_waitcnt vmcnt(4)
	v_readfirstlane_b32 s25, v143
	s_waitcnt vmcnt(3)
	v_readfirstlane_b32 s26, v144
	s_waitcnt vmcnt(2)
	v_readfirstlane_b32 s27, v145
	s_waitcnt vmcnt(1)
	v_readfirstlane_b32 s28, v146
	s_barrier
	s_waitcnt vmcnt(0)
	v_readfirstlane_b32 s29, v147
	v_mov_b32_e32 v1, v0
	s_nop 0
	v_cmp_gt_i32_e32 vcc, 64, v1
	s_and_saveexec_b64 s[6:7], vcc
	s_cbranch_execz .LBB0_2217
	global_load_dword v148, v97, s[20:21] sc1
	global_load_dword v149, v97, s[18:19] sc1
	global_load_dword v150, v97, s[16:17] sc1
	global_load_dword v151, v97, s[14:15] sc1
	global_load_dword v152, v97, s[12:13] sc1
	global_load_dword v153, v97, s[10:11] sc1
	global_load_dword v154, v97, s[8:9] sc1
	global_load_dword v155, v97, s[2:3] sc1
	s_waitcnt vmcnt(7)
	v_readfirstlane_b32 s20, v148
	s_addk_i32 s20, 0xff
	s_ashr_i32 s21, s20, 31
	s_lshr_b32 s21, s21, 24
	s_add_i32 s20, s20, s21
	s_ashr_i32 s20, s20, 8
	s_waitcnt vmcnt(6)
	v_readfirstlane_b32 s18, v149
	s_addk_i32 s18, 0xff
	s_ashr_i32 s19, s18, 31
	s_lshr_b32 s19, s19, 24
	s_add_i32 s18, s18, s19
	s_ashr_i32 s18, s18, 8
	s_add_i32 s18, s18, s20
	s_waitcnt vmcnt(5)
	v_readfirstlane_b32 s16, v150
	s_addk_i32 s16, 0xff
	s_ashr_i32 s17, s16, 31
	s_lshr_b32 s17, s17, 24
	s_add_i32 s16, s16, s17
	s_ashr_i32 s16, s16, 8
	s_add_i32 s16, s16, s18
	s_waitcnt vmcnt(4)
	v_readfirstlane_b32 s14, v151
	s_addk_i32 s14, 0xff
	s_ashr_i32 s15, s14, 31
	s_lshr_b32 s15, s15, 24
	s_add_i32 s14, s14, s15
	s_ashr_i32 s14, s14, 8
	s_add_i32 s14, s14, s16
	s_waitcnt vmcnt(3)
	v_readfirstlane_b32 s12, v152
	s_addk_i32 s12, 0xff
	s_ashr_i32 s13, s12, 31
	s_lshr_b32 s13, s13, 24
	s_add_i32 s12, s12, s13
	s_ashr_i32 s12, s12, 8
	s_add_i32 s12, s12, s14
	v_readlane_b32 s13, v255, 9
	s_waitcnt vmcnt(2)
	v_readfirstlane_b32 s10, v153
	s_addk_i32 s10, 0xff
	s_ashr_i32 s11, s10, 31
	s_lshr_b32 s11, s11, 24
	s_add_i32 s10, s10, s11
	s_ashr_i32 s10, s10, 8
	s_add_i32 s10, s10, s12
	s_waitcnt vmcnt(1)
	v_readfirstlane_b32 s8, v154
	s_addk_i32 s8, 0xff
	s_ashr_i32 s9, s8, 31
	s_lshr_b32 s9, s9, 24
	s_add_i32 s8, s8, s9
	s_ashr_i32 s11, s8, 8
	s_add_i32 s11, s11, s10
	v_readlane_b32 s9, v255, 10
	s_waitcnt vmcnt(0)
	v_readfirstlane_b32 s2, v155
	s_addk_i32 s2, 0xff
	s_ashr_i32 s3, s2, 31
	s_lshr_b32 s3, s3, 24
	s_add_i32 s2, s2, s3
	s_ashr_i32 s2, s2, 8
	s_add_i32 s2, s2, s11
	s_min_i32 s2, s2, 0x48
	s_lshl_b32 s2, s2, 3
	s_abs_i32 s8, s2
	s_mul_hi_u32 s9, s8, s9
	s_mul_i32 s9, s9, s13
	s_sub_i32 s8, s8, s9
	s_ashr_i32 s3, s2, 31
	s_sub_i32 s9, s8, s13
	s_cmp_ge_u32 s8, s13
	s_cselect_b32 s8, s9, s8
	s_sub_i32 s9, s8, s13
	s_cmp_ge_u32 s8, s13
	s_cselect_b32 s8, s9, s8
	s_xor_b32 s8, s8, s3
	s_sub_i32 s3, s8, s3
	v_mul_lo_u32 v2, v1, s96
	v_add_u32_e32 v2, s30, v2
	s_lshl_b32 s8, s3, 2
	v_cmp_gt_i32_e32 vcc, s8, v2
	s_and_saveexec_b64 s[8:9], vcc
	s_cbranch_execz .LBB0_2215
	s_sub_i32 s2, s2, s3
	v_ashrrev_i32_e32 v3, 2, v2
	v_add_u32_e32 v3, s2, v3
	v_ashrrev_i32_e32 v4, 31, v3
	v_lshrrev_b32_e32 v4, 29, v4
	v_add_u32_e32 v5, v3, v4
	v_ashrrev_i32_e32 v4, 3, v5
	v_and_b32_e32 v5, -8, v5
	v_cmp_le_i32_e64 s[2:3], s20, v4
	v_sub_u32_e32 v5, v3, v5
	v_and_b32_e32 v6, 3, v2
	v_cndmask_b32_e64 v3, 0, 1, s[2:3]
	v_cmp_le_i32_e64 s[2:3], s18, v4
	v_mov_b32_e32 v9, s77
	v_mov_b32_e32 v11, s77
	v_cndmask_b32_e64 v7, 0, 1, s[2:3]
	v_cmp_le_i32_e64 s[2:3], s16, v4
	v_and_b32_e32 v2, 1, v2
	s_nop 0
	v_addc_co_u32_e64 v96, s[2:3], v3, v7, s[2:3]
	v_cmp_le_i32_e64 s[2:3], s14, v4
	v_mul_u32_u24_e32 v3, 11, v6
	s_nop 0
	v_cndmask_b32_e64 v8, 0, 1, s[2:3]
	v_cmp_le_i32_e64 s[2:3], s12, v4
	v_lshl_add_u64 v[8:9], v[96:97], 0, v[8:9]
	v_add_lshl_u32 v96, v3, v2, 7
	v_cndmask_b32_e64 v10, 0, 1, s[2:3]
	v_cmp_le_i32_e64 s[2:3], s10, v4
	v_lshl_add_u64 v[8:9], v[8:9], 0, v[10:11]
	v_lshlrev_b32_e32 v2, 1, v2
	v_cndmask_b32_e64 v10, 0, 1, s[2:3]
	v_cmp_le_i32_e64 s[2:3], s11, v4
	v_lshl_add_u64 v[8:9], v[8:9], 0, v[10:11]
	v_sub_u32_e32 v7, 12, v2
	v_cndmask_b32_e64 v10, 0, 1, s[2:3]
	v_mov_b64_e32 v[2:3], s[44:45]
	v_lshl_add_u64 v[10:11], v[8:9], 0, v[10:11]
	v_mad_i64_i32 v[8:9], s[2:3], v4, s78, v[2:3]
	v_lshl_add_u64 v[8:9], v[8:9], 0, v[96:97]
	s_mov_b64 s[2:3], 0x27718000
	s_mov_b32 s10, 0xb00000
	v_lshl_add_u64 v[8:9], v[8:9], 0, s[2:3]
	v_mad_u64_u32 v[2:3], s[2:3], v10, s10, v[2:3]
	v_mul_lo_u32 v10, v5, s78
	v_mad_u32_u24 v3, v11, s10, v3
	v_ashrrev_i32_e32 v11, 31, v10
	v_lshl_add_u64 v[2:3], v[2:3], 0, v[10:11]
	v_lshl_add_u64 v[2:3], v[2:3], 0, v[96:97]
	s_mov_b64 s[2:3], 0x57548000
	v_lshl_add_u64 v[10:11], v[2:3], 0, s[2:3]
	v_lshl_add_u32 v2, v1, 5, 0
	v_add_u32_e32 v2, 0x201c0, v2
	ds_write_b128 v2, v[8:11]
	ds_write_b128 v2, v[4:7] offset:16

.LBB0_2299:
	v_mul_f32_e32 v32, v93, v93
	v_mul_f32_e32 v33, v89, v89
	v_fmac_f32_e32 v32, v92, v92
	v_fmac_f32_e32 v33, v88, v88
	v_fmac_f32_e32 v32, v94, v94
	v_fmac_f32_e32 v33, v90, v90
	v_fmac_f32_e32 v32, v95, v95
	v_fmac_f32_e32 v33, v91, v91
	v_add_f32_e32 v32, v32, v33
	v_mul_f32_e32 v33, v85, v85
	v_fmac_f32_e32 v33, v84, v84
	v_fmac_f32_e32 v33, v86, v86
	v_fmac_f32_e32 v33, v87, v87
	v_add_f32_e32 v32, v33, v32
	v_mul_f32_e32 v33, v81, v81
	v_fmac_f32_e32 v33, v80, v80
	v_fmac_f32_e32 v33, v82, v82
	v_fmac_f32_e32 v33, v83, v83
	v_add_f32_e32 v32, v33, v32
	v_mul_f32_e32 v33, v77, v77
	v_fmac_f32_e32 v33, v76, v76
	v_fmac_f32_e32 v33, v78, v78
	v_fmac_f32_e32 v33, v79, v79
	v_add_f32_e32 v32, v33, v32
	v_mul_f32_e32 v33, v73, v73
	v_fmac_f32_e32 v33, v72, v72
	v_fmac_f32_e32 v33, v74, v74
	v_fmac_f32_e32 v33, v75, v75
	v_add_f32_e32 v32, v33, v32
	v_mul_f32_e32 v33, v69, v69
	v_fmac_f32_e32 v33, v68, v68
	v_fmac_f32_e32 v33, v70, v70
	v_fmac_f32_e32 v33, v71, v71
	v_add_f32_e32 v32, v33, v32
	v_mul_f32_e32 v33, v65, v65
	v_fmac_f32_e32 v33, v64, v64
	v_fmac_f32_e32 v33, v66, v66
	v_fmac_f32_e32 v33, v67, v67
	v_add_f32_e32 v32, v33, v32
	v_lshl_add_u32 v41, v178, 2, v177
	s_ashr_i32 s3, s2, 31
	s_lshl_b64 s[2:3], s[2:3], 13
	s_waitcnt vmcnt(4)
	v_mov_b64_e32 v[144:145], v[116:117]
	s_waitcnt lgkmcnt(0)
	s_nop 1
	v_add_f32_dpp v32, v32, v32 quad_perm:[1,0,3,2] row_mask:0xf bank_mask:0xf
	v_mov_b64_e32 v[148:149], v[118:119]
	v_mov_b64_e32 v[152:153], v[120:121]
	v_mov_b64_e32 v[156:157], v[122:123]
	v_mov_b64_e32 v[160:161], v[108:109]
	s_waitcnt lgkmcnt(0)
	s_nop 1
	v_add_f32_dpp v32, v32, v32 quad_perm:[2,3,0,1] row_mask:0xf bank_mask:0xf
	v_mov_b64_e32 v[164:165], v[110:111]
	v_mov_b64_e32 v[168:169], v[112:113]
	v_mov_b64_e32 v[172:173], v[114:115]
	s_waitcnt vmcnt(0)
	v_mov_b64_e32 v[146:147], v[132:133]
	s_waitcnt lgkmcnt(0)
	s_nop 1
	v_add_f32_dpp v32, v32, v32 row_half_mirror row_mask:0xf bank_mask:0xf
	v_mov_b64_e32 v[150:151], v[134:135]
	v_mov_b64_e32 v[154:155], v[136:137]
	v_mov_b64_e32 v[158:159], v[138:139]
	v_mov_b64_e32 v[162:163], v[124:125]
	s_waitcnt lgkmcnt(0)
	s_nop 1
	v_add_f32_dpp v32, v32, v32 row_mirror row_mask:0xf bank_mask:0xf
	v_mov_b32_e32 v33, v32
	v_mov_b64_e32 v[166:167], v[126:127]
	v_mov_b64_e32 v[170:171], v[128:129]
	v_mov_b64_e32 v[174:175], v[130:131]
	v_mov_b64_e32 v[142:143], v[140:141]
	s_waitcnt lgkmcnt(0)
	s_nop 1
	v_permlane16_swap_b32_e32 v32, v33
	v_add_f32_e32 v32, v32, v33
	v_mov_b32_e32 v33, v32
	s_nop 1
	v_permlane32_swap_b32_e32 v32, v33
	v_add_f32_e32 v32, v32, v33
	v_fmamk_f32 v32, v32, 0x3a000000, v176
	v_mul_f32_e32 v33, 0x4b800000, v32
	v_cmp_gt_f32_e32 vcc, s19, v32
	ds_read_b128 v[36:39], v41 offset:1024
	s_nop 0
	v_cndmask_b32_e32 v32, v32, v33, vcc
	v_rsq_f32_e32 v32, v32
	s_nop 0
	v_mul_f32_e32 v33, 0x45800000, v32
	v_cndmask_b32_e32 v40, v32, v33, vcc
	ds_read_b128 v[32:35], v41
	v_pk_mul_f32 v[42:43], v[92:93], v[40:41] op_sel_hi:[1,0]
	v_pk_mul_f32 v[44:45], v[94:95], v[40:41] op_sel_hi:[1,0]
	v_pk_mul_f32 v[46:47], v[86:87], v[40:41] op_sel_hi:[1,0]
	v_mov_b64_e32 v[94:95], v[2:3]
	s_waitcnt lgkmcnt(0)
	v_pk_fma_f32 v[34:35], v[34:35], v[44:45], 0 op_sel_hi:[1,1,0]
	v_pk_fma_f32 v[32:33], v[32:33], v[42:43], 0 op_sel_hi:[1,1,0]
	v_lshl_add_u64 v[42:43], v[102:103], 0, s[2:3]
	global_store_dwordx4 v[42:43], v[32:35], off
	v_pk_mul_f32 v[44:45], v[84:85], v[40:41] op_sel_hi:[1,0]
	v_mov_b64_e32 v[86:87], v[10:11]
	v_pk_mul_f32 v[32:33], v[88:89], v[40:41] op_sel_hi:[1,0]
	v_pk_mul_f32 v[34:35], v[90:91], v[40:41] op_sel_hi:[1,0]
	v_pk_fma_f32 v[32:33], v[36:37], v[32:33], 0 op_sel_hi:[1,1,0]
	v_pk_fma_f32 v[34:35], v[38:39], v[34:35], 0 op_sel_hi:[1,1,0]
	ds_read_b128 v[36:39], v41 offset:2048
	global_store_dwordx4 v[42:43], v[32:35], off offset:1024
	ds_read_b128 v[32:35], v41 offset:3072
	v_mov_b64_e32 v[90:91], v[6:7]
	v_mov_b64_e32 v[84:85], v[8:9]
	s_waitcnt lgkmcnt(1)
	v_pk_fma_f32 v[38:39], v[38:39], v[46:47], 0 op_sel_hi:[1,1,0]
	v_pk_fma_f32 v[36:37], v[36:37], v[44:45], 0 op_sel_hi:[1,1,0]
	global_store_dwordx4 v[42:43], v[36:39], off offset:2048
	v_pk_mul_f32 v[44:45], v[76:77], v[40:41] op_sel_hi:[1,0]
	v_pk_mul_f32 v[46:47], v[78:79], v[40:41] op_sel_hi:[1,0]
	v_pk_mul_f32 v[36:37], v[80:81], v[40:41] op_sel_hi:[1,0]
	v_pk_mul_f32 v[38:39], v[82:83], v[40:41] op_sel_hi:[1,0]
	s_waitcnt lgkmcnt(0)
	v_pk_fma_f32 v[32:33], v[32:33], v[36:37], 0 op_sel_hi:[1,1,0]
	v_pk_fma_f32 v[34:35], v[34:35], v[38:39], 0 op_sel_hi:[1,1,0]
	ds_read_b128 v[36:39], v41 offset:4096
	global_store_dwordx4 v[42:43], v[32:35], off offset:3072
	ds_read_b128 v[32:35], v41 offset:5120
	v_add_co_u32_e32 v42, vcc, s18, v42
	s_waitcnt lgkmcnt(1)
	v_pk_fma_f32 v[38:39], v[38:39], v[46:47], 0 op_sel_hi:[1,1,0]
	v_pk_fma_f32 v[36:37], v[36:37], v[44:45], 0 op_sel_hi:[1,1,0]
	v_addc_co_u32_e32 v43, vcc, 0, v43, vcc
	global_store_dwordx4 v[42:43], v[36:39], off
	v_pk_mul_f32 v[44:45], v[68:69], v[40:41] op_sel_hi:[1,0]
	v_pk_mul_f32 v[46:47], v[70:71], v[40:41] op_sel_hi:[1,0]
	v_pk_mul_f32 v[36:37], v[72:73], v[40:41] op_sel_hi:[1,0]
	v_pk_mul_f32 v[38:39], v[74:75], v[40:41] op_sel_hi:[1,0]
	s_waitcnt lgkmcnt(0)
	v_pk_fma_f32 v[32:33], v[32:33], v[36:37], 0 op_sel_hi:[1,1,0]
	v_pk_fma_f32 v[34:35], v[34:35], v[38:39], 0 op_sel_hi:[1,1,0]
	ds_read_b128 v[36:39], v41 offset:6144
	global_store_dwordx4 v[42:43], v[32:35], off offset:1024
	ds_read_b128 v[32:35], v41 offset:7168
	v_mov_b64_e32 v[70:71], v[26:27]
	v_mov_b64_e32 v[74:75], v[22:23]
	s_waitcnt lgkmcnt(1)
	v_pk_fma_f32 v[38:39], v[46:47], v[38:39], 0 op_sel_hi:[1,1,0]
	v_pk_fma_f32 v[36:37], v[44:45], v[36:37], 0 op_sel_hi:[1,1,0]
	global_store_dwordx4 v[42:43], v[36:39], off offset:2048
	v_mov_b64_e32 v[78:79], v[18:19]
	v_mov_b64_e32 v[82:83], v[14:15]
	v_pk_mul_f32 v[36:37], v[64:65], v[40:41] op_sel_hi:[1,0]
	v_pk_mul_f32 v[38:39], v[66:67], v[40:41] op_sel_hi:[1,0]
	v_mov_b64_e32 v[66:67], v[30:31]
	s_waitcnt lgkmcnt(0)
	v_pk_fma_f32 v[34:35], v[38:39], v[34:35], 0 op_sel_hi:[1,1,0]
	v_pk_fma_f32 v[32:33], v[36:37], v[32:33], 0 op_sel_hi:[1,1,0]
	s_andn2_b64 vcc, exec, s[10:11]
	v_mov_b64_e32 v[64:65], v[28:29]
	v_mov_b64_e32 v[68:69], v[24:25]
	v_mov_b64_e32 v[72:73], v[20:21]
	v_mov_b64_e32 v[76:77], v[16:17]
	v_mov_b64_e32 v[80:81], v[12:13]
	v_mov_b64_e32 v[88:89], v[4:5]
	v_mov_b64_e32 v[92:93], v[0:1]
	s_mov_b32 s2, s8
	global_store_dwordx4 v[42:43], v[32:35], off offset:3072
	s_cbranch_vccz .LBB0_2308
